# plus: K-loops of all 12 GEMMs lose the no-op lgkmcnt waits between MFMAs and the setprio 0/1 flip pairs inside MFMA segments
# speedup vs baseline: 1.0003x; 1.0003x over previous
.LBB0_244:
	v_add_u32_e32 v78, 0x10000, v183
	v_add_u32_e32 v142, 0x14000, v183
	s_add_u32 s40, s22, 0x100
	ds_read_b128 v[66:69], v78
	ds_read_b128 v[70:73], v78 offset:1024
	ds_read_b128 v[74:77], v78 offset:2048
	ds_read_b128 v[78:81], v78 offset:3072
	ds_read_b128 v[98:101], v142
	ds_read_b128 v[118:121], v142 offset:1024
	ds_read_b128 v[138:141], v142 offset:2048
	ds_read_b128 v[142:145], v142 offset:3072
	s_addc_u32 s41, s23, 0
	s_cmp_eq_u32 s3, 12
	s_cselect_b32 s46, s26, s40
	s_cselect_b32 s47, s27, s41
	s_cselect_b32 s42, s12, s0
	s_cselect_b32 s43, s13, s1
	s_add_u32 s44, s46, 0x80
	s_addc_u32 s45, s47, 0
	s_add_u32 s18, s22, 0x80
	s_addc_u32 s19, s23, 0
	ds_read_b128 v[146:149], v184
	ds_read_b128 v[166:169], v184 offset:1024
	ds_read_b128 v[170:173], v184 offset:2048
	ds_read_b128 v[186:189], v184 offset:3072
	ds_read_b128 v[190:193], v184 offset:4096
	ds_read_b128 v[194:197], v184 offset:5120
	ds_read_b128 v[198:201], v184 offset:6144
	ds_read_b128 v[206:209], v184 offset:7168
	s_mov_b32 m0, s71
	s_nop 0
	global_load_lds_dwordx4 v179, s[18:19]
	s_mov_b32 m0, s72
	s_nop 0
	global_load_lds_dwordx4 v180, s[18:19]
	s_waitcnt vmcnt(8)
	s_waitcnt lgkmcnt(0)
	s_barrier
	s_setprio 1
	v_mfma_f32_16x16x32_bf16 v[162:165], v[66:69], v[146:149], v[162:165]
	v_mfma_f32_16x16x32_bf16 v[158:161], v[74:77], v[146:149], v[158:161]
	v_mfma_f32_16x16x32_bf16 v[134:137], v[66:69], v[170:173], v[134:137]
	v_mfma_f32_16x16x32_bf16 v[130:133], v[74:77], v[170:173], v[130:133]
	v_mfma_f32_16x16x32_bf16 v[114:117], v[66:69], v[190:193], v[114:117]
	v_mfma_f32_16x16x32_bf16 v[110:113], v[74:77], v[190:193], v[110:113]
	v_mfma_f32_16x16x32_bf16 v[94:97], v[66:69], v[198:201], v[94:97]
	v_mfma_f32_16x16x32_bf16 v[90:93], v[74:77], v[198:201], v[90:93]
	v_mfma_f32_16x16x32_bf16 v[162:165], v[70:73], v[166:169], v[162:165]
	v_mfma_f32_16x16x32_bf16 v[158:161], v[78:81], v[166:169], v[158:161]
	v_mfma_f32_16x16x32_bf16 v[134:137], v[70:73], v[186:189], v[134:137]
	v_mfma_f32_16x16x32_bf16 v[130:133], v[78:81], v[186:189], v[130:133]
	v_mfma_f32_16x16x32_bf16 v[114:117], v[70:73], v[194:197], v[114:117]
	v_mfma_f32_16x16x32_bf16 v[110:113], v[78:81], v[194:197], v[110:113]
	v_mfma_f32_16x16x32_bf16 v[94:97], v[70:73], v[206:209], v[94:97]
	v_mfma_f32_16x16x32_bf16 v[90:93], v[78:81], v[206:209], v[90:93]
	v_mfma_f32_16x16x32_bf16 v[154:157], v[98:101], v[146:149], v[154:157]
	v_mfma_f32_16x16x32_bf16 v[126:129], v[98:101], v[170:173], v[126:129]
	v_mfma_f32_16x16x32_bf16 v[122:125], v[138:141], v[170:173], v[122:125]
	v_mfma_f32_16x16x32_bf16 v[106:109], v[98:101], v[190:193], v[106:109]
	v_mfma_f32_16x16x32_bf16 v[102:105], v[138:141], v[190:193], v[102:105]
	v_mfma_f32_16x16x32_bf16 v[86:89], v[98:101], v[198:201], v[86:89]
	v_mfma_f32_16x16x32_bf16 v[82:85], v[138:141], v[198:201], v[82:85]
	v_mfma_f32_16x16x32_bf16 v[154:157], v[118:121], v[166:169], v[154:157]
	v_mfma_f32_16x16x32_bf16 v[146:149], v[138:141], v[146:149], v[150:153]
	v_mfma_f32_16x16x32_bf16 v[126:129], v[118:121], v[186:189], v[126:129]
	v_mfma_f32_16x16x32_bf16 v[122:125], v[142:145], v[186:189], v[122:125]
	v_mfma_f32_16x16x32_bf16 v[106:109], v[118:121], v[194:197], v[106:109]
	v_mfma_f32_16x16x32_bf16 v[102:105], v[142:145], v[194:197], v[102:105]
	v_mfma_f32_16x16x32_bf16 v[86:89], v[118:121], v[206:209], v[86:89]
	v_mfma_f32_16x16x32_bf16 v[82:85], v[142:145], v[206:209], v[82:85]
	v_mfma_f32_16x16x32_bf16 v[146:149], v[142:145], v[166:169], v[146:149]
	s_setprio 0
	s_barrier
	ds_read_b128 v[150:153], v184 offset:16384
	ds_read_b128 v[166:169], v184 offset:17408
	ds_read_b128 v[170:173], v184 offset:18432
	ds_read_b128 v[186:189], v184 offset:19456
	ds_read_b128 v[190:193], v184 offset:20480
	ds_read_b128 v[194:197], v184 offset:21504
	ds_read_b128 v[198:201], v184 offset:22528
	ds_read_b128 v[206:209], v184 offset:23552
	s_mov_b32 m0, s54
	s_nop 0
	global_load_lds_dwordx4 v1, s[42:43]
	s_mov_b32 m0, s55
	s_nop 0
	global_load_lds_dwordx4 v176, s[42:43]
	s_add_u32 s18, s42, 0x40000
	s_addc_u32 s19, s43, 0
	s_mov_b32 m0, s56
	s_nop 0
	global_load_lds_dwordx4 v1, s[18:19]
	s_mov_b32 m0, s57
	s_nop 0
	global_load_lds_dwordx4 v176, s[18:19]
	s_mov_b32 m0, s53
	s_nop 0
	global_load_lds_dwordx4 v177, s[46:47]
	s_mov_b32 m0, s58
	s_nop 0
	global_load_lds_dwordx4 v178, s[46:47]
	s_waitcnt vmcnt(8)
	s_waitcnt lgkmcnt(0)
	s_barrier
	s_setprio 1
	v_mfma_f32_16x16x32_bf16 v[54:57], v[66:69], v[150:153], v[54:57]
	v_mfma_f32_16x16x32_bf16 v[50:53], v[74:77], v[150:153], v[50:53]
	v_mfma_f32_16x16x32_bf16 v[38:41], v[66:69], v[170:173], v[38:41]
	v_mfma_f32_16x16x32_bf16 v[34:37], v[74:77], v[170:173], v[34:37]
	v_mfma_f32_16x16x32_bf16 v[22:25], v[66:69], v[190:193], v[22:25]
	v_mfma_f32_16x16x32_bf16 v[18:21], v[74:77], v[190:193], v[18:21]
	v_mfma_f32_16x16x32_bf16 v[6:9], v[66:69], v[198:201], v[6:9]
	v_mfma_f32_16x16x32_bf16 v[2:5], v[74:77], v[198:201], v[2:5]
	v_mfma_f32_16x16x32_bf16 v[54:57], v[70:73], v[166:169], v[54:57]
	v_mfma_f32_16x16x32_bf16 v[50:53], v[78:81], v[166:169], v[50:53]
	v_mfma_f32_16x16x32_bf16 v[38:41], v[70:73], v[186:189], v[38:41]
	v_mfma_f32_16x16x32_bf16 v[34:37], v[78:81], v[186:189], v[34:37]
	v_mfma_f32_16x16x32_bf16 v[22:25], v[70:73], v[194:197], v[22:25]
	v_mfma_f32_16x16x32_bf16 v[18:21], v[78:81], v[194:197], v[18:21]
	v_mfma_f32_16x16x32_bf16 v[6:9], v[70:73], v[206:209], v[6:9]
	v_mfma_f32_16x16x32_bf16 v[2:5], v[78:81], v[206:209], v[2:5]
	v_mfma_f32_16x16x32_bf16 v[58:61], v[98:101], v[150:153], v[58:61]
	v_mfma_f32_16x16x32_bf16 v[62:65], v[138:141], v[150:153], v[62:65]
	v_mfma_f32_16x16x32_bf16 v[42:45], v[98:101], v[170:173], v[42:45]
	v_mfma_f32_16x16x32_bf16 v[46:49], v[138:141], v[170:173], v[46:49]
	v_mfma_f32_16x16x32_bf16 v[26:29], v[98:101], v[190:193], v[26:29]
	v_mfma_f32_16x16x32_bf16 v[30:33], v[138:141], v[190:193], v[30:33]
	v_mfma_f32_16x16x32_bf16 v[10:13], v[98:101], v[198:201], v[10:13]
	v_mfma_f32_16x16x32_bf16 v[14:17], v[138:141], v[198:201], v[14:17]
	v_mfma_f32_16x16x32_bf16 v[58:61], v[118:121], v[166:169], v[58:61]
	v_mfma_f32_16x16x32_bf16 v[62:65], v[142:145], v[166:169], v[62:65]
	v_mfma_f32_16x16x32_bf16 v[42:45], v[118:121], v[186:189], v[42:45]
	v_mfma_f32_16x16x32_bf16 v[46:49], v[142:145], v[186:189], v[46:49]
	v_mfma_f32_16x16x32_bf16 v[26:29], v[118:121], v[194:197], v[26:29]
	v_mfma_f32_16x16x32_bf16 v[30:33], v[142:145], v[194:197], v[30:33]
	v_mfma_f32_16x16x32_bf16 v[10:13], v[118:121], v[206:209], v[10:13]
	v_mfma_f32_16x16x32_bf16 v[14:17], v[142:145], v[206:209], v[14:17]
	s_setprio 0
	s_barrier
	v_add_u32_e32 v78, 0x18000, v183
	v_add_u32_e32 v142, 0x1c000, v183
	ds_read_b128 v[66:69], v78
	ds_read_b128 v[70:73], v78 offset:1024
	ds_read_b128 v[74:77], v78 offset:2048
	ds_read_b128 v[78:81], v78 offset:3072
	ds_read_b128 v[98:101], v142
	ds_read_b128 v[118:121], v142 offset:1024
	ds_read_b128 v[138:141], v142 offset:2048
	ds_read_b128 v[142:145], v142 offset:3072
	ds_read_b128 v[150:153], v184 offset:32768
	ds_read_b128 v[166:169], v184 offset:33792
	ds_read_b128 v[170:173], v184 offset:34816
	ds_read_b128 v[186:189], v184 offset:35840
	ds_read_b128 v[190:193], v184 offset:36864
	ds_read_b128 v[194:197], v184 offset:37888
	ds_read_b128 v[198:201], v184 offset:38912
	ds_read_b128 v[206:209], v184 offset:39936
	s_mov_b32 m0, s59
	s_nop 0
	global_load_lds_dwordx4 v179, s[46:47]
	s_mov_b32 m0, s60
	s_nop 0
	global_load_lds_dwordx4 v180, s[46:47]
	s_waitcnt vmcnt(8)
	s_waitcnt lgkmcnt(0)
	s_barrier
	s_setprio 1
	v_mfma_f32_16x16x32_bf16 v[162:165], v[66:69], v[150:153], v[162:165]
	v_mfma_f32_16x16x32_bf16 v[158:161], v[74:77], v[150:153], v[158:161]
	v_mfma_f32_16x16x32_bf16 v[134:137], v[66:69], v[170:173], v[134:137]
	v_mfma_f32_16x16x32_bf16 v[130:133], v[74:77], v[170:173], v[130:133]
	v_mfma_f32_16x16x32_bf16 v[114:117], v[66:69], v[190:193], v[114:117]
	v_mfma_f32_16x16x32_bf16 v[110:113], v[74:77], v[190:193], v[110:113]
	v_mfma_f32_16x16x32_bf16 v[94:97], v[66:69], v[198:201], v[94:97]
	v_mfma_f32_16x16x32_bf16 v[90:93], v[74:77], v[198:201], v[90:93]
	v_mfma_f32_16x16x32_bf16 v[162:165], v[70:73], v[166:169], v[162:165]
	v_mfma_f32_16x16x32_bf16 v[158:161], v[78:81], v[166:169], v[158:161]
	v_mfma_f32_16x16x32_bf16 v[134:137], v[70:73], v[186:189], v[134:137]
	v_mfma_f32_16x16x32_bf16 v[130:133], v[78:81], v[186:189], v[130:133]
	v_mfma_f32_16x16x32_bf16 v[114:117], v[70:73], v[194:197], v[114:117]
	v_mfma_f32_16x16x32_bf16 v[110:113], v[78:81], v[194:197], v[110:113]
	v_mfma_f32_16x16x32_bf16 v[94:97], v[70:73], v[206:209], v[94:97]
	v_mfma_f32_16x16x32_bf16 v[90:93], v[78:81], v[206:209], v[90:93]
	v_mfma_f32_16x16x32_bf16 v[154:157], v[98:101], v[150:153], v[154:157]
	v_mfma_f32_16x16x32_bf16 v[146:149], v[138:141], v[150:153], v[146:149]
	v_mfma_f32_16x16x32_bf16 v[126:129], v[98:101], v[170:173], v[126:129]
	v_mfma_f32_16x16x32_bf16 v[122:125], v[138:141], v[170:173], v[122:125]
	v_mfma_f32_16x16x32_bf16 v[106:109], v[98:101], v[190:193], v[106:109]
	v_mfma_f32_16x16x32_bf16 v[102:105], v[138:141], v[190:193], v[102:105]
	v_mfma_f32_16x16x32_bf16 v[86:89], v[98:101], v[198:201], v[86:89]
	v_mfma_f32_16x16x32_bf16 v[82:85], v[138:141], v[198:201], v[82:85]
	v_mfma_f32_16x16x32_bf16 v[154:157], v[118:121], v[166:169], v[154:157]
	v_mfma_f32_16x16x32_bf16 v[150:153], v[142:145], v[166:169], v[146:149]
	v_mfma_f32_16x16x32_bf16 v[126:129], v[118:121], v[186:189], v[126:129]
	v_mfma_f32_16x16x32_bf16 v[122:125], v[142:145], v[186:189], v[122:125]
	v_mfma_f32_16x16x32_bf16 v[106:109], v[118:121], v[194:197], v[106:109]
	v_mfma_f32_16x16x32_bf16 v[102:105], v[142:145], v[194:197], v[102:105]
	v_mfma_f32_16x16x32_bf16 v[86:89], v[118:121], v[206:209], v[86:89]
	v_mfma_f32_16x16x32_bf16 v[82:85], v[142:145], v[206:209], v[82:85]
	s_setprio 0
	s_barrier
	ds_read_b128 v[146:149], v184 offset:49152
	ds_read_b128 v[166:169], v184 offset:50176
	ds_read_b128 v[170:173], v184 offset:51200
	ds_read_b128 v[186:189], v184 offset:52224
	ds_read_b128 v[190:193], v184 offset:53248
	ds_read_b128 v[194:197], v184 offset:54272
	ds_read_b128 v[198:201], v184 offset:55296
	ds_read_b128 v[206:209], v184 offset:56320
	s_add_u32 s18, s42, 0x80
	s_addc_u32 s19, s43, 0
	s_mov_b32 m0, s65
	s_nop 0
	global_load_lds_dwordx4 v1, s[18:19]
	s_mov_b32 m0, s66
	s_nop 0
	global_load_lds_dwordx4 v176, s[18:19]
	s_add_u32 s18, s42, 0x40080
	s_addc_u32 s19, s43, 0
	s_mov_b32 m0, s69
	s_nop 0
	global_load_lds_dwordx4 v1, s[18:19]
	s_mov_b32 m0, s70
	s_nop 0
	global_load_lds_dwordx4 v176, s[18:19]
	s_mov_b32 m0, s67
	s_nop 0
	global_load_lds_dwordx4 v177, s[44:45]
	s_mov_b32 m0, s68
	s_nop 0
	global_load_lds_dwordx4 v178, s[44:45]
	s_waitcnt vmcnt(8)
	s_waitcnt lgkmcnt(0)
	s_barrier
	s_setprio 1
	v_mfma_f32_16x16x32_bf16 v[54:57], v[66:69], v[146:149], v[54:57]
	v_mfma_f32_16x16x32_bf16 v[50:53], v[74:77], v[146:149], v[50:53]
	v_mfma_f32_16x16x32_bf16 v[38:41], v[66:69], v[170:173], v[38:41]
	v_mfma_f32_16x16x32_bf16 v[34:37], v[74:77], v[170:173], v[34:37]
	v_mfma_f32_16x16x32_bf16 v[22:25], v[66:69], v[190:193], v[22:25]
	v_mfma_f32_16x16x32_bf16 v[18:21], v[74:77], v[190:193], v[18:21]
	v_mfma_f32_16x16x32_bf16 v[6:9], v[66:69], v[198:201], v[6:9]
	v_mfma_f32_16x16x32_bf16 v[2:5], v[74:77], v[198:201], v[2:5]
	v_mfma_f32_16x16x32_bf16 v[54:57], v[70:73], v[166:169], v[54:57]
	v_mfma_f32_16x16x32_bf16 v[50:53], v[78:81], v[166:169], v[50:53]
	v_mfma_f32_16x16x32_bf16 v[38:41], v[70:73], v[186:189], v[38:41]
	v_mfma_f32_16x16x32_bf16 v[34:37], v[78:81], v[186:189], v[34:37]
	v_mfma_f32_16x16x32_bf16 v[22:25], v[70:73], v[194:197], v[22:25]
	v_mfma_f32_16x16x32_bf16 v[18:21], v[78:81], v[194:197], v[18:21]
	v_mfma_f32_16x16x32_bf16 v[6:9], v[70:73], v[206:209], v[6:9]
	v_mfma_f32_16x16x32_bf16 v[2:5], v[78:81], v[206:209], v[2:5]
	v_mfma_f32_16x16x32_bf16 v[58:61], v[98:101], v[146:149], v[58:61]
	v_mfma_f32_16x16x32_bf16 v[62:65], v[138:141], v[146:149], v[62:65]
	v_mfma_f32_16x16x32_bf16 v[42:45], v[98:101], v[170:173], v[42:45]
	v_mfma_f32_16x16x32_bf16 v[46:49], v[138:141], v[170:173], v[46:49]
	v_mfma_f32_16x16x32_bf16 v[26:29], v[98:101], v[190:193], v[26:29]
	v_mfma_f32_16x16x32_bf16 v[30:33], v[138:141], v[190:193], v[30:33]
	v_mfma_f32_16x16x32_bf16 v[10:13], v[98:101], v[198:201], v[10:13]
	v_mfma_f32_16x16x32_bf16 v[14:17], v[138:141], v[198:201], v[14:17]
	v_mfma_f32_16x16x32_bf16 v[58:61], v[118:121], v[166:169], v[58:61]
	v_mfma_f32_16x16x32_bf16 v[62:65], v[142:145], v[166:169], v[62:65]
	v_mfma_f32_16x16x32_bf16 v[42:45], v[118:121], v[186:189], v[42:45]
	v_mfma_f32_16x16x32_bf16 v[46:49], v[142:145], v[186:189], v[46:49]
	v_mfma_f32_16x16x32_bf16 v[26:29], v[118:121], v[194:197], v[26:29]
	v_mfma_f32_16x16x32_bf16 v[30:33], v[142:145], v[194:197], v[30:33]
	v_mfma_f32_16x16x32_bf16 v[10:13], v[118:121], v[206:209], v[10:13]
	v_mfma_f32_16x16x32_bf16 v[14:17], v[142:145], v[206:209], v[14:17]
	s_setprio 0
	s_barrier
	s_add_i32 s3, s3, 2
	s_add_u32 s0, s0, 0x100
	s_addc_u32 s1, s1, 0
	s_cmp_gt_u32 s3, 13
	s_mov_b64 s[22:23], s[40:41]
	s_cbranch_scc0 .LBB0_244
	s_and_b64 vcc, exec, s[6:7]
	s_cbranch_vccz .LBB0_247
	s_barrier

.LBB0_451:
	v_add_u32_e32 v130, 0x10000, v230
	v_add_u32_e32 v134, 0x14000, v230
	ds_read_b128 v[154:157], v130
	ds_read_b128 v[158:161], v130 offset:1024
	ds_read_b128 v[146:149], v130 offset:2048
	ds_read_b128 v[150:153], v130 offset:3072
	ds_read_b128 v[138:141], v134
	ds_read_b128 v[142:145], v134 offset:1024
	ds_read_b128 v[130:133], v134 offset:2048
	ds_read_b128 v[134:137], v134 offset:3072
	s_cmp_eq_u32 s19, 4
	s_cselect_b32 s50, s44, s17
	s_cselect_b32 s51, s45, s18
	s_cselect_b32 s48, s12, s5
	s_cselect_b32 s49, s13, s16
	s_add_u32 s46, s50, 0x80
	s_addc_u32 s47, s51, 0
	ds_read_b128 v[162:165], v231
	ds_read_b128 v[166:169], v231 offset:1024
	ds_read_b128 v[170:173], v231 offset:2048
	ds_read_b128 v[174:177], v231 offset:3072
	ds_read_b128 v[178:181], v231 offset:4096
	ds_read_b128 v[182:185], v231 offset:5120
	ds_read_b128 v[186:189], v231 offset:6144
	ds_read_b128 v[190:193], v231 offset:7168
	s_mov_b32 m0, s72
	s_nop 0
	global_load_lds_dwordx4 v226, s[2:3]
	s_mov_b32 m0, s73
	s_nop 0
	global_load_lds_dwordx4 v227, s[2:3]
	s_waitcnt vmcnt(8)
	s_waitcnt lgkmcnt(0)
	s_barrier
	s_setprio 1
	v_mfma_f32_16x16x128_f8f6f4 v[114:117], v[154:161], v[162:169], v[114:117]
	v_mfma_f32_16x16x128_f8f6f4 v[118:121], v[146:153], v[162:169], v[118:121]
	v_mfma_f32_16x16x128_f8f6f4 v[122:125], v[154:161], v[170:177], v[122:125]
	v_mfma_f32_16x16x128_f8f6f4 v[126:129], v[146:153], v[170:177], v[126:129]
	v_mfma_f32_16x16x128_f8f6f4 v[82:85], v[154:161], v[178:185], v[82:85]
	v_mfma_f32_16x16x128_f8f6f4 v[86:89], v[146:153], v[178:185], v[86:89]
	v_mfma_f32_16x16x128_f8f6f4 v[90:93], v[154:161], v[186:193], v[90:93]
	v_mfma_f32_16x16x128_f8f6f4 v[94:97], v[146:153], v[186:193], v[94:97]
	v_mfma_f32_16x16x128_f8f6f4 v[98:101], v[138:145], v[162:169], v[98:101]
	v_mfma_f32_16x16x128_f8f6f4 v[102:105], v[130:137], v[162:169], v[102:105]
	v_mfma_f32_16x16x128_f8f6f4 v[106:109], v[138:145], v[170:177], v[106:109]
	v_mfma_f32_16x16x128_f8f6f4 v[110:113], v[130:137], v[170:177], v[110:113]
	v_mfma_f32_16x16x128_f8f6f4 v[66:69], v[138:145], v[178:185], v[66:69]
	v_mfma_f32_16x16x128_f8f6f4 v[70:73], v[130:137], v[178:185], v[70:73]
	v_mfma_f32_16x16x128_f8f6f4 v[74:77], v[138:145], v[186:193], v[74:77]
	v_mfma_f32_16x16x128_f8f6f4 v[78:81], v[130:137], v[186:193], v[78:81]
	s_setprio 0
	s_barrier
	ds_read_b128 v[162:165], v231 offset:16384
	ds_read_b128 v[166:169], v231 offset:17408
	ds_read_b128 v[170:173], v231 offset:18432
	ds_read_b128 v[174:177], v231 offset:19456
	ds_read_b128 v[178:181], v231 offset:20480
	ds_read_b128 v[182:185], v231 offset:21504
	ds_read_b128 v[186:189], v231 offset:22528
	ds_read_b128 v[190:193], v231 offset:23552
	s_mov_b32 m0, s55
	s_nop 0
	global_load_lds_dwordx4 v1, s[48:49]
	s_mov_b32 m0, s56
	s_nop 0
	global_load_lds_dwordx4 v223, s[48:49]
	s_add_u32 s0, s48, 0x20000
	s_addc_u32 s1, s49, 0
	s_mov_b32 m0, s57
	s_nop 0
	global_load_lds_dwordx4 v1, s[0:1]
	s_mov_b32 m0, s58
	s_nop 0
	global_load_lds_dwordx4 v223, s[0:1]
	s_mov_b32 m0, s54
	s_nop 0
	global_load_lds_dwordx4 v224, s[50:51]
	s_mov_b32 m0, s59
	s_nop 0
	global_load_lds_dwordx4 v225, s[50:51]
	s_waitcnt vmcnt(8)
	s_waitcnt lgkmcnt(0)
	s_barrier
	s_setprio 1
	v_mfma_f32_16x16x128_f8f6f4 v[50:53], v[154:161], v[162:169], v[50:53]
	v_mfma_f32_16x16x128_f8f6f4 v[54:57], v[146:153], v[162:169], v[54:57]
	v_mfma_f32_16x16x128_f8f6f4 v[58:61], v[154:161], v[170:177], v[58:61]
	v_mfma_f32_16x16x128_f8f6f4 v[62:65], v[146:153], v[170:177], v[62:65]
	v_mfma_f32_16x16x128_f8f6f4 v[194:197], v[154:161], v[178:185], v[18:21]
	v_mfma_f32_16x16x128_f8f6f4 v[198:201], v[146:153], v[178:185], v[22:25]
	v_mfma_f32_16x16x128_f8f6f4 v[206:209], v[154:161], v[186:193], v[26:29]
	v_mfma_f32_16x16x128_f8f6f4 v[218:221], v[146:153], v[186:193], v[30:33]
	v_mfma_f32_16x16x128_f8f6f4 v[232:235], v[138:145], v[162:169], v[34:37]
	v_mfma_f32_16x16x128_f8f6f4 v[236:239], v[130:137], v[162:169], v[38:41]
	v_mfma_f32_16x16x128_f8f6f4 v[240:243], v[138:145], v[170:177], v[42:45]
	v_mfma_f32_16x16x128_f8f6f4 v[170:173], v[130:137], v[170:177], v[46:49]
	v_mfma_f32_16x16x128_f8f6f4 v[174:177], v[138:145], v[178:185], v[2:5]
	v_mfma_f32_16x16x128_f8f6f4 v[178:181], v[130:137], v[178:185], v[6:9]
	v_mfma_f32_16x16x128_f8f6f4 v[182:185], v[138:145], v[186:193], v[10:13]
	v_mfma_f32_16x16x128_f8f6f4 v[186:189], v[130:137], v[186:193], v[14:17]
	s_setprio 0
	s_barrier
	s_nop 4
	v_add_u32_e32 v14, 0x18000, v230
	v_add_u32_e32 v18, 0x1c000, v230
	ds_read_b128 v[2:5], v14
	ds_read_b128 v[6:9], v14 offset:1024
	ds_read_b128 v[10:13], v14 offset:2048
	ds_read_b128 v[14:17], v14 offset:3072
	ds_read_b128 v[130:133], v18
	ds_read_b128 v[134:137], v18 offset:1024
	ds_read_b128 v[138:141], v18 offset:2048
	ds_read_b128 v[142:145], v18 offset:3072
	ds_read_b128 v[18:21], v231 offset:32768
	ds_read_b128 v[22:25], v231 offset:33792
	ds_read_b128 v[26:29], v231 offset:34816
	ds_read_b128 v[30:33], v231 offset:35840
	ds_read_b128 v[34:37], v231 offset:36864
	ds_read_b128 v[38:41], v231 offset:37888
	ds_read_b128 v[42:45], v231 offset:38912
	ds_read_b128 v[46:49], v231 offset:39936
	s_mov_b32 m0, s60
	s_nop 0
	global_load_lds_dwordx4 v226, s[50:51]
	s_mov_b32 m0, s61
	s_nop 0
	global_load_lds_dwordx4 v227, s[50:51]
	s_waitcnt vmcnt(8)
	s_waitcnt lgkmcnt(0)
	s_barrier
	s_setprio 1
	v_mfma_f32_16x16x128_f8f6f4 v[114:117], v[2:9], v[18:25], v[114:117]
	v_mfma_f32_16x16x128_f8f6f4 v[118:121], v[10:17], v[18:25], v[118:121]
	v_mfma_f32_16x16x128_f8f6f4 v[122:125], v[2:9], v[26:33], v[122:125]
	v_mfma_f32_16x16x128_f8f6f4 v[126:129], v[10:17], v[26:33], v[126:129]
	v_mfma_f32_16x16x128_f8f6f4 v[82:85], v[2:9], v[34:41], v[82:85]
	v_mfma_f32_16x16x128_f8f6f4 v[86:89], v[10:17], v[34:41], v[86:89]
	v_mfma_f32_16x16x128_f8f6f4 v[90:93], v[2:9], v[42:49], v[90:93]
	v_mfma_f32_16x16x128_f8f6f4 v[94:97], v[10:17], v[42:49], v[94:97]
	v_mfma_f32_16x16x128_f8f6f4 v[98:101], v[130:137], v[18:25], v[98:101]
	v_mfma_f32_16x16x128_f8f6f4 v[102:105], v[138:145], v[18:25], v[102:105]
	v_mfma_f32_16x16x128_f8f6f4 v[106:109], v[130:137], v[26:33], v[106:109]
	v_mfma_f32_16x16x128_f8f6f4 v[110:113], v[138:145], v[26:33], v[110:113]
	v_mfma_f32_16x16x128_f8f6f4 v[66:69], v[130:137], v[34:41], v[66:69]
	v_mfma_f32_16x16x128_f8f6f4 v[70:73], v[138:145], v[34:41], v[70:73]
	v_mfma_f32_16x16x128_f8f6f4 v[74:77], v[130:137], v[42:49], v[74:77]
	v_mfma_f32_16x16x128_f8f6f4 v[78:81], v[138:145], v[42:49], v[78:81]
	s_setprio 0
	s_barrier
	ds_read_b128 v[38:41], v231 offset:49152
	ds_read_b128 v[42:45], v231 offset:50176
	ds_read_b128 v[146:149], v231 offset:51200
	ds_read_b128 v[150:153], v231 offset:52224
	ds_read_b128 v[154:157], v231 offset:53248
	ds_read_b128 v[158:161], v231 offset:54272
	ds_read_b128 v[162:165], v231 offset:55296
	ds_read_b128 v[166:169], v231 offset:56320
	s_add_u32 s0, s48, 0x80
	s_addc_u32 s1, s49, 0
	s_mov_b32 m0, s66
	s_nop 0
	global_load_lds_dwordx4 v1, s[0:1]
	s_mov_b32 m0, s67
	s_nop 0
	global_load_lds_dwordx4 v223, s[0:1]
	s_add_u32 s0, s48, 0x20080
	s_addc_u32 s1, s49, 0
	s_mov_b32 m0, s70
	s_nop 0
	global_load_lds_dwordx4 v1, s[0:1]
	s_mov_b32 m0, s71
	s_nop 0
	global_load_lds_dwordx4 v223, s[0:1]
	s_mov_b32 m0, s68
	s_nop 0
	global_load_lds_dwordx4 v224, s[46:47]
	s_mov_b32 m0, s69
	s_nop 0
	global_load_lds_dwordx4 v225, s[46:47]
	s_waitcnt vmcnt(8)
	s_waitcnt lgkmcnt(0)
	s_barrier
	s_setprio 1
	v_mfma_f32_16x16x128_f8f6f4 v[50:53], v[2:9], v[38:45], v[50:53]
	v_mfma_f32_16x16x128_f8f6f4 v[54:57], v[10:17], v[38:45], v[54:57]
	v_mfma_f32_16x16x128_f8f6f4 v[58:61], v[2:9], v[146:153], v[58:61]
	v_mfma_f32_16x16x128_f8f6f4 v[62:65], v[10:17], v[146:153], v[62:65]
	v_mfma_f32_16x16x128_f8f6f4 v[18:21], v[2:9], v[154:161], v[194:197]
	v_mfma_f32_16x16x128_f8f6f4 v[22:25], v[10:17], v[154:161], v[198:201]
	v_mfma_f32_16x16x128_f8f6f4 v[26:29], v[2:9], v[162:169], v[206:209]
	v_mfma_f32_16x16x128_f8f6f4 v[30:33], v[10:17], v[162:169], v[218:221]
	v_mfma_f32_16x16x128_f8f6f4 v[34:37], v[130:137], v[38:45], v[232:235]
	v_mfma_f32_16x16x128_f8f6f4 v[38:41], v[138:145], v[38:45], v[236:239]
	v_mfma_f32_16x16x128_f8f6f4 v[42:45], v[130:137], v[146:153], v[240:243]
	v_mfma_f32_16x16x128_f8f6f4 v[46:49], v[138:145], v[146:153], v[170:173]
	v_mfma_f32_16x16x128_f8f6f4 v[2:5], v[130:137], v[154:161], v[174:177]
	v_mfma_f32_16x16x128_f8f6f4 v[6:9], v[138:145], v[154:161], v[178:181]
	v_mfma_f32_16x16x128_f8f6f4 v[10:13], v[130:137], v[162:169], v[182:185]
	v_mfma_f32_16x16x128_f8f6f4 v[14:17], v[138:145], v[162:169], v[186:189]
	s_setprio 0
	s_barrier
	s_add_i32 s19, s19, 2
	s_add_u32 s5, s5, 0x100
	s_addc_u32 s16, s16, 0
	s_add_u32 s17, s17, 0x100
	s_addc_u32 s18, s18, 0
	s_add_u32 s2, s2, 0x100
	s_addc_u32 s3, s3, 0
	s_cmp_gt_u32 s19, 5
	s_cbranch_scc0 .LBB0_451
	s_and_b64 vcc, exec, s[26:27]
	s_cbranch_vccz .LBB0_454
	s_barrier

.LBB0_564:
	s_add_u32 s22, s2, 0x100
	v_add_u32_e32 v46, 0x10000, v181
	v_add_u32_e32 v78, 0x14000, v181
	s_addc_u32 s23, s3, 0
	ds_read_b128 v[34:37], v46
	ds_read_b128 v[38:41], v46 offset:1024
	ds_read_b128 v[42:45], v46 offset:2048
	ds_read_b128 v[46:49], v46 offset:3072
	ds_read_b128 v[66:69], v78
	ds_read_b128 v[70:73], v78 offset:1024
	ds_read_b128 v[74:77], v78 offset:2048
	ds_read_b128 v[78:81], v78 offset:3072
	s_cmp_eq_u32 s13, 12
	s_cselect_b32 s44, s56, s22
	s_cselect_b32 s45, s57, s23
	s_cselect_b32 s40, s54, s0
	s_cselect_b32 s41, s55, s1
	s_add_u32 s42, s44, 0x80
	s_addc_u32 s43, s45, 0
	s_add_u32 s2, s2, 0x80
	s_addc_u32 s3, s3, 0
	ds_read_b128 v[162:165], v182
	ds_read_b128 v[166:169], v182 offset:1024
	ds_read_b128 v[170:173], v182 offset:2048
	ds_read_b128 v[184:187], v182 offset:3072
	ds_read_b128 v[188:191], v182 offset:4096
	ds_read_b128 v[192:195], v182 offset:5120
	ds_read_b128 v[196:199], v182 offset:6144
	ds_read_b128 v[206:209], v182 offset:7168
	s_mov_b32 m0, s79
	s_nop 0
	global_load_lds_dwordx4 v177, s[2:3]
	s_mov_b32 m0, s80
	s_nop 0
	global_load_lds_dwordx4 v178, s[2:3]
	s_waitcnt vmcnt(8)
	s_waitcnt lgkmcnt(0)
	s_barrier
	s_setprio 1
	v_mfma_f32_16x16x32_bf16 v[158:161], v[34:37], v[162:165], v[158:161]
	v_mfma_f32_16x16x32_bf16 v[154:157], v[42:45], v[162:165], v[154:157]
	v_mfma_f32_16x16x32_bf16 v[142:145], v[34:37], v[170:173], v[142:145]
	v_mfma_f32_16x16x32_bf16 v[138:141], v[42:45], v[170:173], v[138:141]
	v_mfma_f32_16x16x32_bf16 v[126:129], v[34:37], v[188:191], v[126:129]
	v_mfma_f32_16x16x32_bf16 v[122:125], v[42:45], v[188:191], v[122:125]
	v_mfma_f32_16x16x32_bf16 v[110:113], v[34:37], v[196:199], v[110:113]
	v_mfma_f32_16x16x32_bf16 v[106:109], v[42:45], v[196:199], v[106:109]
	v_mfma_f32_16x16x32_bf16 v[158:161], v[38:41], v[166:169], v[158:161]
	v_mfma_f32_16x16x32_bf16 v[154:157], v[46:49], v[166:169], v[154:157]
	v_mfma_f32_16x16x32_bf16 v[142:145], v[38:41], v[184:187], v[142:145]
	v_mfma_f32_16x16x32_bf16 v[138:141], v[46:49], v[184:187], v[138:141]
	v_mfma_f32_16x16x32_bf16 v[126:129], v[38:41], v[192:195], v[126:129]
	v_mfma_f32_16x16x32_bf16 v[122:125], v[46:49], v[192:195], v[122:125]
	v_mfma_f32_16x16x32_bf16 v[110:113], v[38:41], v[206:209], v[110:113]
	v_mfma_f32_16x16x32_bf16 v[106:109], v[46:49], v[206:209], v[106:109]
	v_mfma_f32_16x16x32_bf16 v[150:153], v[66:69], v[162:165], v[150:153]
	v_mfma_f32_16x16x32_bf16 v[146:149], v[74:77], v[162:165], v[146:149]
	v_mfma_f32_16x16x32_bf16 v[134:137], v[66:69], v[170:173], v[134:137]
	v_mfma_f32_16x16x32_bf16 v[130:133], v[74:77], v[170:173], v[130:133]
	v_mfma_f32_16x16x32_bf16 v[118:121], v[66:69], v[188:191], v[118:121]
	v_mfma_f32_16x16x32_bf16 v[114:117], v[74:77], v[188:191], v[114:117]
	v_mfma_f32_16x16x32_bf16 v[102:105], v[66:69], v[196:199], v[102:105]
	v_mfma_f32_16x16x32_bf16 v[98:101], v[74:77], v[196:199], v[98:101]
	v_mfma_f32_16x16x32_bf16 v[150:153], v[70:73], v[166:169], v[150:153]
	v_mfma_f32_16x16x32_bf16 v[146:149], v[78:81], v[166:169], v[146:149]
	v_mfma_f32_16x16x32_bf16 v[134:137], v[70:73], v[184:187], v[134:137]
	v_mfma_f32_16x16x32_bf16 v[130:133], v[78:81], v[184:187], v[130:133]
	v_mfma_f32_16x16x32_bf16 v[118:121], v[70:73], v[192:195], v[118:121]
	v_mfma_f32_16x16x32_bf16 v[114:117], v[78:81], v[192:195], v[114:117]
	v_mfma_f32_16x16x32_bf16 v[102:105], v[70:73], v[206:209], v[102:105]
	v_mfma_f32_16x16x32_bf16 v[98:101], v[78:81], v[206:209], v[98:101]
	s_setprio 0
	s_barrier
	ds_read_b128 v[162:165], v182 offset:16384
	ds_read_b128 v[166:169], v182 offset:17408
	ds_read_b128 v[170:173], v182 offset:18432
	ds_read_b128 v[184:187], v182 offset:19456
	ds_read_b128 v[188:191], v182 offset:20480
	ds_read_b128 v[192:195], v182 offset:21504
	ds_read_b128 v[196:199], v182 offset:22528
	ds_read_b128 v[206:209], v182 offset:23552
	s_mov_b32 m0, s64
	s_nop 0
	global_load_lds_dwordx4 v1, s[40:41]
	s_mov_b32 m0, s65
	s_nop 0
	global_load_lds_dwordx4 v174, s[40:41]
	s_add_u32 s2, s40, 0x40000
	s_addc_u32 s3, s41, 0
	s_mov_b32 m0, s66
	s_nop 0
	global_load_lds_dwordx4 v1, s[2:3]
	s_mov_b32 m0, s67
	s_nop 0
	global_load_lds_dwordx4 v174, s[2:3]
	s_mov_b32 m0, s59
	s_nop 0
	global_load_lds_dwordx4 v175, s[44:45]
	s_mov_b32 m0, s68
	s_nop 0
	global_load_lds_dwordx4 v176, s[44:45]
	s_waitcnt vmcnt(8)
	s_waitcnt lgkmcnt(0)
	s_barrier
	s_setprio 1
	v_mfma_f32_16x16x32_bf16 v[86:89], v[34:37], v[162:165], v[86:89]
	v_mfma_f32_16x16x32_bf16 v[82:85], v[42:45], v[162:165], v[82:85]
	v_mfma_f32_16x16x32_bf16 v[54:57], v[34:37], v[170:173], v[54:57]
	v_mfma_f32_16x16x32_bf16 v[50:53], v[42:45], v[170:173], v[50:53]
	v_mfma_f32_16x16x32_bf16 v[22:25], v[34:37], v[188:191], v[22:25]
	v_mfma_f32_16x16x32_bf16 v[18:21], v[42:45], v[188:191], v[18:21]
	v_mfma_f32_16x16x32_bf16 v[6:9], v[34:37], v[196:199], v[6:9]
	v_mfma_f32_16x16x32_bf16 v[2:5], v[42:45], v[196:199], v[2:5]
	v_mfma_f32_16x16x32_bf16 v[86:89], v[38:41], v[166:169], v[86:89]
	v_mfma_f32_16x16x32_bf16 v[82:85], v[46:49], v[166:169], v[82:85]
	v_mfma_f32_16x16x32_bf16 v[54:57], v[38:41], v[184:187], v[54:57]
	v_mfma_f32_16x16x32_bf16 v[50:53], v[46:49], v[184:187], v[50:53]
	v_mfma_f32_16x16x32_bf16 v[22:25], v[38:41], v[192:195], v[22:25]
	v_mfma_f32_16x16x32_bf16 v[18:21], v[46:49], v[192:195], v[18:21]
	v_mfma_f32_16x16x32_bf16 v[6:9], v[38:41], v[206:209], v[6:9]
	v_mfma_f32_16x16x32_bf16 v[2:5], v[46:49], v[206:209], v[2:5]
	v_mfma_f32_16x16x32_bf16 v[26:29], v[66:69], v[188:191], v[26:29]
	v_mfma_f32_16x16x32_bf16 v[30:33], v[74:77], v[188:191], v[30:33]
	v_mfma_f32_16x16x32_bf16 v[10:13], v[66:69], v[196:199], v[10:13]
	v_mfma_f32_16x16x32_bf16 v[14:17], v[74:77], v[196:199], v[14:17]
	v_mfma_f32_16x16x32_bf16 v[34:37], v[66:69], v[162:165], v[90:93]
	v_mfma_f32_16x16x32_bf16 v[38:41], v[74:77], v[162:165], v[94:97]
	v_mfma_f32_16x16x32_bf16 v[42:45], v[66:69], v[170:173], v[58:61]
	v_mfma_f32_16x16x32_bf16 v[46:49], v[74:77], v[170:173], v[62:65]
	v_mfma_f32_16x16x32_bf16 v[26:29], v[70:73], v[192:195], v[26:29]
	v_mfma_f32_16x16x32_bf16 v[30:33], v[78:81], v[192:195], v[30:33]
	v_mfma_f32_16x16x32_bf16 v[10:13], v[70:73], v[206:209], v[10:13]
	v_mfma_f32_16x16x32_bf16 v[14:17], v[78:81], v[206:209], v[14:17]
	v_mfma_f32_16x16x32_bf16 v[34:37], v[70:73], v[166:169], v[34:37]
	v_mfma_f32_16x16x32_bf16 v[38:41], v[78:81], v[166:169], v[38:41]
	v_mfma_f32_16x16x32_bf16 v[42:45], v[70:73], v[184:187], v[42:45]
	v_mfma_f32_16x16x32_bf16 v[46:49], v[78:81], v[184:187], v[46:49]
	s_setprio 0
	s_barrier
	v_add_u32_e32 v70, 0x18000, v181
	v_add_u32_e32 v90, 0x1c000, v181
	ds_read_b128 v[58:61], v70
	ds_read_b128 v[62:65], v70 offset:1024
	ds_read_b128 v[66:69], v70 offset:2048
	ds_read_b128 v[70:73], v70 offset:3072
	ds_read_b128 v[74:77], v90
	ds_read_b128 v[78:81], v90 offset:1024
	ds_read_b128 v[162:165], v90 offset:2048
	ds_read_b128 v[166:169], v90 offset:3072
	ds_read_b128 v[90:93], v182 offset:32768
	ds_read_b128 v[94:97], v182 offset:33792
	ds_read_b128 v[170:173], v182 offset:34816
	ds_read_b128 v[184:187], v182 offset:35840
	ds_read_b128 v[188:191], v182 offset:36864
	ds_read_b128 v[192:195], v182 offset:37888
	ds_read_b128 v[196:199], v182 offset:38912
	ds_read_b128 v[206:209], v182 offset:39936
	s_mov_b32 m0, s69
	s_nop 0
	global_load_lds_dwordx4 v177, s[44:45]
	s_mov_b32 m0, s70
	s_nop 0
	global_load_lds_dwordx4 v178, s[44:45]
	s_waitcnt vmcnt(8)
	s_waitcnt lgkmcnt(0)
	s_barrier
	s_setprio 1
	v_mfma_f32_16x16x32_bf16 v[158:161], v[58:61], v[90:93], v[158:161]
	v_mfma_f32_16x16x32_bf16 v[154:157], v[66:69], v[90:93], v[154:157]
	v_mfma_f32_16x16x32_bf16 v[142:145], v[58:61], v[170:173], v[142:145]
	v_mfma_f32_16x16x32_bf16 v[138:141], v[66:69], v[170:173], v[138:141]
	v_mfma_f32_16x16x32_bf16 v[126:129], v[58:61], v[188:191], v[126:129]
	v_mfma_f32_16x16x32_bf16 v[122:125], v[66:69], v[188:191], v[122:125]
	v_mfma_f32_16x16x32_bf16 v[110:113], v[58:61], v[196:199], v[110:113]
	v_mfma_f32_16x16x32_bf16 v[106:109], v[66:69], v[196:199], v[106:109]
	v_mfma_f32_16x16x32_bf16 v[158:161], v[62:65], v[94:97], v[158:161]
	v_mfma_f32_16x16x32_bf16 v[154:157], v[70:73], v[94:97], v[154:157]
	v_mfma_f32_16x16x32_bf16 v[142:145], v[62:65], v[184:187], v[142:145]
	v_mfma_f32_16x16x32_bf16 v[138:141], v[70:73], v[184:187], v[138:141]
	v_mfma_f32_16x16x32_bf16 v[126:129], v[62:65], v[192:195], v[126:129]
	v_mfma_f32_16x16x32_bf16 v[122:125], v[70:73], v[192:195], v[122:125]
	v_mfma_f32_16x16x32_bf16 v[110:113], v[62:65], v[206:209], v[110:113]
	v_mfma_f32_16x16x32_bf16 v[106:109], v[70:73], v[206:209], v[106:109]
	v_mfma_f32_16x16x32_bf16 v[150:153], v[74:77], v[90:93], v[150:153]
	v_mfma_f32_16x16x32_bf16 v[90:93], v[162:165], v[90:93], v[146:149]
	v_mfma_f32_16x16x32_bf16 v[146:149], v[166:169], v[94:97], v[90:93]
	v_mfma_f32_16x16x32_bf16 v[90:93], v[74:77], v[170:173], v[134:137]
	v_mfma_f32_16x16x32_bf16 v[134:137], v[78:81], v[184:187], v[90:93]
	v_mfma_f32_16x16x32_bf16 v[90:93], v[162:165], v[170:173], v[130:133]
	v_mfma_f32_16x16x32_bf16 v[130:133], v[166:169], v[184:187], v[90:93]
	v_mfma_f32_16x16x32_bf16 v[90:93], v[74:77], v[188:191], v[118:121]
	v_mfma_f32_16x16x32_bf16 v[118:121], v[78:81], v[192:195], v[90:93]
	v_mfma_f32_16x16x32_bf16 v[90:93], v[162:165], v[188:191], v[114:117]
	v_mfma_f32_16x16x32_bf16 v[114:117], v[166:169], v[192:195], v[90:93]
	v_mfma_f32_16x16x32_bf16 v[90:93], v[74:77], v[196:199], v[102:105]
	v_mfma_f32_16x16x32_bf16 v[102:105], v[78:81], v[206:209], v[90:93]
	v_mfma_f32_16x16x32_bf16 v[90:93], v[162:165], v[196:199], v[98:101]
	v_mfma_f32_16x16x32_bf16 v[150:153], v[78:81], v[94:97], v[150:153]
	v_mfma_f32_16x16x32_bf16 v[98:101], v[166:169], v[206:209], v[90:93]
	s_setprio 0
	s_barrier
	ds_read_b128 v[94:97], v182 offset:49152
	ds_read_b128 v[170:173], v182 offset:50176
	ds_read_b128 v[184:187], v182 offset:51200
	ds_read_b128 v[188:191], v182 offset:52224
	ds_read_b128 v[192:195], v182 offset:53248
	ds_read_b128 v[196:199], v182 offset:54272
	ds_read_b128 v[206:209], v182 offset:55296
	ds_read_b128 v[224:227], v182 offset:56320
	s_add_u32 s2, s40, 0x80
	s_addc_u32 s3, s41, 0
	s_mov_b32 m0, s73
	s_nop 0
	global_load_lds_dwordx4 v1, s[2:3]
	s_mov_b32 m0, s74
	s_nop 0
	global_load_lds_dwordx4 v174, s[2:3]
	s_add_u32 s2, s40, 0x40080
	s_addc_u32 s3, s41, 0
	s_mov_b32 m0, s77
	s_nop 0
	global_load_lds_dwordx4 v1, s[2:3]
	s_mov_b32 m0, s78
	s_nop 0
	global_load_lds_dwordx4 v174, s[2:3]
	s_mov_b32 m0, s75
	s_nop 0
	global_load_lds_dwordx4 v175, s[42:43]
	s_mov_b32 m0, s76
	s_nop 0
	global_load_lds_dwordx4 v176, s[42:43]
	s_waitcnt vmcnt(8)
	s_waitcnt lgkmcnt(0)
	s_barrier
	s_setprio 1
	v_mfma_f32_16x16x32_bf16 v[86:89], v[58:61], v[94:97], v[86:89]
	v_mfma_f32_16x16x32_bf16 v[82:85], v[66:69], v[94:97], v[82:85]
	v_mfma_f32_16x16x32_bf16 v[54:57], v[58:61], v[184:187], v[54:57]
	v_mfma_f32_16x16x32_bf16 v[50:53], v[66:69], v[184:187], v[50:53]
	v_mfma_f32_16x16x32_bf16 v[22:25], v[58:61], v[192:195], v[22:25]
	v_mfma_f32_16x16x32_bf16 v[18:21], v[66:69], v[192:195], v[18:21]
	v_mfma_f32_16x16x32_bf16 v[6:9], v[58:61], v[206:209], v[6:9]
	v_mfma_f32_16x16x32_bf16 v[2:5], v[66:69], v[206:209], v[2:5]
	v_mfma_f32_16x16x32_bf16 v[86:89], v[62:65], v[170:173], v[86:89]
	v_mfma_f32_16x16x32_bf16 v[82:85], v[70:73], v[170:173], v[82:85]
	v_mfma_f32_16x16x32_bf16 v[54:57], v[62:65], v[188:191], v[54:57]
	v_mfma_f32_16x16x32_bf16 v[50:53], v[70:73], v[188:191], v[50:53]
	v_mfma_f32_16x16x32_bf16 v[22:25], v[62:65], v[196:199], v[22:25]
	v_mfma_f32_16x16x32_bf16 v[18:21], v[70:73], v[196:199], v[18:21]
	v_mfma_f32_16x16x32_bf16 v[6:9], v[62:65], v[224:227], v[6:9]
	v_mfma_f32_16x16x32_bf16 v[2:5], v[70:73], v[224:227], v[2:5]
	v_mfma_f32_16x16x32_bf16 v[34:37], v[74:77], v[94:97], v[34:37]
	v_mfma_f32_16x16x32_bf16 v[90:93], v[78:81], v[170:173], v[34:37]
	v_mfma_f32_16x16x32_bf16 v[34:37], v[162:165], v[94:97], v[38:41]
	v_mfma_f32_16x16x32_bf16 v[94:97], v[166:169], v[170:173], v[34:37]
	v_mfma_f32_16x16x32_bf16 v[34:37], v[74:77], v[184:187], v[42:45]
	v_mfma_f32_16x16x32_bf16 v[58:61], v[78:81], v[188:191], v[34:37]
	v_mfma_f32_16x16x32_bf16 v[34:37], v[162:165], v[184:187], v[46:49]
	v_mfma_f32_16x16x32_bf16 v[26:29], v[74:77], v[192:195], v[26:29]
	v_mfma_f32_16x16x32_bf16 v[30:33], v[162:165], v[192:195], v[30:33]
	v_mfma_f32_16x16x32_bf16 v[10:13], v[74:77], v[206:209], v[10:13]
	v_mfma_f32_16x16x32_bf16 v[14:17], v[162:165], v[206:209], v[14:17]
	v_mfma_f32_16x16x32_bf16 v[62:65], v[166:169], v[188:191], v[34:37]
	v_mfma_f32_16x16x32_bf16 v[26:29], v[78:81], v[196:199], v[26:29]
	v_mfma_f32_16x16x32_bf16 v[30:33], v[166:169], v[196:199], v[30:33]
	v_mfma_f32_16x16x32_bf16 v[10:13], v[78:81], v[224:227], v[10:13]
	v_mfma_f32_16x16x32_bf16 v[14:17], v[166:169], v[224:227], v[14:17]
	s_setprio 0
	s_barrier
	s_add_i32 s13, s13, 2
	s_add_u32 s0, s0, 0x100
	s_addc_u32 s1, s1, 0
	s_cmp_gt_u32 s13, 13
	s_mov_b64 s[2:3], s[22:23]
	s_cbranch_scc0 .LBB0_564
	s_and_b64 vcc, exec, s[8:9]
	s_cbranch_vccz .LBB0_567
	s_barrier

.LBB0_793:
	s_add_u32 s22, s2, 0x100
	v_add_u32_e32 v94, 0x10000, v209
	v_add_u32_e32 v118, 0x14000, v209
	s_addc_u32 s23, s3, 0
	ds_read_b128 v[74:77], v94
	ds_read_b128 v[86:89], v94 offset:1024
	ds_read_b128 v[90:93], v94 offset:2048
	ds_read_b128 v[94:97], v94 offset:3072
	ds_read_b128 v[98:101], v118
	ds_read_b128 v[102:105], v118 offset:1024
	ds_read_b128 v[110:113], v118 offset:2048
	ds_read_b128 v[118:121], v118 offset:3072
	s_cmp_eq_u32 s5, 2
	s_cselect_b32 s44, s26, s22
	s_cselect_b32 s45, s27, s23
	s_cselect_b32 s40, s12, s0
	s_cselect_b32 s41, s13, s1
	s_add_u32 s42, s44, 0x80
	s_addc_u32 s43, s45, 0
	s_add_u32 s2, s2, 0x80
	s_addc_u32 s3, s3, 0
	ds_read_b128 v[130:133], v223
	ds_read_b128 v[134:137], v223 offset:1024
	ds_read_b128 v[138:141], v223 offset:2048
	ds_read_b128 v[142:145], v223 offset:3072
	ds_read_b128 v[162:165], v223 offset:4096
	ds_read_b128 v[166:169], v223 offset:5120
	ds_read_b128 v[170:173], v223 offset:6144
	ds_read_b128 v[174:177], v223 offset:7168
	s_mov_b32 m0, s37
	s_nop 0
	global_load_lds_dwordx4 v195, s[2:3]
	s_mov_b32 m0, s61
	s_nop 0
	global_load_lds_dwordx4 v197, s[2:3]
	s_waitcnt vmcnt(8)
	s_waitcnt lgkmcnt(0)
	s_barrier
	s_setprio 1
	v_mfma_f32_16x16x32_bf16 v[190:193], v[74:77], v[130:133], v[190:193]
	v_mfma_f32_16x16x32_bf16 v[186:189], v[90:93], v[130:133], v[186:189]
	v_mfma_f32_16x16x32_bf16 v[158:161], v[74:77], v[138:141], v[158:161]
	v_mfma_f32_16x16x32_bf16 v[154:157], v[90:93], v[138:141], v[154:157]
	v_mfma_f32_16x16x32_bf16 v[126:129], v[74:77], v[162:165], v[126:129]
	v_mfma_f32_16x16x32_bf16 v[122:125], v[90:93], v[162:165], v[122:125]
	v_mfma_f32_16x16x32_bf16 v[82:85], v[74:77], v[170:173], v[82:85]
	v_mfma_f32_16x16x32_bf16 v[78:81], v[90:93], v[170:173], v[78:81]
	v_mfma_f32_16x16x32_bf16 v[190:193], v[86:89], v[134:137], v[190:193]
	v_mfma_f32_16x16x32_bf16 v[186:189], v[94:97], v[134:137], v[186:189]
	v_mfma_f32_16x16x32_bf16 v[158:161], v[86:89], v[142:145], v[158:161]
	v_mfma_f32_16x16x32_bf16 v[154:157], v[94:97], v[142:145], v[154:157]
	v_mfma_f32_16x16x32_bf16 v[126:129], v[86:89], v[166:169], v[126:129]
	v_mfma_f32_16x16x32_bf16 v[122:125], v[94:97], v[166:169], v[122:125]
	v_mfma_f32_16x16x32_bf16 v[82:85], v[86:89], v[174:177], v[82:85]
	v_mfma_f32_16x16x32_bf16 v[78:81], v[94:97], v[174:177], v[78:81]
	v_mfma_f32_16x16x32_bf16 v[182:185], v[98:101], v[130:133], v[182:185]
	v_mfma_f32_16x16x32_bf16 v[130:133], v[110:113], v[130:133], v[178:181]
	v_mfma_f32_16x16x32_bf16 v[114:117], v[98:101], v[162:165], v[114:117]
	v_mfma_f32_16x16x32_bf16 v[106:109], v[110:113], v[162:165], v[106:109]
	v_mfma_f32_16x16x32_bf16 v[70:73], v[98:101], v[170:173], v[70:73]
	v_mfma_f32_16x16x32_bf16 v[66:69], v[110:113], v[170:173], v[66:69]
	v_mfma_f32_16x16x32_bf16 v[182:185], v[102:105], v[134:137], v[182:185]
	v_mfma_f32_16x16x32_bf16 v[130:133], v[118:121], v[134:137], v[130:133]
	v_mfma_f32_16x16x32_bf16 v[134:137], v[98:101], v[138:141], v[150:153]
	v_mfma_f32_16x16x32_bf16 v[138:141], v[110:113], v[138:141], v[146:149]
	v_mfma_f32_16x16x32_bf16 v[114:117], v[102:105], v[166:169], v[114:117]
	v_mfma_f32_16x16x32_bf16 v[106:109], v[118:121], v[166:169], v[106:109]
	v_mfma_f32_16x16x32_bf16 v[70:73], v[102:105], v[174:177], v[70:73]
	v_mfma_f32_16x16x32_bf16 v[66:69], v[118:121], v[174:177], v[66:69]
	v_mfma_f32_16x16x32_bf16 v[134:137], v[102:105], v[142:145], v[134:137]
	v_mfma_f32_16x16x32_bf16 v[138:141], v[118:121], v[142:145], v[138:141]
	s_setprio 0
	s_barrier
	ds_read_b128 v[142:145], v223 offset:16384
	ds_read_b128 v[146:149], v223 offset:17408
	ds_read_b128 v[150:153], v223 offset:18432
	ds_read_b128 v[162:165], v223 offset:19456
	ds_read_b128 v[166:169], v223 offset:20480
	ds_read_b128 v[170:173], v223 offset:21504
	ds_read_b128 v[174:177], v223 offset:22528
	ds_read_b128 v[178:181], v223 offset:23552
	s_mov_b32 m0, s48
	s_nop 0
	global_load_lds_dwordx4 v1, s[40:41]
	s_mov_b32 m0, s49
	s_nop 0
	global_load_lds_dwordx4 v206, s[40:41]
	s_add_u32 s2, s40, 0x18000
	s_addc_u32 s3, s41, 0
	s_mov_b32 m0, s50
	s_nop 0
	global_load_lds_dwordx4 v1, s[2:3]
	s_mov_b32 m0, s51
	s_nop 0
	global_load_lds_dwordx4 v206, s[2:3]
	s_mov_b32 m0, s47
	s_nop 0
	global_load_lds_dwordx4 v194, s[44:45]
	s_mov_b32 m0, s52
	s_nop 0
	global_load_lds_dwordx4 v196, s[44:45]
	s_waitcnt vmcnt(8)
	s_waitcnt lgkmcnt(0)
	s_barrier
	s_setprio 1
	v_mfma_f32_16x16x32_bf16 v[54:57], v[74:77], v[142:145], v[54:57]
	v_mfma_f32_16x16x32_bf16 v[50:53], v[90:93], v[142:145], v[50:53]
	v_mfma_f32_16x16x32_bf16 v[38:41], v[74:77], v[150:153], v[38:41]
	v_mfma_f32_16x16x32_bf16 v[34:37], v[90:93], v[150:153], v[34:37]
	v_mfma_f32_16x16x32_bf16 v[22:25], v[74:77], v[166:169], v[22:25]
	v_mfma_f32_16x16x32_bf16 v[18:21], v[90:93], v[166:169], v[18:21]
	v_mfma_f32_16x16x32_bf16 v[6:9], v[74:77], v[174:177], v[6:9]
	v_mfma_f32_16x16x32_bf16 v[2:5], v[90:93], v[174:177], v[2:5]
	v_mfma_f32_16x16x32_bf16 v[54:57], v[86:89], v[146:149], v[54:57]
	v_mfma_f32_16x16x32_bf16 v[50:53], v[94:97], v[146:149], v[50:53]
	v_mfma_f32_16x16x32_bf16 v[38:41], v[86:89], v[162:165], v[38:41]
	v_mfma_f32_16x16x32_bf16 v[34:37], v[94:97], v[162:165], v[34:37]
	v_mfma_f32_16x16x32_bf16 v[22:25], v[86:89], v[170:173], v[22:25]
	v_mfma_f32_16x16x32_bf16 v[18:21], v[94:97], v[170:173], v[18:21]
	v_mfma_f32_16x16x32_bf16 v[6:9], v[86:89], v[178:181], v[6:9]
	v_mfma_f32_16x16x32_bf16 v[2:5], v[94:97], v[178:181], v[2:5]
	v_mfma_f32_16x16x32_bf16 v[58:61], v[98:101], v[142:145], v[58:61]
	v_mfma_f32_16x16x32_bf16 v[62:65], v[110:113], v[142:145], v[62:65]
	v_mfma_f32_16x16x32_bf16 v[42:45], v[98:101], v[150:153], v[42:45]
	v_mfma_f32_16x16x32_bf16 v[46:49], v[110:113], v[150:153], v[46:49]
	v_mfma_f32_16x16x32_bf16 v[26:29], v[98:101], v[166:169], v[26:29]
	v_mfma_f32_16x16x32_bf16 v[30:33], v[110:113], v[166:169], v[30:33]
	v_mfma_f32_16x16x32_bf16 v[10:13], v[98:101], v[174:177], v[10:13]
	v_mfma_f32_16x16x32_bf16 v[14:17], v[110:113], v[174:177], v[14:17]
	v_mfma_f32_16x16x32_bf16 v[58:61], v[102:105], v[146:149], v[58:61]
	v_mfma_f32_16x16x32_bf16 v[62:65], v[118:121], v[146:149], v[62:65]
	v_mfma_f32_16x16x32_bf16 v[42:45], v[102:105], v[162:165], v[42:45]
	v_mfma_f32_16x16x32_bf16 v[46:49], v[118:121], v[162:165], v[46:49]
	v_mfma_f32_16x16x32_bf16 v[26:29], v[102:105], v[170:173], v[26:29]
	v_mfma_f32_16x16x32_bf16 v[30:33], v[118:121], v[170:173], v[30:33]
	v_mfma_f32_16x16x32_bf16 v[10:13], v[102:105], v[178:181], v[10:13]
	v_mfma_f32_16x16x32_bf16 v[14:17], v[118:121], v[178:181], v[14:17]
	s_setprio 0
	s_barrier
	v_add_u32_e32 v94, 0x18000, v209
	v_add_u32_e32 v118, 0x1c000, v209
	ds_read_b128 v[74:77], v94
	ds_read_b128 v[86:89], v94 offset:1024
	ds_read_b128 v[90:93], v94 offset:2048
	ds_read_b128 v[94:97], v94 offset:3072
	ds_read_b128 v[98:101], v118
	ds_read_b128 v[102:105], v118 offset:1024
	ds_read_b128 v[110:113], v118 offset:2048
	ds_read_b128 v[118:121], v118 offset:3072
	ds_read_b128 v[142:145], v223 offset:32768
	ds_read_b128 v[146:149], v223 offset:33792
	ds_read_b128 v[162:165], v223 offset:34816
	ds_read_b128 v[166:169], v223 offset:35840
	ds_read_b128 v[170:173], v223 offset:36864
	ds_read_b128 v[174:177], v223 offset:37888
	ds_read_b128 v[198:201], v223 offset:38912
	ds_read_b128 v[224:227], v223 offset:39936
	s_mov_b32 m0, s53
	s_nop 0
	global_load_lds_dwordx4 v195, s[44:45]
	s_mov_b32 m0, s54
	s_nop 0
	global_load_lds_dwordx4 v197, s[44:45]
	s_waitcnt vmcnt(8)
	s_waitcnt lgkmcnt(0)
	s_barrier
	s_setprio 1
	v_mfma_f32_16x16x32_bf16 v[150:153], v[74:77], v[142:145], v[190:193]
	v_mfma_f32_16x16x32_bf16 v[190:193], v[86:89], v[146:149], v[150:153]
	v_mfma_f32_16x16x32_bf16 v[150:153], v[90:93], v[142:145], v[186:189]
	v_mfma_f32_16x16x32_bf16 v[186:189], v[94:97], v[146:149], v[150:153]
	v_mfma_f32_16x16x32_bf16 v[150:153], v[74:77], v[162:165], v[158:161]
	v_mfma_f32_16x16x32_bf16 v[158:161], v[86:89], v[166:169], v[150:153]
	v_mfma_f32_16x16x32_bf16 v[150:153], v[90:93], v[162:165], v[154:157]
	v_mfma_f32_16x16x32_bf16 v[126:129], v[74:77], v[170:173], v[126:129]
	v_mfma_f32_16x16x32_bf16 v[122:125], v[90:93], v[170:173], v[122:125]
	v_mfma_f32_16x16x32_bf16 v[82:85], v[74:77], v[198:201], v[82:85]
	v_mfma_f32_16x16x32_bf16 v[78:81], v[90:93], v[198:201], v[78:81]
	v_mfma_f32_16x16x32_bf16 v[154:157], v[94:97], v[166:169], v[150:153]
	v_mfma_f32_16x16x32_bf16 v[126:129], v[86:89], v[174:177], v[126:129]
	v_mfma_f32_16x16x32_bf16 v[122:125], v[94:97], v[174:177], v[122:125]
	v_mfma_f32_16x16x32_bf16 v[82:85], v[86:89], v[224:227], v[82:85]
	v_mfma_f32_16x16x32_bf16 v[78:81], v[94:97], v[224:227], v[78:81]
	v_mfma_f32_16x16x32_bf16 v[130:133], v[110:113], v[142:145], v[130:133]
	v_mfma_f32_16x16x32_bf16 v[150:153], v[98:101], v[142:145], v[182:185]
	v_mfma_f32_16x16x32_bf16 v[178:181], v[118:121], v[146:149], v[130:133]
	v_mfma_f32_16x16x32_bf16 v[130:133], v[98:101], v[162:165], v[134:137]
	v_mfma_f32_16x16x32_bf16 v[182:185], v[102:105], v[146:149], v[150:153]
	v_mfma_f32_16x16x32_bf16 v[150:153], v[102:105], v[166:169], v[130:133]
	v_mfma_f32_16x16x32_bf16 v[130:133], v[110:113], v[162:165], v[138:141]
	v_mfma_f32_16x16x32_bf16 v[114:117], v[98:101], v[170:173], v[114:117]
	v_mfma_f32_16x16x32_bf16 v[106:109], v[110:113], v[170:173], v[106:109]
	v_mfma_f32_16x16x32_bf16 v[70:73], v[98:101], v[198:201], v[70:73]
	v_mfma_f32_16x16x32_bf16 v[66:69], v[110:113], v[198:201], v[66:69]
	v_mfma_f32_16x16x32_bf16 v[146:149], v[118:121], v[166:169], v[130:133]
	v_mfma_f32_16x16x32_bf16 v[114:117], v[102:105], v[174:177], v[114:117]
	v_mfma_f32_16x16x32_bf16 v[106:109], v[118:121], v[174:177], v[106:109]
	v_mfma_f32_16x16x32_bf16 v[70:73], v[102:105], v[224:227], v[70:73]
	v_mfma_f32_16x16x32_bf16 v[66:69], v[118:121], v[224:227], v[66:69]
	s_setprio 0
	s_barrier
	ds_read_b128 v[130:133], v223 offset:49152
	ds_read_b128 v[134:137], v223 offset:50176
	ds_read_b128 v[138:141], v223 offset:51200
	ds_read_b128 v[142:145], v223 offset:52224
	ds_read_b128 v[162:165], v223 offset:53248
	ds_read_b128 v[166:169], v223 offset:54272
	ds_read_b128 v[170:173], v223 offset:55296
	ds_read_b128 v[174:177], v223 offset:56320
	s_add_u32 s2, s40, 0x80
	s_addc_u32 s3, s41, 0
	s_mov_b32 m0, s57
	s_nop 0
	global_load_lds_dwordx4 v1, s[2:3]
	s_mov_b32 m0, s58
	s_nop 0
	global_load_lds_dwordx4 v206, s[2:3]
	s_add_u32 s2, s40, 0x18080
	s_addc_u32 s3, s41, 0
	s_mov_b32 m0, s34
	s_nop 0
	global_load_lds_dwordx4 v1, s[2:3]
	s_mov_b32 m0, s35
	s_nop 0
	global_load_lds_dwordx4 v206, s[2:3]
	s_mov_b32 m0, s59
	s_nop 0
	global_load_lds_dwordx4 v194, s[42:43]
	s_mov_b32 m0, s60
	s_nop 0
	global_load_lds_dwordx4 v196, s[42:43]
	s_waitcnt vmcnt(8)
	s_waitcnt lgkmcnt(0)
	s_barrier
	s_setprio 1
	v_mfma_f32_16x16x32_bf16 v[54:57], v[74:77], v[130:133], v[54:57]
	v_mfma_f32_16x16x32_bf16 v[50:53], v[90:93], v[130:133], v[50:53]
	v_mfma_f32_16x16x32_bf16 v[38:41], v[74:77], v[138:141], v[38:41]
	v_mfma_f32_16x16x32_bf16 v[34:37], v[90:93], v[138:141], v[34:37]
	v_mfma_f32_16x16x32_bf16 v[22:25], v[74:77], v[162:165], v[22:25]
	v_mfma_f32_16x16x32_bf16 v[18:21], v[90:93], v[162:165], v[18:21]
	v_mfma_f32_16x16x32_bf16 v[6:9], v[74:77], v[170:173], v[6:9]
	v_mfma_f32_16x16x32_bf16 v[2:5], v[90:93], v[170:173], v[2:5]
	v_mfma_f32_16x16x32_bf16 v[54:57], v[86:89], v[134:137], v[54:57]
	v_mfma_f32_16x16x32_bf16 v[50:53], v[94:97], v[134:137], v[50:53]
	v_mfma_f32_16x16x32_bf16 v[38:41], v[86:89], v[142:145], v[38:41]
	v_mfma_f32_16x16x32_bf16 v[34:37], v[94:97], v[142:145], v[34:37]
	v_mfma_f32_16x16x32_bf16 v[22:25], v[86:89], v[166:169], v[22:25]
	v_mfma_f32_16x16x32_bf16 v[18:21], v[94:97], v[166:169], v[18:21]
	v_mfma_f32_16x16x32_bf16 v[6:9], v[86:89], v[174:177], v[6:9]
	v_mfma_f32_16x16x32_bf16 v[2:5], v[94:97], v[174:177], v[2:5]
	v_mfma_f32_16x16x32_bf16 v[58:61], v[98:101], v[130:133], v[58:61]
	v_mfma_f32_16x16x32_bf16 v[62:65], v[110:113], v[130:133], v[62:65]
	v_mfma_f32_16x16x32_bf16 v[42:45], v[98:101], v[138:141], v[42:45]
	v_mfma_f32_16x16x32_bf16 v[46:49], v[110:113], v[138:141], v[46:49]
	v_mfma_f32_16x16x32_bf16 v[26:29], v[98:101], v[162:165], v[26:29]
	v_mfma_f32_16x16x32_bf16 v[30:33], v[110:113], v[162:165], v[30:33]
	v_mfma_f32_16x16x32_bf16 v[10:13], v[98:101], v[170:173], v[10:13]
	v_mfma_f32_16x16x32_bf16 v[14:17], v[110:113], v[170:173], v[14:17]
	v_mfma_f32_16x16x32_bf16 v[58:61], v[102:105], v[134:137], v[58:61]
	v_mfma_f32_16x16x32_bf16 v[62:65], v[118:121], v[134:137], v[62:65]
	v_mfma_f32_16x16x32_bf16 v[42:45], v[102:105], v[142:145], v[42:45]
	v_mfma_f32_16x16x32_bf16 v[46:49], v[118:121], v[142:145], v[46:49]
	v_mfma_f32_16x16x32_bf16 v[26:29], v[102:105], v[166:169], v[26:29]
	v_mfma_f32_16x16x32_bf16 v[30:33], v[118:121], v[166:169], v[30:33]
	v_mfma_f32_16x16x32_bf16 v[10:13], v[102:105], v[174:177], v[10:13]
	v_mfma_f32_16x16x32_bf16 v[14:17], v[118:121], v[174:177], v[14:17]
	s_setprio 0
	s_barrier
	s_add_i32 s5, s5, 2
	s_add_u32 s0, s0, 0x100
	s_addc_u32 s1, s1, 0
	s_cmp_gt_u32 s5, 3
	s_mov_b64 s[2:3], s[22:23]
	s_cbranch_scc0 .LBB0_793
	s_and_b64 vcc, exec, s[10:11]
	s_cbranch_vccz .LBB0_796
	s_barrier

.LBB0_857:
	s_add_u32 s5, s44, s50
	s_addc_u32 s13, s45, s51
	s_add_u32 s16, s5, 0x100
	s_addc_u32 s17, s13, 0
	s_and_b64 s[0:1], s[48:49], exec
	s_cselect_b32 s55, s41, s17
	s_cselect_b32 s54, s40, s16
	s_add_u32 s0, s42, s50
	s_addc_u32 s1, s43, s51
	s_add_u32 s16, s0, 0x100
	s_addc_u32 s17, s1, 0
	s_add_u32 s50, s54, 0x80
	s_addc_u32 s51, s55, 0
	s_and_b64 s[0:1], s[48:49], exec
	s_cselect_b32 s57, s39, s17
	s_cselect_b32 s56, s38, s16
	s_add_u32 s60, s5, 0x80
	v_add_u32_e32 v14, 0x10000, v207
	v_add_u32_e32 v30, 0x14000, v207
	s_addc_u32 s61, s13, 0
	ds_read_b128 v[2:5], v14
	ds_read_b128 v[6:9], v14 offset:1024
	ds_read_b128 v[10:13], v14 offset:2048
	ds_read_b128 v[14:17], v14 offset:3072
	ds_read_b128 v[18:21], v30
	ds_read_b128 v[22:25], v30 offset:1024
	ds_read_b128 v[26:29], v30 offset:2048
	ds_read_b128 v[30:33], v30 offset:3072
	s_add_u32 s58, s56, 0x10000
	s_addc_u32 s59, s57, 0
	s_add_u32 s52, s56, 0x80
	s_addc_u32 s53, s57, 0
	s_add_u32 s48, s56, 0x10080
	s_addc_u32 s49, s57, 0
	ds_read_b128 v[34:37], v208
	ds_read_b128 v[38:41], v208 offset:1024
	ds_read_b128 v[42:45], v208 offset:2048
	ds_read_b128 v[46:49], v208 offset:3072
	ds_read_b128 v[50:53], v208 offset:4096
	ds_read_b128 v[54:57], v208 offset:5120
	ds_read_b128 v[58:61], v208 offset:6144
	ds_read_b128 v[62:65], v208 offset:7168
	s_mov_b32 m0, s21
	s_nop 0
	global_load_lds_dwordx4 v199, s[60:61]
	s_mov_b32 m0, s75
	s_nop 0
	global_load_lds_dwordx4 v200, s[60:61]
	s_waitcnt vmcnt(8)
	s_waitcnt lgkmcnt(0)
	s_barrier
	s_setprio 1
	v_mfma_f32_16x16x32_bf16 v[190:193], v[2:5], v[34:37], v[190:193]
	v_mfma_f32_16x16x32_bf16 v[186:189], v[10:13], v[34:37], v[186:189]
	v_mfma_f32_16x16x32_bf16 v[174:177], v[2:5], v[42:45], v[174:177]
	v_mfma_f32_16x16x32_bf16 v[170:173], v[10:13], v[42:45], v[170:173]
	v_mfma_f32_16x16x32_bf16 v[158:161], v[2:5], v[50:53], v[158:161]
	v_mfma_f32_16x16x32_bf16 v[154:157], v[10:13], v[50:53], v[154:157]
	v_mfma_f32_16x16x32_bf16 v[142:145], v[2:5], v[58:61], v[142:145]
	v_mfma_f32_16x16x32_bf16 v[138:141], v[10:13], v[58:61], v[138:141]
	v_mfma_f32_16x16x32_bf16 v[190:193], v[6:9], v[38:41], v[190:193]
	v_mfma_f32_16x16x32_bf16 v[186:189], v[14:17], v[38:41], v[186:189]
	v_mfma_f32_16x16x32_bf16 v[174:177], v[6:9], v[46:49], v[174:177]
	v_mfma_f32_16x16x32_bf16 v[170:173], v[14:17], v[46:49], v[170:173]
	v_mfma_f32_16x16x32_bf16 v[158:161], v[6:9], v[54:57], v[158:161]
	v_mfma_f32_16x16x32_bf16 v[154:157], v[14:17], v[54:57], v[154:157]
	v_mfma_f32_16x16x32_bf16 v[142:145], v[6:9], v[62:65], v[142:145]
	v_mfma_f32_16x16x32_bf16 v[138:141], v[14:17], v[62:65], v[138:141]
	v_mfma_f32_16x16x32_bf16 v[182:185], v[18:21], v[34:37], v[182:185]
	v_mfma_f32_16x16x32_bf16 v[34:37], v[26:29], v[34:37], v[178:181]
	v_mfma_f32_16x16x32_bf16 v[182:185], v[22:25], v[38:41], v[182:185]
	v_mfma_f32_16x16x32_bf16 v[34:37], v[30:33], v[38:41], v[34:37]
	v_mfma_f32_16x16x32_bf16 v[38:41], v[18:21], v[42:45], v[166:169]
	v_mfma_f32_16x16x32_bf16 v[42:45], v[26:29], v[42:45], v[162:165]
	v_mfma_f32_16x16x32_bf16 v[38:41], v[22:25], v[46:49], v[38:41]
	v_mfma_f32_16x16x32_bf16 v[42:45], v[30:33], v[46:49], v[42:45]
	v_mfma_f32_16x16x32_bf16 v[46:49], v[18:21], v[50:53], v[150:153]
	v_mfma_f32_16x16x32_bf16 v[50:53], v[26:29], v[50:53], v[146:149]
	v_mfma_f32_16x16x32_bf16 v[46:49], v[22:25], v[54:57], v[46:49]
	v_mfma_f32_16x16x32_bf16 v[50:53], v[30:33], v[54:57], v[50:53]
	v_mfma_f32_16x16x32_bf16 v[54:57], v[18:21], v[58:61], v[134:137]
	v_mfma_f32_16x16x32_bf16 v[58:61], v[26:29], v[58:61], v[130:133]
	v_mfma_f32_16x16x32_bf16 v[54:57], v[22:25], v[62:65], v[54:57]
	v_mfma_f32_16x16x32_bf16 v[58:61], v[30:33], v[62:65], v[58:61]
	s_setprio 0
	s_barrier
	ds_read_b128 v[62:65], v208 offset:16384
	ds_read_b128 v[130:133], v208 offset:17408
	ds_read_b128 v[134:137], v208 offset:18432
	ds_read_b128 v[146:149], v208 offset:19456
	ds_read_b128 v[150:153], v208 offset:20480
	ds_read_b128 v[162:165], v208 offset:21504
	ds_read_b128 v[166:169], v208 offset:22528
	ds_read_b128 v[178:181], v208 offset:23552
	s_mov_b32 m0, s37
	s_nop 0
	global_load_lds_dwordx4 v1, s[56:57]
	s_mov_b32 m0, s62
	s_nop 0
	global_load_lds_dwordx4 v196, s[56:57]
	s_mov_b32 m0, s63
	s_nop 0
	global_load_lds_dwordx4 v1, s[58:59]
	s_mov_b32 m0, s64
	s_nop 0
	global_load_lds_dwordx4 v196, s[58:59]
	s_mov_b32 m0, s35
	s_nop 0
	global_load_lds_dwordx4 v197, s[54:55]
	s_mov_b32 m0, s65
	s_nop 0
	global_load_lds_dwordx4 v198, s[54:55]
	s_waitcnt vmcnt(8)
	s_waitcnt lgkmcnt(0)
	s_barrier
	s_setprio 1
	v_mfma_f32_16x16x32_bf16 v[118:121], v[2:5], v[62:65], v[118:121]
	v_mfma_f32_16x16x32_bf16 v[114:117], v[10:13], v[62:65], v[114:117]
	v_mfma_f32_16x16x32_bf16 v[102:105], v[2:5], v[134:137], v[102:105]
	v_mfma_f32_16x16x32_bf16 v[98:101], v[10:13], v[134:137], v[98:101]
	v_mfma_f32_16x16x32_bf16 v[86:89], v[2:5], v[150:153], v[86:89]
	v_mfma_f32_16x16x32_bf16 v[82:85], v[10:13], v[150:153], v[82:85]
	v_mfma_f32_16x16x32_bf16 v[2:5], v[2:5], v[166:169], v[70:73]
	v_mfma_f32_16x16x32_bf16 v[118:121], v[6:9], v[130:133], v[118:121]
	v_mfma_f32_16x16x32_bf16 v[114:117], v[14:17], v[130:133], v[114:117]
	v_mfma_f32_16x16x32_bf16 v[102:105], v[6:9], v[146:149], v[102:105]
	v_mfma_f32_16x16x32_bf16 v[98:101], v[14:17], v[146:149], v[98:101]
	v_mfma_f32_16x16x32_bf16 v[86:89], v[6:9], v[162:165], v[86:89]
	v_mfma_f32_16x16x32_bf16 v[82:85], v[14:17], v[162:165], v[82:85]
	v_mfma_f32_16x16x32_bf16 v[2:5], v[6:9], v[178:181], v[2:5]
	v_mfma_f32_16x16x32_bf16 v[6:9], v[10:13], v[166:169], v[66:69]
	v_mfma_f32_16x16x32_bf16 v[6:9], v[14:17], v[178:181], v[6:9]
	v_mfma_f32_16x16x32_bf16 v[66:69], v[26:29], v[134:137], v[110:113]
	v_mfma_f32_16x16x32_bf16 v[110:113], v[30:33], v[146:149], v[66:69]
	v_mfma_f32_16x16x32_bf16 v[66:69], v[18:21], v[150:153], v[90:93]
	v_mfma_f32_16x16x32_bf16 v[10:13], v[18:21], v[62:65], v[122:125]
	v_mfma_f32_16x16x32_bf16 v[14:17], v[26:29], v[62:65], v[126:129]
	v_mfma_f32_16x16x32_bf16 v[62:65], v[18:21], v[134:137], v[106:109]
	v_mfma_f32_16x16x32_bf16 v[90:93], v[22:25], v[162:165], v[66:69]
	v_mfma_f32_16x16x32_bf16 v[66:69], v[26:29], v[150:153], v[94:97]
	v_mfma_f32_16x16x32_bf16 v[18:21], v[18:21], v[166:169], v[74:77]
	v_mfma_f32_16x16x32_bf16 v[10:13], v[22:25], v[130:133], v[10:13]
	v_mfma_f32_16x16x32_bf16 v[62:65], v[22:25], v[146:149], v[62:65]
	v_mfma_f32_16x16x32_bf16 v[94:97], v[30:33], v[162:165], v[66:69]
	v_mfma_f32_16x16x32_bf16 v[18:21], v[22:25], v[178:181], v[18:21]
	v_mfma_f32_16x16x32_bf16 v[22:25], v[26:29], v[166:169], v[78:81]
	v_mfma_f32_16x16x32_bf16 v[14:17], v[30:33], v[130:133], v[14:17]
	v_mfma_f32_16x16x32_bf16 v[22:25], v[30:33], v[178:181], v[22:25]
	s_setprio 0
	s_barrier
	v_add_u32_e32 v70, 0x18000, v207
	ds_read_b128 v[26:29], v70
	ds_read_b128 v[30:33], v70 offset:1024
	ds_read_b128 v[66:69], v70 offset:2048
	ds_read_b128 v[74:77], v70 offset:3072
	v_add_u32_e32 v70, 0x1c000, v207
	ds_read_b128 v[78:81], v70
	ds_read_b128 v[224:227], v70 offset:1024
	ds_read_b128 v[228:231], v70 offset:2048
	ds_read_b128 v[232:235], v70 offset:3072
	ds_read_b128 v[70:73], v208 offset:32768
	ds_read_b128 v[106:109], v208 offset:33792
	ds_read_b128 v[122:125], v208 offset:34816
	ds_read_b128 v[126:129], v208 offset:35840
	ds_read_b128 v[130:133], v208 offset:36864
	ds_read_b128 v[134:137], v208 offset:37888
	ds_read_b128 v[236:239], v208 offset:38912
	ds_read_b128 v[240:243], v208 offset:39936
	s_mov_b32 m0, s66
	s_nop 0
	global_load_lds_dwordx4 v199, s[54:55]
	s_mov_b32 m0, s67
	s_nop 0
	global_load_lds_dwordx4 v200, s[54:55]
	s_waitcnt vmcnt(8)
	s_waitcnt lgkmcnt(0)
	s_barrier
	s_setprio 1
	v_mfma_f32_16x16x32_bf16 v[146:149], v[26:29], v[70:73], v[190:193]
	v_mfma_f32_16x16x32_bf16 v[190:193], v[30:33], v[106:109], v[146:149]
	v_mfma_f32_16x16x32_bf16 v[146:149], v[66:69], v[70:73], v[186:189]
	v_mfma_f32_16x16x32_bf16 v[186:189], v[74:77], v[106:109], v[146:149]
	v_mfma_f32_16x16x32_bf16 v[146:149], v[26:29], v[122:125], v[174:177]
	v_mfma_f32_16x16x32_bf16 v[174:177], v[30:33], v[126:129], v[146:149]
	v_mfma_f32_16x16x32_bf16 v[146:149], v[66:69], v[122:125], v[170:173]
	v_mfma_f32_16x16x32_bf16 v[170:173], v[74:77], v[126:129], v[146:149]
	v_mfma_f32_16x16x32_bf16 v[146:149], v[26:29], v[130:133], v[158:161]
	v_mfma_f32_16x16x32_bf16 v[158:161], v[30:33], v[134:137], v[146:149]
	v_mfma_f32_16x16x32_bf16 v[146:149], v[66:69], v[130:133], v[154:157]
	v_mfma_f32_16x16x32_bf16 v[142:145], v[26:29], v[236:239], v[142:145]
	v_mfma_f32_16x16x32_bf16 v[138:141], v[66:69], v[236:239], v[138:141]
	v_mfma_f32_16x16x32_bf16 v[154:157], v[74:77], v[134:137], v[146:149]
	v_mfma_f32_16x16x32_bf16 v[142:145], v[30:33], v[240:243], v[142:145]
	v_mfma_f32_16x16x32_bf16 v[138:141], v[74:77], v[240:243], v[138:141]
	v_mfma_f32_16x16x32_bf16 v[34:37], v[228:231], v[70:73], v[34:37]
	v_mfma_f32_16x16x32_bf16 v[178:181], v[232:235], v[106:109], v[34:37]
	v_mfma_f32_16x16x32_bf16 v[34:37], v[78:81], v[122:125], v[38:41]
	v_mfma_f32_16x16x32_bf16 v[166:169], v[224:227], v[126:129], v[34:37]
	v_mfma_f32_16x16x32_bf16 v[34:37], v[228:231], v[122:125], v[42:45]
	v_mfma_f32_16x16x32_bf16 v[162:165], v[232:235], v[126:129], v[34:37]
	v_mfma_f32_16x16x32_bf16 v[34:37], v[78:81], v[130:133], v[46:49]
	v_mfma_f32_16x16x32_bf16 v[146:149], v[78:81], v[70:73], v[182:185]
	v_mfma_f32_16x16x32_bf16 v[150:153], v[224:227], v[134:137], v[34:37]
	v_mfma_f32_16x16x32_bf16 v[34:37], v[228:231], v[130:133], v[50:53]
	v_mfma_f32_16x16x32_bf16 v[182:185], v[224:227], v[106:109], v[146:149]
	v_mfma_f32_16x16x32_bf16 v[146:149], v[232:235], v[134:137], v[34:37]
	v_mfma_f32_16x16x32_bf16 v[34:37], v[78:81], v[236:239], v[54:57]
	v_mfma_f32_16x16x32_bf16 v[134:137], v[224:227], v[240:243], v[34:37]
	v_mfma_f32_16x16x32_bf16 v[34:37], v[228:231], v[236:239], v[58:61]
	v_mfma_f32_16x16x32_bf16 v[130:133], v[232:235], v[240:243], v[34:37]
	s_setprio 0
	s_barrier
	s_nop 4
	ds_read_b128 v[34:37], v208 offset:49152
	ds_read_b128 v[38:41], v208 offset:50176
	ds_read_b128 v[42:45], v208 offset:51200
	ds_read_b128 v[46:49], v208 offset:52224
	ds_read_b128 v[50:53], v208 offset:53248
	ds_read_b128 v[54:57], v208 offset:54272
	ds_read_b128 v[58:61], v208 offset:55296
	ds_read_b128 v[236:239], v208 offset:56320
	s_mov_b32 m0, s69
	s_nop 0
	global_load_lds_dwordx4 v1, s[52:53]
	s_mov_b32 m0, s70
	s_nop 0
	global_load_lds_dwordx4 v196, s[52:53]
	s_mov_b32 m0, s73
	s_nop 0
	global_load_lds_dwordx4 v1, s[48:49]
	s_mov_b32 m0, s74
	s_nop 0
	global_load_lds_dwordx4 v196, s[48:49]
	s_mov_b32 m0, s71
	s_nop 0
	global_load_lds_dwordx4 v197, s[50:51]
	s_mov_b32 m0, s72
	s_nop 0
	global_load_lds_dwordx4 v198, s[50:51]
	s_waitcnt vmcnt(8)
	s_waitcnt lgkmcnt(0)
	s_barrier
	s_setprio 1
	v_mfma_f32_16x16x32_bf16 v[70:73], v[26:29], v[34:37], v[118:121]
	v_mfma_f32_16x16x32_bf16 v[118:121], v[30:33], v[38:41], v[70:73]
	v_mfma_f32_16x16x32_bf16 v[70:73], v[66:69], v[34:37], v[114:117]
	v_mfma_f32_16x16x32_bf16 v[114:117], v[74:77], v[38:41], v[70:73]
	v_mfma_f32_16x16x32_bf16 v[70:73], v[26:29], v[42:45], v[102:105]
	v_mfma_f32_16x16x32_bf16 v[102:105], v[30:33], v[46:49], v[70:73]
	v_mfma_f32_16x16x32_bf16 v[70:73], v[66:69], v[42:45], v[98:101]
	v_mfma_f32_16x16x32_bf16 v[98:101], v[74:77], v[46:49], v[70:73]
	v_mfma_f32_16x16x32_bf16 v[70:73], v[26:29], v[50:53], v[86:89]
	v_mfma_f32_16x16x32_bf16 v[86:89], v[30:33], v[54:57], v[70:73]
	v_mfma_f32_16x16x32_bf16 v[70:73], v[66:69], v[50:53], v[82:85]
	v_mfma_f32_16x16x32_bf16 v[2:5], v[26:29], v[58:61], v[2:5]
	v_mfma_f32_16x16x32_bf16 v[82:85], v[74:77], v[54:57], v[70:73]
	v_mfma_f32_16x16x32_bf16 v[70:73], v[30:33], v[236:239], v[2:5]
	v_mfma_f32_16x16x32_bf16 v[2:5], v[66:69], v[58:61], v[6:9]
	v_mfma_f32_16x16x32_bf16 v[66:69], v[74:77], v[236:239], v[2:5]
	v_mfma_f32_16x16x32_bf16 v[2:5], v[78:81], v[34:37], v[10:13]
	v_mfma_f32_16x16x32_bf16 v[122:125], v[224:227], v[38:41], v[2:5]
	v_mfma_f32_16x16x32_bf16 v[2:5], v[228:231], v[34:37], v[14:17]
	v_mfma_f32_16x16x32_bf16 v[126:129], v[232:235], v[38:41], v[2:5]
	v_mfma_f32_16x16x32_bf16 v[2:5], v[78:81], v[42:45], v[62:65]
	v_mfma_f32_16x16x32_bf16 v[106:109], v[224:227], v[46:49], v[2:5]
	v_mfma_f32_16x16x32_bf16 v[2:5], v[228:231], v[42:45], v[110:113]
	v_mfma_f32_16x16x32_bf16 v[110:113], v[232:235], v[46:49], v[2:5]
	v_mfma_f32_16x16x32_bf16 v[2:5], v[78:81], v[50:53], v[90:93]
	v_mfma_f32_16x16x32_bf16 v[90:93], v[224:227], v[54:57], v[2:5]
	v_mfma_f32_16x16x32_bf16 v[2:5], v[228:231], v[50:53], v[94:97]
	v_mfma_f32_16x16x32_bf16 v[94:97], v[232:235], v[54:57], v[2:5]
	v_mfma_f32_16x16x32_bf16 v[2:5], v[78:81], v[58:61], v[18:21]
	v_mfma_f32_16x16x32_bf16 v[74:77], v[224:227], v[236:239], v[2:5]
	v_mfma_f32_16x16x32_bf16 v[2:5], v[228:231], v[58:61], v[22:25]
	v_mfma_f32_16x16x32_bf16 v[78:81], v[232:235], v[236:239], v[2:5]
	s_setprio 0
	s_barrier
	s_andn2_b64 vcc, exec, s[46:47]
	s_mov_b64 s[48:49], -1
	s_mov_b64 s[46:47], 0
	s_mov_b64 s[50:51], 0x100
	s_cbranch_vccz .LBB0_857
	s_and_b64 vcc, exec, s[10:11]
	s_cbranch_vccz .LBB0_860
	s_barrier

.LBB0_1161:
	v_add_u32_e32 v130, 0x10000, v209
	v_add_u32_e32 v134, 0x14000, v209
	ds_read_b128 v[154:157], v130
	ds_read_b128 v[158:161], v130 offset:1024
	ds_read_b128 v[146:149], v130 offset:2048
	ds_read_b128 v[150:153], v130 offset:3072
	ds_read_b128 v[138:141], v134
	ds_read_b128 v[142:145], v134 offset:1024
	ds_read_b128 v[130:133], v134 offset:2048
	ds_read_b128 v[134:137], v134 offset:3072
	s_cmp_eq_u32 s19, 4
	s_cselect_b32 s48, s40, s17
	s_cselect_b32 s49, s41, s18
	s_cselect_b32 s46, s12, s5
	s_cselect_b32 s47, s13, s16
	s_add_u32 s44, s48, 0x80
	s_addc_u32 s45, s49, 0
	ds_read_b128 v[162:165], v223
	ds_read_b128 v[166:169], v223 offset:1024
	ds_read_b128 v[170:173], v223 offset:2048
	ds_read_b128 v[174:177], v223 offset:3072
	ds_read_b128 v[178:181], v223 offset:4096
	ds_read_b128 v[182:185], v223 offset:5120
	ds_read_b128 v[186:189], v223 offset:6144
	ds_read_b128 v[190:193], v223 offset:7168
	s_mov_b32 m0, s66
	s_nop 0
	global_load_lds_dwordx4 v201, s[42:43]
	s_mov_b32 m0, s67
	s_nop 0
	global_load_lds_dwordx4 v206, s[42:43]
	s_waitcnt vmcnt(8)
	s_waitcnt lgkmcnt(0)
	s_barrier
	s_setprio 1
	v_mfma_f32_16x16x128_f8f6f4 v[114:117], v[154:161], v[162:169], v[114:117]
	v_mfma_f32_16x16x128_f8f6f4 v[118:121], v[146:153], v[162:169], v[118:121]
	v_mfma_f32_16x16x128_f8f6f4 v[122:125], v[154:161], v[170:177], v[122:125]
	v_mfma_f32_16x16x128_f8f6f4 v[126:129], v[146:153], v[170:177], v[126:129]
	v_mfma_f32_16x16x128_f8f6f4 v[82:85], v[154:161], v[178:185], v[82:85]
	v_mfma_f32_16x16x128_f8f6f4 v[86:89], v[146:153], v[178:185], v[86:89]
	v_mfma_f32_16x16x128_f8f6f4 v[90:93], v[154:161], v[186:193], v[90:93]
	v_mfma_f32_16x16x128_f8f6f4 v[94:97], v[146:153], v[186:193], v[94:97]
	v_mfma_f32_16x16x128_f8f6f4 v[98:101], v[138:145], v[162:169], v[98:101]
	v_mfma_f32_16x16x128_f8f6f4 v[102:105], v[130:137], v[162:169], v[102:105]
	v_mfma_f32_16x16x128_f8f6f4 v[106:109], v[138:145], v[170:177], v[106:109]
	v_mfma_f32_16x16x128_f8f6f4 v[110:113], v[130:137], v[170:177], v[110:113]
	v_mfma_f32_16x16x128_f8f6f4 v[66:69], v[138:145], v[178:185], v[66:69]
	v_mfma_f32_16x16x128_f8f6f4 v[70:73], v[130:137], v[178:185], v[70:73]
	v_mfma_f32_16x16x128_f8f6f4 v[74:77], v[138:145], v[186:193], v[74:77]
	v_mfma_f32_16x16x128_f8f6f4 v[78:81], v[130:137], v[186:193], v[78:81]
	s_setprio 0
	s_barrier
	ds_read_b128 v[162:165], v223 offset:16384
	ds_read_b128 v[166:169], v223 offset:17408
	ds_read_b128 v[170:173], v223 offset:18432
	ds_read_b128 v[174:177], v223 offset:19456
	ds_read_b128 v[178:181], v223 offset:20480
	ds_read_b128 v[182:185], v223 offset:21504
	ds_read_b128 v[186:189], v223 offset:22528
	ds_read_b128 v[190:193], v223 offset:23552
	s_mov_b32 m0, s52
	s_nop 0
	global_load_lds_dwordx4 v1, s[46:47]
	s_mov_b32 m0, s53
	s_nop 0
	global_load_lds_dwordx4 v198, s[46:47]
	s_add_u32 s0, s46, 0x20000
	s_addc_u32 s1, s47, 0
	s_mov_b32 m0, s54
	s_nop 0
	global_load_lds_dwordx4 v1, s[0:1]
	s_mov_b32 m0, s55
	s_nop 0
	global_load_lds_dwordx4 v198, s[0:1]
	s_mov_b32 m0, s51
	s_nop 0
	global_load_lds_dwordx4 v199, s[48:49]
	s_mov_b32 m0, s56
	s_nop 0
	global_load_lds_dwordx4 v200, s[48:49]
	s_waitcnt vmcnt(8)
	s_waitcnt lgkmcnt(0)
	s_barrier
	s_setprio 1
	v_mfma_f32_16x16x128_f8f6f4 v[50:53], v[154:161], v[162:169], v[50:53]
	v_mfma_f32_16x16x128_f8f6f4 v[54:57], v[146:153], v[162:169], v[54:57]
	v_mfma_f32_16x16x128_f8f6f4 v[58:61], v[154:161], v[170:177], v[58:61]
	v_mfma_f32_16x16x128_f8f6f4 v[62:65], v[146:153], v[170:177], v[62:65]
	v_mfma_f32_16x16x128_f8f6f4 v[194:197], v[154:161], v[178:185], v[18:21]
	v_mfma_f32_16x16x128_f8f6f4 v[218:221], v[146:153], v[178:185], v[22:25]
	v_mfma_f32_16x16x128_f8f6f4 v[224:227], v[154:161], v[186:193], v[26:29]
	v_mfma_f32_16x16x128_f8f6f4 v[228:231], v[146:153], v[186:193], v[30:33]
	v_mfma_f32_16x16x128_f8f6f4 v[232:235], v[138:145], v[162:169], v[34:37]
	v_mfma_f32_16x16x128_f8f6f4 v[236:239], v[130:137], v[162:169], v[38:41]
	v_mfma_f32_16x16x128_f8f6f4 v[240:243], v[138:145], v[170:177], v[42:45]
	v_mfma_f32_16x16x128_f8f6f4 v[170:173], v[130:137], v[170:177], v[46:49]
	v_mfma_f32_16x16x128_f8f6f4 v[174:177], v[138:145], v[178:185], v[2:5]
	v_mfma_f32_16x16x128_f8f6f4 v[178:181], v[130:137], v[178:185], v[6:9]
	v_mfma_f32_16x16x128_f8f6f4 v[182:185], v[138:145], v[186:193], v[10:13]
	v_mfma_f32_16x16x128_f8f6f4 v[186:189], v[130:137], v[186:193], v[14:17]
	s_setprio 0
	s_barrier
	s_nop 4
	v_add_u32_e32 v14, 0x18000, v209
	v_add_u32_e32 v18, 0x1c000, v209
	ds_read_b128 v[2:5], v14
	ds_read_b128 v[6:9], v14 offset:1024
	ds_read_b128 v[10:13], v14 offset:2048
	ds_read_b128 v[14:17], v14 offset:3072
	ds_read_b128 v[130:133], v18
	ds_read_b128 v[134:137], v18 offset:1024
	ds_read_b128 v[138:141], v18 offset:2048
	ds_read_b128 v[142:145], v18 offset:3072
	ds_read_b128 v[18:21], v223 offset:32768
	ds_read_b128 v[22:25], v223 offset:33792
	ds_read_b128 v[26:29], v223 offset:34816
	ds_read_b128 v[30:33], v223 offset:35840
	ds_read_b128 v[34:37], v223 offset:36864
	ds_read_b128 v[38:41], v223 offset:37888
	ds_read_b128 v[42:45], v223 offset:38912
	ds_read_b128 v[46:49], v223 offset:39936
	s_mov_b32 m0, s57
	s_nop 0
	global_load_lds_dwordx4 v201, s[48:49]
	s_mov_b32 m0, s58
	s_nop 0
	global_load_lds_dwordx4 v206, s[48:49]
	s_waitcnt vmcnt(8)
	s_waitcnt lgkmcnt(0)
	s_barrier
	s_setprio 1
	v_mfma_f32_16x16x128_f8f6f4 v[114:117], v[2:9], v[18:25], v[114:117]
	v_mfma_f32_16x16x128_f8f6f4 v[118:121], v[10:17], v[18:25], v[118:121]
	v_mfma_f32_16x16x128_f8f6f4 v[122:125], v[2:9], v[26:33], v[122:125]
	v_mfma_f32_16x16x128_f8f6f4 v[126:129], v[10:17], v[26:33], v[126:129]
	v_mfma_f32_16x16x128_f8f6f4 v[82:85], v[2:9], v[34:41], v[82:85]
	v_mfma_f32_16x16x128_f8f6f4 v[86:89], v[10:17], v[34:41], v[86:89]
	v_mfma_f32_16x16x128_f8f6f4 v[90:93], v[2:9], v[42:49], v[90:93]
	v_mfma_f32_16x16x128_f8f6f4 v[94:97], v[10:17], v[42:49], v[94:97]
	v_mfma_f32_16x16x128_f8f6f4 v[98:101], v[130:137], v[18:25], v[98:101]
	v_mfma_f32_16x16x128_f8f6f4 v[102:105], v[138:145], v[18:25], v[102:105]
	v_mfma_f32_16x16x128_f8f6f4 v[106:109], v[130:137], v[26:33], v[106:109]
	v_mfma_f32_16x16x128_f8f6f4 v[110:113], v[138:145], v[26:33], v[110:113]
	v_mfma_f32_16x16x128_f8f6f4 v[66:69], v[130:137], v[34:41], v[66:69]
	v_mfma_f32_16x16x128_f8f6f4 v[70:73], v[138:145], v[34:41], v[70:73]
	v_mfma_f32_16x16x128_f8f6f4 v[74:77], v[130:137], v[42:49], v[74:77]
	v_mfma_f32_16x16x128_f8f6f4 v[78:81], v[138:145], v[42:49], v[78:81]
	s_setprio 0
	s_barrier
	ds_read_b128 v[38:41], v223 offset:49152
	ds_read_b128 v[42:45], v223 offset:50176
	ds_read_b128 v[146:149], v223 offset:51200
	ds_read_b128 v[150:153], v223 offset:52224
	ds_read_b128 v[154:157], v223 offset:53248
	ds_read_b128 v[158:161], v223 offset:54272
	ds_read_b128 v[162:165], v223 offset:55296
	ds_read_b128 v[166:169], v223 offset:56320
	s_add_u32 s0, s46, 0x80
	s_addc_u32 s1, s47, 0
	s_mov_b32 m0, s60
	s_nop 0
	global_load_lds_dwordx4 v1, s[0:1]
	s_mov_b32 m0, s61
	s_nop 0
	global_load_lds_dwordx4 v198, s[0:1]
	s_add_u32 s0, s46, 0x20080
	s_addc_u32 s1, s47, 0
	s_mov_b32 m0, s64
	s_nop 0
	global_load_lds_dwordx4 v1, s[0:1]
	s_mov_b32 m0, s65
	s_nop 0
	global_load_lds_dwordx4 v198, s[0:1]
	s_mov_b32 m0, s62
	s_nop 0
	global_load_lds_dwordx4 v199, s[44:45]
	s_mov_b32 m0, s63
	s_nop 0
	global_load_lds_dwordx4 v200, s[44:45]
	s_waitcnt vmcnt(8)
	s_waitcnt lgkmcnt(0)
	s_barrier
	s_setprio 1
	v_mfma_f32_16x16x128_f8f6f4 v[50:53], v[2:9], v[38:45], v[50:53]
	v_mfma_f32_16x16x128_f8f6f4 v[54:57], v[10:17], v[38:45], v[54:57]
	v_mfma_f32_16x16x128_f8f6f4 v[58:61], v[2:9], v[146:153], v[58:61]
	v_mfma_f32_16x16x128_f8f6f4 v[62:65], v[10:17], v[146:153], v[62:65]
	v_mfma_f32_16x16x128_f8f6f4 v[18:21], v[2:9], v[154:161], v[194:197]
	v_mfma_f32_16x16x128_f8f6f4 v[22:25], v[10:17], v[154:161], v[218:221]
	v_mfma_f32_16x16x128_f8f6f4 v[26:29], v[2:9], v[162:169], v[224:227]
	v_mfma_f32_16x16x128_f8f6f4 v[30:33], v[10:17], v[162:169], v[228:231]
	v_mfma_f32_16x16x128_f8f6f4 v[34:37], v[130:137], v[38:45], v[232:235]
	v_mfma_f32_16x16x128_f8f6f4 v[38:41], v[138:145], v[38:45], v[236:239]
	v_mfma_f32_16x16x128_f8f6f4 v[42:45], v[130:137], v[146:153], v[240:243]
	v_mfma_f32_16x16x128_f8f6f4 v[46:49], v[138:145], v[146:153], v[170:173]
	v_mfma_f32_16x16x128_f8f6f4 v[2:5], v[130:137], v[154:161], v[174:177]
	v_mfma_f32_16x16x128_f8f6f4 v[6:9], v[138:145], v[154:161], v[178:181]
	v_mfma_f32_16x16x128_f8f6f4 v[10:13], v[130:137], v[162:169], v[182:185]
	v_mfma_f32_16x16x128_f8f6f4 v[14:17], v[138:145], v[162:169], v[186:189]
	s_setprio 0
	s_barrier
	s_add_i32 s19, s19, 2
	s_add_u32 s5, s5, 0x100
	s_addc_u32 s16, s16, 0
	s_add_u32 s17, s17, 0x100
	s_addc_u32 s18, s18, 0
	s_add_u32 s42, s42, 0x100
	s_addc_u32 s43, s43, 0
	s_cmp_gt_u32 s19, 5
	s_cbranch_scc0 .LBB0_1161
	s_and_b64 vcc, exec, s[10:11]
	s_cbranch_vccz .LBB0_1164
	s_barrier

.LBB0_1729:
	s_add_u32 s22, s56, 0x100
	s_addc_u32 s23, s57, 0
	v_add_u32_e32 v130, 0x10000, v166
	v_add_u32_e32 v134, 0x14000, v166
	s_cmp_eq_u32 s18, 4
	ds_read_b128 v[154:157], v130
	ds_read_b128 v[158:161], v130 offset:1024
	ds_read_b128 v[146:149], v130 offset:2048
	ds_read_b128 v[150:153], v130 offset:3072
	ds_read_b128 v[138:141], v134
	ds_read_b128 v[142:145], v134 offset:1024
	ds_read_b128 v[130:133], v134 offset:2048
	ds_read_b128 v[134:137], v134 offset:3072
	s_cselect_b64 vcc, -1, 0
	s_and_b64 s[0:1], vcc, exec
	s_cselect_b32 s58, s30, s22
	s_cselect_b32 s59, s31, s23
	s_cselect_b32 s52, s50, s16
	s_cselect_b32 s53, s51, s17
	s_add_u32 s54, s58, 0x80
	s_addc_u32 s55, s59, 0
	s_add_u32 s0, s56, 0x80
	v_cndmask_b32_e32 v200, v171, v168, vcc
	v_cndmask_b32_e32 v201, v174, v170, vcc
	v_cndmask_b32_e32 v202, v172, v169, vcc
	v_cndmask_b32_e32 v223, v175, v173, vcc
	s_addc_u32 s1, s57, 0
	ds_read_b128 v[176:179], v167
	ds_read_b128 v[180:183], v167 offset:1024
	ds_read_b128 v[184:187], v167 offset:2048
	ds_read_b128 v[188:191], v167 offset:3072
	ds_read_b128 v[192:195], v167 offset:4096
	ds_read_b128 v[196:199], v167 offset:5120
	ds_read_b128 v[224:227], v167 offset:6144
	ds_read_b128 v[228:231], v167 offset:7168
	s_mov_b32 m0, s90
	s_nop 0
	global_load_lds_dwordx4 v172, s[0:1]
	s_mov_b32 m0, s91
	s_nop 0
	global_load_lds_dwordx4 v175, s[0:1]
	s_waitcnt vmcnt(8)
	s_waitcnt lgkmcnt(0)
	s_barrier
	s_setprio 1
	v_mfma_f32_16x16x128_f8f6f4 v[114:117], v[154:161], v[176:183], v[114:117]
	v_mfma_f32_16x16x128_f8f6f4 v[118:121], v[146:153], v[176:183], v[118:121]
	v_mfma_f32_16x16x128_f8f6f4 v[122:125], v[154:161], v[184:191], v[122:125]
	v_mfma_f32_16x16x128_f8f6f4 v[126:129], v[146:153], v[184:191], v[126:129]
	v_mfma_f32_16x16x128_f8f6f4 v[82:85], v[154:161], v[192:199], v[82:85]
	v_mfma_f32_16x16x128_f8f6f4 v[86:89], v[146:153], v[192:199], v[86:89]
	v_mfma_f32_16x16x128_f8f6f4 v[90:93], v[154:161], v[224:231], v[90:93]
	v_mfma_f32_16x16x128_f8f6f4 v[94:97], v[146:153], v[224:231], v[94:97]
	v_mfma_f32_16x16x128_f8f6f4 v[98:101], v[138:145], v[176:183], v[98:101]
	v_mfma_f32_16x16x128_f8f6f4 v[102:105], v[130:137], v[176:183], v[102:105]
	v_mfma_f32_16x16x128_f8f6f4 v[106:109], v[138:145], v[184:191], v[106:109]
	v_mfma_f32_16x16x128_f8f6f4 v[110:113], v[130:137], v[184:191], v[110:113]
	v_mfma_f32_16x16x128_f8f6f4 v[66:69], v[138:145], v[192:199], v[66:69]
	v_mfma_f32_16x16x128_f8f6f4 v[70:73], v[130:137], v[192:199], v[70:73]
	v_mfma_f32_16x16x128_f8f6f4 v[74:77], v[138:145], v[224:231], v[74:77]
	v_mfma_f32_16x16x128_f8f6f4 v[78:81], v[130:137], v[224:231], v[78:81]
	s_setprio 0
	s_barrier
	ds_read_b128 v[176:179], v167 offset:16384
	ds_read_b128 v[180:183], v167 offset:17408
	ds_read_b128 v[184:187], v167 offset:18432
	ds_read_b128 v[188:191], v167 offset:19456
	ds_read_b128 v[192:195], v167 offset:20480
	ds_read_b128 v[196:199], v167 offset:21504
	ds_read_b128 v[224:227], v167 offset:22528
	ds_read_b128 v[228:231], v167 offset:23552
	s_mov_b32 m0, s35
	s_nop 0
	global_load_lds_dwordx4 v162, s[52:53]
	s_mov_b32 m0, s37
	s_nop 0
	global_load_lds_dwordx4 v163, s[52:53]
	s_add_u32 s0, s52, 0x20000
	s_addc_u32 s1, s53, 0
	s_mov_b32 m0, s47
	s_nop 0
	global_load_lds_dwordx4 v162, s[0:1]
	s_mov_b32 m0, s75
	s_nop 0
	global_load_lds_dwordx4 v163, s[0:1]
	s_mov_b32 m0, s34
	s_nop 0
	global_load_lds_dwordx4 v200, s[58:59]
	s_mov_b32 m0, s77
	s_nop 0
	global_load_lds_dwordx4 v201, s[58:59]
	s_waitcnt vmcnt(8)
	s_waitcnt lgkmcnt(0)
	s_barrier
	s_setprio 1
	v_mfma_f32_16x16x128_f8f6f4 v[50:53], v[154:161], v[176:183], v[50:53]
	v_mfma_f32_16x16x128_f8f6f4 v[54:57], v[146:153], v[176:183], v[54:57]
	v_mfma_f32_16x16x128_f8f6f4 v[58:61], v[154:161], v[184:191], v[58:61]
	v_mfma_f32_16x16x128_f8f6f4 v[62:65], v[146:153], v[184:191], v[62:65]
	v_mfma_f32_16x16x128_f8f6f4 v[206:209], v[154:161], v[192:199], v[18:21]
	v_mfma_f32_16x16x128_f8f6f4 v[218:221], v[146:153], v[192:199], v[22:25]
	v_mfma_f32_16x16x128_f8f6f4 v[232:235], v[154:161], v[224:231], v[26:29]
	v_mfma_f32_16x16x128_f8f6f4 v[236:239], v[146:153], v[224:231], v[30:33]
	v_mfma_f32_16x16x128_f8f6f4 v[240:243], v[138:145], v[176:183], v[34:37]
	v_mfma_f32_16x16x128_f8f6f4 v[244:247], v[130:137], v[176:183], v[38:41]
	v_mfma_f32_16x16x128_f8f6f4 v[210:213], v[138:145], v[184:191], v[42:45]
	v_mfma_f32_16x16x128_f8f6f4 v[184:187], v[130:137], v[184:191], v[46:49]
	v_mfma_f32_16x16x128_f8f6f4 v[188:191], v[138:145], v[192:199], v[2:5]
	v_mfma_f32_16x16x128_f8f6f4 v[192:195], v[130:137], v[192:199], v[6:9]
	v_mfma_f32_16x16x128_f8f6f4 v[196:199], v[138:145], v[224:231], v[10:13]
	v_mfma_f32_16x16x128_f8f6f4 v[224:227], v[130:137], v[224:231], v[14:17]
	s_setprio 0
	s_barrier
	s_nop 4
	v_add_u32_e32 v14, 0x18000, v166
	v_add_u32_e32 v18, 0x1c000, v166
	ds_read_b128 v[2:5], v14
	ds_read_b128 v[6:9], v14 offset:1024
	ds_read_b128 v[10:13], v14 offset:2048
	ds_read_b128 v[14:17], v14 offset:3072
	ds_read_b128 v[130:133], v18
	ds_read_b128 v[134:137], v18 offset:1024
	ds_read_b128 v[138:141], v18 offset:2048
	ds_read_b128 v[142:145], v18 offset:3072
	ds_read_b128 v[18:21], v167 offset:32768
	ds_read_b128 v[22:25], v167 offset:33792
	ds_read_b128 v[26:29], v167 offset:34816
	ds_read_b128 v[30:33], v167 offset:35840
	ds_read_b128 v[34:37], v167 offset:36864
	ds_read_b128 v[38:41], v167 offset:37888
	ds_read_b128 v[42:45], v167 offset:38912
	ds_read_b128 v[46:49], v167 offset:39936
	s_mov_b32 m0, s78
	s_nop 0
	global_load_lds_dwordx4 v202, s[58:59]
	s_mov_b32 m0, s79
	s_nop 0
	global_load_lds_dwordx4 v223, s[58:59]
	s_waitcnt vmcnt(8)
	s_waitcnt lgkmcnt(0)
	s_barrier
	s_setprio 1
	v_mfma_f32_16x16x128_f8f6f4 v[114:117], v[2:9], v[18:25], v[114:117]
	v_mfma_f32_16x16x128_f8f6f4 v[118:121], v[10:17], v[18:25], v[118:121]
	v_mfma_f32_16x16x128_f8f6f4 v[122:125], v[2:9], v[26:33], v[122:125]
	v_mfma_f32_16x16x128_f8f6f4 v[126:129], v[10:17], v[26:33], v[126:129]
	v_mfma_f32_16x16x128_f8f6f4 v[82:85], v[2:9], v[34:41], v[82:85]
	v_mfma_f32_16x16x128_f8f6f4 v[86:89], v[10:17], v[34:41], v[86:89]
	v_mfma_f32_16x16x128_f8f6f4 v[90:93], v[2:9], v[42:49], v[90:93]
	v_mfma_f32_16x16x128_f8f6f4 v[94:97], v[10:17], v[42:49], v[94:97]
	v_mfma_f32_16x16x128_f8f6f4 v[98:101], v[130:137], v[18:25], v[98:101]
	v_mfma_f32_16x16x128_f8f6f4 v[102:105], v[138:145], v[18:25], v[102:105]
	v_mfma_f32_16x16x128_f8f6f4 v[106:109], v[130:137], v[26:33], v[106:109]
	v_mfma_f32_16x16x128_f8f6f4 v[110:113], v[138:145], v[26:33], v[110:113]
	v_mfma_f32_16x16x128_f8f6f4 v[66:69], v[130:137], v[34:41], v[66:69]
	v_mfma_f32_16x16x128_f8f6f4 v[70:73], v[138:145], v[34:41], v[70:73]
	v_mfma_f32_16x16x128_f8f6f4 v[74:77], v[130:137], v[42:49], v[74:77]
	v_mfma_f32_16x16x128_f8f6f4 v[78:81], v[138:145], v[42:49], v[78:81]
	s_setprio 0
	s_barrier
	ds_read_b128 v[38:41], v167 offset:49152
	ds_read_b128 v[42:45], v167 offset:50176
	ds_read_b128 v[146:149], v167 offset:51200
	ds_read_b128 v[150:153], v167 offset:52224
	ds_read_b128 v[154:157], v167 offset:53248
	ds_read_b128 v[158:161], v167 offset:54272
	ds_read_b128 v[176:179], v167 offset:55296
	ds_read_b128 v[180:183], v167 offset:56320
	s_add_u32 s0, s52, 0x80
	s_addc_u32 s1, s53, 0
	s_mov_b32 m0, s84
	s_nop 0
	global_load_lds_dwordx4 v162, s[0:1]
	s_mov_b32 m0, s85
	s_nop 0
	global_load_lds_dwordx4 v163, s[0:1]
	s_add_u32 s0, s52, 0x20080
	s_addc_u32 s1, s53, 0
	s_mov_b32 m0, s88
	s_nop 0
	global_load_lds_dwordx4 v162, s[0:1]
	s_mov_b32 m0, s89
	s_nop 0
	global_load_lds_dwordx4 v163, s[0:1]
	s_mov_b32 m0, s86
	s_nop 0
	global_load_lds_dwordx4 v200, s[54:55]
	s_mov_b32 m0, s87
	s_nop 0
	global_load_lds_dwordx4 v201, s[54:55]
	s_waitcnt vmcnt(8)
	s_waitcnt lgkmcnt(0)
	s_barrier
	s_setprio 1
	v_mfma_f32_16x16x128_f8f6f4 v[50:53], v[2:9], v[38:45], v[50:53]
	v_mfma_f32_16x16x128_f8f6f4 v[54:57], v[10:17], v[38:45], v[54:57]
	v_mfma_f32_16x16x128_f8f6f4 v[58:61], v[2:9], v[146:153], v[58:61]
	v_mfma_f32_16x16x128_f8f6f4 v[62:65], v[10:17], v[146:153], v[62:65]
	v_mfma_f32_16x16x128_f8f6f4 v[18:21], v[2:9], v[154:161], v[206:209]
	v_mfma_f32_16x16x128_f8f6f4 v[22:25], v[10:17], v[154:161], v[218:221]
	v_mfma_f32_16x16x128_f8f6f4 v[26:29], v[2:9], v[176:183], v[232:235]
	v_mfma_f32_16x16x128_f8f6f4 v[30:33], v[10:17], v[176:183], v[236:239]
	v_mfma_f32_16x16x128_f8f6f4 v[34:37], v[130:137], v[38:45], v[240:243]
	v_mfma_f32_16x16x128_f8f6f4 v[38:41], v[138:145], v[38:45], v[244:247]
	v_mfma_f32_16x16x128_f8f6f4 v[42:45], v[130:137], v[146:153], v[210:213]
	v_mfma_f32_16x16x128_f8f6f4 v[46:49], v[138:145], v[146:153], v[184:187]
	v_mfma_f32_16x16x128_f8f6f4 v[2:5], v[130:137], v[154:161], v[188:191]
	v_mfma_f32_16x16x128_f8f6f4 v[6:9], v[138:145], v[154:161], v[192:195]
	v_mfma_f32_16x16x128_f8f6f4 v[10:13], v[130:137], v[176:183], v[196:199]
	v_mfma_f32_16x16x128_f8f6f4 v[14:17], v[138:145], v[176:183], v[224:227]
	s_setprio 0
	s_barrier
	s_add_i32 s18, s18, 2
	s_add_u32 s16, s16, 0x100
	s_addc_u32 s17, s17, 0
	s_cmp_gt_u32 s18, 5
	s_mov_b64 s[56:57], s[22:23]
	s_cbranch_scc0 .LBB0_1729
	s_and_b64 vcc, exec, s[12:13]
	s_cbranch_vccz .LBB0_1732
	s_barrier

.LBB0_1815:
	v_add_u32_e32 v130, 0x10000, v224
	s_waitcnt vmcnt(0)
	v_add_u32_e32 v134, 0x14000, v224
	s_add_u32 s4, s8, 0x100
	ds_read_b128 v[154:157], v130
	ds_read_b128 v[158:161], v130 offset:1024
	ds_read_b128 v[146:149], v130 offset:2048
	ds_read_b128 v[150:153], v130 offset:3072
	ds_read_b128 v[138:141], v134
	ds_read_b128 v[142:145], v134 offset:1024
	ds_read_b128 v[130:133], v134 offset:2048
	ds_read_b128 v[134:137], v134 offset:3072
	s_addc_u32 s5, s9, 0
	s_cmp_eq_u32 s21, 24
	s_cselect_b32 s56, s54, s4
	s_cselect_b32 s57, s55, s5
	s_cselect_b32 s6, s12, s18
	s_cselect_b32 s7, s13, s19
	s_add_u32 s22, s56, 0x80
	s_addc_u32 s23, s57, 0
	s_add_u32 s0, s8, 0x80
	s_addc_u32 s1, s9, 0
	ds_read_b128 v[162:165], v225
	ds_read_b128 v[166:169], v225 offset:1024
	ds_read_b128 v[170:173], v225 offset:2048
	ds_read_b128 v[174:177], v225 offset:3072
	ds_read_b128 v[178:181], v225 offset:4096
	ds_read_b128 v[182:185], v225 offset:5120
	ds_read_b128 v[190:193], v225 offset:6144
	ds_read_b128 v[194:197], v225 offset:7168
	s_mov_b32 m0, s88
	s_nop 0
	global_load_lds_dwordx4 v187, s[0:1]
	s_mov_b32 m0, s89
	s_nop 0
	global_load_lds_dwordx4 v189, s[0:1]
	s_waitcnt vmcnt(8)
	s_waitcnt lgkmcnt(0)
	s_barrier
	s_setprio 1
	v_mfma_f32_16x16x128_f8f6f4 v[114:117], v[154:161], v[162:169], v[114:117]
	v_mfma_f32_16x16x128_f8f6f4 v[118:121], v[146:153], v[162:169], v[118:121]
	v_mfma_f32_16x16x128_f8f6f4 v[122:125], v[154:161], v[170:177], v[122:125]
	v_mfma_f32_16x16x128_f8f6f4 v[126:129], v[146:153], v[170:177], v[126:129]
	v_mfma_f32_16x16x128_f8f6f4 v[82:85], v[154:161], v[178:185], v[82:85]
	v_mfma_f32_16x16x128_f8f6f4 v[86:89], v[146:153], v[178:185], v[86:89]
	v_mfma_f32_16x16x128_f8f6f4 v[90:93], v[154:161], v[190:197], v[90:93]
	v_mfma_f32_16x16x128_f8f6f4 v[94:97], v[146:153], v[190:197], v[94:97]
	v_mfma_f32_16x16x128_f8f6f4 v[98:101], v[138:145], v[162:169], v[98:101]
	v_mfma_f32_16x16x128_f8f6f4 v[102:105], v[130:137], v[162:169], v[102:105]
	v_mfma_f32_16x16x128_f8f6f4 v[106:109], v[138:145], v[170:177], v[106:109]
	v_mfma_f32_16x16x128_f8f6f4 v[110:113], v[130:137], v[170:177], v[110:113]
	v_mfma_f32_16x16x128_f8f6f4 v[66:69], v[138:145], v[178:185], v[66:69]
	v_mfma_f32_16x16x128_f8f6f4 v[70:73], v[130:137], v[178:185], v[70:73]
	v_mfma_f32_16x16x128_f8f6f4 v[74:77], v[138:145], v[190:197], v[74:77]
	v_mfma_f32_16x16x128_f8f6f4 v[78:81], v[130:137], v[190:197], v[78:81]
	s_setprio 0
	s_barrier
	ds_read_b128 v[162:165], v225 offset:16384
	ds_read_b128 v[166:169], v225 offset:17408
	ds_read_b128 v[170:173], v225 offset:18432
	ds_read_b128 v[174:177], v225 offset:19456
	ds_read_b128 v[178:181], v225 offset:20480
	ds_read_b128 v[182:185], v225 offset:21504
	ds_read_b128 v[190:193], v225 offset:22528
	ds_read_b128 v[194:197], v225 offset:23552
	s_mov_b32 m0, s72
	s_nop 0
	global_load_lds_dwordx4 v1, s[6:7]
	s_mov_b32 m0, s73
	s_nop 0
	global_load_lds_dwordx4 v202, s[6:7]
	s_add_u32 s0, s6, 0x70000
	s_addc_u32 s1, s7, 0
	s_mov_b32 m0, s74
	s_nop 0
	global_load_lds_dwordx4 v1, s[0:1]
	s_mov_b32 m0, s75
	s_nop 0
	global_load_lds_dwordx4 v202, s[0:1]
	s_mov_b32 m0, s71
	s_nop 0
	global_load_lds_dwordx4 v186, s[56:57]
	s_mov_b32 m0, s77
	s_nop 0
	global_load_lds_dwordx4 v188, s[56:57]
	s_waitcnt vmcnt(8)
	s_waitcnt lgkmcnt(0)
	s_barrier
	s_setprio 1
	v_mfma_f32_16x16x128_f8f6f4 v[50:53], v[154:161], v[162:169], v[50:53]
	v_mfma_f32_16x16x128_f8f6f4 v[54:57], v[146:153], v[162:169], v[54:57]
	v_mfma_f32_16x16x128_f8f6f4 v[58:61], v[154:161], v[170:177], v[58:61]
	v_mfma_f32_16x16x128_f8f6f4 v[62:65], v[146:153], v[170:177], v[62:65]
	v_mfma_f32_16x16x128_f8f6f4 v[198:201], v[154:161], v[178:185], v[18:21]
	v_mfma_f32_16x16x128_f8f6f4 v[210:213], v[146:153], v[178:185], v[22:25]
	v_mfma_f32_16x16x128_f8f6f4 v[218:221], v[154:161], v[190:197], v[26:29]
	v_mfma_f32_16x16x128_f8f6f4 v[226:229], v[146:153], v[190:197], v[30:33]
	v_mfma_f32_16x16x128_f8f6f4 v[230:233], v[138:145], v[162:169], v[34:37]
	v_mfma_f32_16x16x128_f8f6f4 v[234:237], v[130:137], v[162:169], v[38:41]
	v_mfma_f32_16x16x128_f8f6f4 v[238:241], v[138:145], v[170:177], v[42:45]
	v_mfma_f32_16x16x128_f8f6f4 v[170:173], v[130:137], v[170:177], v[46:49]
	v_mfma_f32_16x16x128_f8f6f4 v[174:177], v[138:145], v[178:185], v[2:5]
	v_mfma_f32_16x16x128_f8f6f4 v[178:181], v[130:137], v[178:185], v[6:9]
	v_mfma_f32_16x16x128_f8f6f4 v[182:185], v[138:145], v[190:197], v[10:13]
	v_mfma_f32_16x16x128_f8f6f4 v[190:193], v[130:137], v[190:197], v[14:17]
	s_setprio 0
	s_barrier
	s_nop 4
	v_add_u32_e32 v14, 0x18000, v224
	v_add_u32_e32 v18, 0x1c000, v224
	ds_read_b128 v[2:5], v14
	ds_read_b128 v[6:9], v14 offset:1024
	ds_read_b128 v[10:13], v14 offset:2048
	ds_read_b128 v[14:17], v14 offset:3072
	ds_read_b128 v[130:133], v18
	ds_read_b128 v[134:137], v18 offset:1024
	ds_read_b128 v[138:141], v18 offset:2048
	ds_read_b128 v[142:145], v18 offset:3072
	ds_read_b128 v[18:21], v225 offset:32768
	ds_read_b128 v[22:25], v225 offset:33792
	ds_read_b128 v[26:29], v225 offset:34816
	ds_read_b128 v[30:33], v225 offset:35840
	ds_read_b128 v[34:37], v225 offset:36864
	ds_read_b128 v[38:41], v225 offset:37888
	ds_read_b128 v[42:45], v225 offset:38912
	ds_read_b128 v[46:49], v225 offset:39936
	s_mov_b32 m0, s78
	s_nop 0
	global_load_lds_dwordx4 v187, s[56:57]
	s_mov_b32 m0, s79
	s_nop 0
	global_load_lds_dwordx4 v189, s[56:57]
	s_waitcnt vmcnt(8)
	s_waitcnt lgkmcnt(0)
	s_barrier
	s_setprio 1
	v_mfma_f32_16x16x128_f8f6f4 v[114:117], v[2:9], v[18:25], v[114:117]
	v_mfma_f32_16x16x128_f8f6f4 v[118:121], v[10:17], v[18:25], v[118:121]
	v_mfma_f32_16x16x128_f8f6f4 v[122:125], v[2:9], v[26:33], v[122:125]
	v_mfma_f32_16x16x128_f8f6f4 v[126:129], v[10:17], v[26:33], v[126:129]
	v_mfma_f32_16x16x128_f8f6f4 v[82:85], v[2:9], v[34:41], v[82:85]
	v_mfma_f32_16x16x128_f8f6f4 v[86:89], v[10:17], v[34:41], v[86:89]
	v_mfma_f32_16x16x128_f8f6f4 v[90:93], v[2:9], v[42:49], v[90:93]
	v_mfma_f32_16x16x128_f8f6f4 v[94:97], v[10:17], v[42:49], v[94:97]
	v_mfma_f32_16x16x128_f8f6f4 v[98:101], v[130:137], v[18:25], v[98:101]
	v_mfma_f32_16x16x128_f8f6f4 v[102:105], v[138:145], v[18:25], v[102:105]
	v_mfma_f32_16x16x128_f8f6f4 v[106:109], v[130:137], v[26:33], v[106:109]
	v_mfma_f32_16x16x128_f8f6f4 v[110:113], v[138:145], v[26:33], v[110:113]
	v_mfma_f32_16x16x128_f8f6f4 v[66:69], v[130:137], v[34:41], v[66:69]
	v_mfma_f32_16x16x128_f8f6f4 v[70:73], v[138:145], v[34:41], v[70:73]
	v_mfma_f32_16x16x128_f8f6f4 v[74:77], v[130:137], v[42:49], v[74:77]
	v_mfma_f32_16x16x128_f8f6f4 v[78:81], v[138:145], v[42:49], v[78:81]
	s_setprio 0
	s_barrier
	ds_read_b128 v[38:41], v225 offset:49152
	ds_read_b128 v[42:45], v225 offset:50176
	ds_read_b128 v[146:149], v225 offset:51200
	ds_read_b128 v[150:153], v225 offset:52224
	ds_read_b128 v[154:157], v225 offset:53248
	ds_read_b128 v[158:161], v225 offset:54272
	ds_read_b128 v[162:165], v225 offset:55296
	ds_read_b128 v[166:169], v225 offset:56320
	s_add_u32 s0, s6, 0x80
	s_addc_u32 s1, s7, 0
	s_mov_b32 m0, s82
	s_nop 0
	global_load_lds_dwordx4 v1, s[0:1]
	s_mov_b32 m0, s83
	s_nop 0
	global_load_lds_dwordx4 v202, s[0:1]
	s_add_u32 s0, s6, 0x70080
	s_addc_u32 s1, s7, 0
	s_mov_b32 m0, s86
	s_nop 0
	global_load_lds_dwordx4 v1, s[0:1]
	s_mov_b32 m0, s87
	s_nop 0
	global_load_lds_dwordx4 v202, s[0:1]
	s_mov_b32 m0, s84
	s_nop 0
	global_load_lds_dwordx4 v186, s[22:23]
	s_mov_b32 m0, s85
	s_nop 0
	global_load_lds_dwordx4 v188, s[22:23]
	s_waitcnt vmcnt(8)
	s_waitcnt lgkmcnt(0)
	s_barrier
	s_setprio 1
	v_mfma_f32_16x16x128_f8f6f4 v[50:53], v[2:9], v[38:45], v[50:53]
	v_mfma_f32_16x16x128_f8f6f4 v[54:57], v[10:17], v[38:45], v[54:57]
	v_mfma_f32_16x16x128_f8f6f4 v[58:61], v[2:9], v[146:153], v[58:61]
	v_mfma_f32_16x16x128_f8f6f4 v[62:65], v[10:17], v[146:153], v[62:65]
	v_mfma_f32_16x16x128_f8f6f4 v[18:21], v[2:9], v[154:161], v[198:201]
	v_mfma_f32_16x16x128_f8f6f4 v[22:25], v[10:17], v[154:161], v[210:213]
	v_mfma_f32_16x16x128_f8f6f4 v[26:29], v[2:9], v[162:169], v[218:221]
	v_mfma_f32_16x16x128_f8f6f4 v[30:33], v[10:17], v[162:169], v[226:229]
	v_mfma_f32_16x16x128_f8f6f4 v[34:37], v[130:137], v[38:45], v[230:233]
	v_mfma_f32_16x16x128_f8f6f4 v[38:41], v[138:145], v[38:45], v[234:237]
	v_mfma_f32_16x16x128_f8f6f4 v[42:45], v[130:137], v[146:153], v[238:241]
	v_mfma_f32_16x16x128_f8f6f4 v[46:49], v[138:145], v[146:153], v[170:173]
	v_mfma_f32_16x16x128_f8f6f4 v[2:5], v[130:137], v[154:161], v[174:177]
	v_mfma_f32_16x16x128_f8f6f4 v[6:9], v[138:145], v[154:161], v[178:181]
	v_mfma_f32_16x16x128_f8f6f4 v[10:13], v[130:137], v[162:169], v[182:185]
	v_mfma_f32_16x16x128_f8f6f4 v[14:17], v[138:145], v[162:169], v[190:193]
	s_setprio 0
	s_barrier
	s_add_i32 s21, s21, 2
	s_add_u32 s18, s18, 0x100
	s_addc_u32 s19, s19, 0
	s_cmp_gt_u32 s21, 25
	s_mov_b64 s[8:9], s[4:5]
	s_cbranch_scc0 .LBB0_1815
	s_and_b64 vcc, exec, s[52:53]
	s_cbranch_vccz .LBB0_1818
	s_barrier

.LBB0_1939:
	s_add_u32 s22, s12, 0x100
	v_add_u32_e32 v110, 0x10000, v169
	v_add_u32_e32 v158, 0x14000, v169
	s_addc_u32 s23, s13, 0
	ds_read_b128 v[50:53], v110
	ds_read_b128 v[70:73], v110 offset:1024
	ds_read_b128 v[90:93], v110 offset:2048
	ds_read_b128 v[110:113], v110 offset:3072
	ds_read_b128 v[130:133], v158
	ds_read_b128 v[134:137], v158 offset:1024
	ds_read_b128 v[154:157], v158 offset:2048
	ds_read_b128 v[158:161], v158 offset:3072
	s_cmp_eq_u32 s3, 12
	s_cselect_b32 s50, s44, s22
	s_cselect_b32 s51, s45, s23
	s_cselect_b32 s46, s42, s0
	s_cselect_b32 s47, s43, s1
	s_add_u32 s48, s50, 0x80
	s_addc_u32 s49, s51, 0
	s_add_u32 s12, s12, 0x80
	s_addc_u32 s13, s13, 0
	ds_read_b128 v[172:175], v170
	ds_read_b128 v[176:179], v170 offset:1024
	ds_read_b128 v[180:183], v170 offset:2048
	ds_read_b128 v[184:187], v170 offset:3072
	ds_read_b128 v[188:191], v170 offset:4096
	ds_read_b128 v[192:195], v170 offset:5120
	ds_read_b128 v[196:199], v170 offset:6144
	ds_read_b128 v[206:209], v170 offset:7168
	s_mov_b32 m0, s68
	s_nop 0
	global_load_lds_dwordx4 v165, s[12:13]
	s_mov_b32 m0, s69
	s_nop 0
	global_load_lds_dwordx4 v166, s[12:13]
	s_waitcnt vmcnt(8)
	s_waitcnt lgkmcnt(0)
	s_barrier
	s_setprio 1
	v_mfma_f32_16x16x32_bf16 v[150:153], v[50:53], v[172:175], v[150:153]
	v_mfma_f32_16x16x32_bf16 v[142:145], v[90:93], v[172:175], v[142:145]
	v_mfma_f32_16x16x32_bf16 v[126:129], v[50:53], v[180:183], v[126:129]
	v_mfma_f32_16x16x32_bf16 v[118:121], v[90:93], v[180:183], v[118:121]
	v_mfma_f32_16x16x32_bf16 v[106:109], v[50:53], v[188:191], v[106:109]
	v_mfma_f32_16x16x32_bf16 v[98:101], v[90:93], v[188:191], v[98:101]
	v_mfma_f32_16x16x32_bf16 v[86:89], v[50:53], v[196:199], v[86:89]
	v_mfma_f32_16x16x32_bf16 v[78:81], v[90:93], v[196:199], v[78:81]
	v_mfma_f32_16x16x32_bf16 v[150:153], v[70:73], v[176:179], v[150:153]
	v_mfma_f32_16x16x32_bf16 v[142:145], v[110:113], v[176:179], v[142:145]
	v_mfma_f32_16x16x32_bf16 v[126:129], v[70:73], v[184:187], v[126:129]
	v_mfma_f32_16x16x32_bf16 v[118:121], v[110:113], v[184:187], v[118:121]
	v_mfma_f32_16x16x32_bf16 v[106:109], v[70:73], v[192:195], v[106:109]
	v_mfma_f32_16x16x32_bf16 v[98:101], v[110:113], v[192:195], v[98:101]
	v_mfma_f32_16x16x32_bf16 v[86:89], v[70:73], v[206:209], v[86:89]
	v_mfma_f32_16x16x32_bf16 v[78:81], v[110:113], v[206:209], v[78:81]
	v_mfma_f32_16x16x32_bf16 v[146:149], v[130:133], v[172:175], v[146:149]
	v_mfma_f32_16x16x32_bf16 v[138:141], v[154:157], v[172:175], v[138:141]
	v_mfma_f32_16x16x32_bf16 v[122:125], v[130:133], v[180:183], v[122:125]
	v_mfma_f32_16x16x32_bf16 v[114:117], v[154:157], v[180:183], v[114:117]
	v_mfma_f32_16x16x32_bf16 v[102:105], v[130:133], v[188:191], v[102:105]
	v_mfma_f32_16x16x32_bf16 v[94:97], v[154:157], v[188:191], v[94:97]
	v_mfma_f32_16x16x32_bf16 v[82:85], v[130:133], v[196:199], v[82:85]
	v_mfma_f32_16x16x32_bf16 v[74:77], v[154:157], v[196:199], v[74:77]
	v_mfma_f32_16x16x32_bf16 v[146:149], v[134:137], v[176:179], v[146:149]
	v_mfma_f32_16x16x32_bf16 v[138:141], v[158:161], v[176:179], v[138:141]
	v_mfma_f32_16x16x32_bf16 v[122:125], v[134:137], v[184:187], v[122:125]
	v_mfma_f32_16x16x32_bf16 v[114:117], v[158:161], v[184:187], v[114:117]
	v_mfma_f32_16x16x32_bf16 v[102:105], v[134:137], v[192:195], v[102:105]
	v_mfma_f32_16x16x32_bf16 v[94:97], v[158:161], v[192:195], v[94:97]
	v_mfma_f32_16x16x32_bf16 v[82:85], v[134:137], v[206:209], v[82:85]
	v_mfma_f32_16x16x32_bf16 v[74:77], v[158:161], v[206:209], v[74:77]
	s_setprio 0
	s_barrier
	ds_read_b128 v[172:175], v170 offset:16384
	ds_read_b128 v[176:179], v170 offset:17408
	ds_read_b128 v[180:183], v170 offset:18432
	ds_read_b128 v[184:187], v170 offset:19456
	ds_read_b128 v[188:191], v170 offset:20480
	ds_read_b128 v[192:195], v170 offset:21504
	ds_read_b128 v[196:199], v170 offset:22528
	ds_read_b128 v[206:209], v170 offset:23552
	s_mov_b32 m0, s54
	s_nop 0
	global_load_lds_dwordx4 v1, s[46:47]
	s_mov_b32 m0, s55
	s_nop 0
	global_load_lds_dwordx4 v162, s[46:47]
	s_add_u32 s12, s46, 0x40000
	s_addc_u32 s13, s47, 0
	s_mov_b32 m0, s56
	s_nop 0
	global_load_lds_dwordx4 v1, s[12:13]
	s_mov_b32 m0, s57
	s_nop 0
	global_load_lds_dwordx4 v162, s[12:13]
	s_mov_b32 m0, s53
	s_nop 0
	global_load_lds_dwordx4 v163, s[50:51]
	s_mov_b32 m0, s58
	s_nop 0
	global_load_lds_dwordx4 v164, s[50:51]
	s_waitcnt vmcnt(8)
	s_waitcnt lgkmcnt(0)
	s_barrier
	s_setprio 1
	v_mfma_f32_16x16x32_bf16 v[62:65], v[50:53], v[172:175], v[62:65]
	v_mfma_f32_16x16x32_bf16 v[54:57], v[90:93], v[172:175], v[54:57]
	v_mfma_f32_16x16x32_bf16 v[42:45], v[50:53], v[180:183], v[42:45]
	v_mfma_f32_16x16x32_bf16 v[34:37], v[90:93], v[180:183], v[34:37]
	v_mfma_f32_16x16x32_bf16 v[26:29], v[50:53], v[188:191], v[26:29]
	v_mfma_f32_16x16x32_bf16 v[18:21], v[90:93], v[188:191], v[18:21]
	v_mfma_f32_16x16x32_bf16 v[10:13], v[50:53], v[196:199], v[10:13]
	v_mfma_f32_16x16x32_bf16 v[2:5], v[90:93], v[196:199], v[2:5]
	v_mfma_f32_16x16x32_bf16 v[62:65], v[70:73], v[176:179], v[62:65]
	v_mfma_f32_16x16x32_bf16 v[54:57], v[110:113], v[176:179], v[54:57]
	v_mfma_f32_16x16x32_bf16 v[42:45], v[70:73], v[184:187], v[42:45]
	v_mfma_f32_16x16x32_bf16 v[34:37], v[110:113], v[184:187], v[34:37]
	v_mfma_f32_16x16x32_bf16 v[26:29], v[70:73], v[192:195], v[26:29]
	v_mfma_f32_16x16x32_bf16 v[18:21], v[110:113], v[192:195], v[18:21]
	v_mfma_f32_16x16x32_bf16 v[10:13], v[70:73], v[206:209], v[10:13]
	v_mfma_f32_16x16x32_bf16 v[2:5], v[110:113], v[206:209], v[2:5]
	v_mfma_f32_16x16x32_bf16 v[58:61], v[154:157], v[172:175], v[58:61]
	v_mfma_f32_16x16x32_bf16 v[46:49], v[130:133], v[180:183], v[46:49]
	v_mfma_f32_16x16x32_bf16 v[38:41], v[154:157], v[180:183], v[38:41]
	v_mfma_f32_16x16x32_bf16 v[30:33], v[130:133], v[188:191], v[30:33]
	v_mfma_f32_16x16x32_bf16 v[22:25], v[154:157], v[188:191], v[22:25]
	v_mfma_f32_16x16x32_bf16 v[14:17], v[130:133], v[196:199], v[14:17]
	v_mfma_f32_16x16x32_bf16 v[6:9], v[154:157], v[196:199], v[6:9]
	v_mfma_f32_16x16x32_bf16 v[50:53], v[130:133], v[172:175], v[66:69]
	v_mfma_f32_16x16x32_bf16 v[58:61], v[158:161], v[176:179], v[58:61]
	v_mfma_f32_16x16x32_bf16 v[46:49], v[134:137], v[184:187], v[46:49]
	v_mfma_f32_16x16x32_bf16 v[38:41], v[158:161], v[184:187], v[38:41]
	v_mfma_f32_16x16x32_bf16 v[30:33], v[134:137], v[192:195], v[30:33]
	v_mfma_f32_16x16x32_bf16 v[22:25], v[158:161], v[192:195], v[22:25]
	v_mfma_f32_16x16x32_bf16 v[14:17], v[134:137], v[206:209], v[14:17]
	v_mfma_f32_16x16x32_bf16 v[6:9], v[158:161], v[206:209], v[6:9]
	v_mfma_f32_16x16x32_bf16 v[50:53], v[134:137], v[176:179], v[50:53]
	s_setprio 0
	s_barrier
	v_add_u32_e32 v110, 0x18000, v169
	v_add_u32_e32 v158, 0x1c000, v169
	ds_read_b128 v[66:69], v110
	ds_read_b128 v[70:73], v110 offset:1024
	ds_read_b128 v[90:93], v110 offset:2048
	ds_read_b128 v[110:113], v110 offset:3072
	ds_read_b128 v[130:133], v158
	ds_read_b128 v[134:137], v158 offset:1024
	ds_read_b128 v[154:157], v158 offset:2048
	ds_read_b128 v[158:161], v158 offset:3072
	ds_read_b128 v[172:175], v170 offset:32768
	ds_read_b128 v[176:179], v170 offset:33792
	ds_read_b128 v[180:183], v170 offset:34816
	ds_read_b128 v[184:187], v170 offset:35840
	ds_read_b128 v[188:191], v170 offset:36864
	ds_read_b128 v[192:195], v170 offset:37888
	ds_read_b128 v[196:199], v170 offset:38912
	ds_read_b128 v[206:209], v170 offset:39936
	s_mov_b32 m0, s59
	s_nop 0
	global_load_lds_dwordx4 v165, s[50:51]
	s_mov_b32 m0, s60
	s_nop 0
	global_load_lds_dwordx4 v166, s[50:51]
	s_waitcnt vmcnt(8)
	s_waitcnt lgkmcnt(0)
	s_barrier
	s_setprio 1
	v_mfma_f32_16x16x32_bf16 v[150:153], v[66:69], v[172:175], v[150:153]
	v_mfma_f32_16x16x32_bf16 v[142:145], v[90:93], v[172:175], v[142:145]
	v_mfma_f32_16x16x32_bf16 v[126:129], v[66:69], v[180:183], v[126:129]
	v_mfma_f32_16x16x32_bf16 v[118:121], v[90:93], v[180:183], v[118:121]
	v_mfma_f32_16x16x32_bf16 v[106:109], v[66:69], v[188:191], v[106:109]
	v_mfma_f32_16x16x32_bf16 v[98:101], v[90:93], v[188:191], v[98:101]
	v_mfma_f32_16x16x32_bf16 v[86:89], v[66:69], v[196:199], v[86:89]
	v_mfma_f32_16x16x32_bf16 v[78:81], v[90:93], v[196:199], v[78:81]
	v_mfma_f32_16x16x32_bf16 v[150:153], v[70:73], v[176:179], v[150:153]
	v_mfma_f32_16x16x32_bf16 v[142:145], v[110:113], v[176:179], v[142:145]
	v_mfma_f32_16x16x32_bf16 v[126:129], v[70:73], v[184:187], v[126:129]
	v_mfma_f32_16x16x32_bf16 v[118:121], v[110:113], v[184:187], v[118:121]
	v_mfma_f32_16x16x32_bf16 v[106:109], v[70:73], v[192:195], v[106:109]
	v_mfma_f32_16x16x32_bf16 v[98:101], v[110:113], v[192:195], v[98:101]
	v_mfma_f32_16x16x32_bf16 v[86:89], v[70:73], v[206:209], v[86:89]
	v_mfma_f32_16x16x32_bf16 v[78:81], v[110:113], v[206:209], v[78:81]
	v_mfma_f32_16x16x32_bf16 v[146:149], v[130:133], v[172:175], v[146:149]
	v_mfma_f32_16x16x32_bf16 v[138:141], v[154:157], v[172:175], v[138:141]
	v_mfma_f32_16x16x32_bf16 v[122:125], v[130:133], v[180:183], v[122:125]
	v_mfma_f32_16x16x32_bf16 v[114:117], v[154:157], v[180:183], v[114:117]
	v_mfma_f32_16x16x32_bf16 v[102:105], v[130:133], v[188:191], v[102:105]
	v_mfma_f32_16x16x32_bf16 v[94:97], v[154:157], v[188:191], v[94:97]
	v_mfma_f32_16x16x32_bf16 v[82:85], v[130:133], v[196:199], v[82:85]
	v_mfma_f32_16x16x32_bf16 v[74:77], v[154:157], v[196:199], v[74:77]
	v_mfma_f32_16x16x32_bf16 v[146:149], v[134:137], v[176:179], v[146:149]
	v_mfma_f32_16x16x32_bf16 v[138:141], v[158:161], v[176:179], v[138:141]
	v_mfma_f32_16x16x32_bf16 v[122:125], v[134:137], v[184:187], v[122:125]
	v_mfma_f32_16x16x32_bf16 v[114:117], v[158:161], v[184:187], v[114:117]
	v_mfma_f32_16x16x32_bf16 v[102:105], v[134:137], v[192:195], v[102:105]
	v_mfma_f32_16x16x32_bf16 v[94:97], v[158:161], v[192:195], v[94:97]
	v_mfma_f32_16x16x32_bf16 v[82:85], v[134:137], v[206:209], v[82:85]
	v_mfma_f32_16x16x32_bf16 v[74:77], v[158:161], v[206:209], v[74:77]
	s_setprio 0
	s_barrier
	ds_read_b128 v[172:175], v170 offset:49152
	ds_read_b128 v[176:179], v170 offset:50176
	ds_read_b128 v[180:183], v170 offset:51200
	ds_read_b128 v[184:187], v170 offset:52224
	ds_read_b128 v[188:191], v170 offset:53248
	ds_read_b128 v[192:195], v170 offset:54272
	ds_read_b128 v[196:199], v170 offset:55296
	ds_read_b128 v[206:209], v170 offset:56320
	s_add_u32 s12, s46, 0x80
	s_addc_u32 s13, s47, 0
	s_mov_b32 m0, s62
	s_nop 0
	global_load_lds_dwordx4 v1, s[12:13]
	s_mov_b32 m0, s63
	s_nop 0
	global_load_lds_dwordx4 v162, s[12:13]
	s_add_u32 s12, s46, 0x40080
	s_addc_u32 s13, s47, 0
	s_mov_b32 m0, s66
	s_nop 0
	global_load_lds_dwordx4 v1, s[12:13]
	s_mov_b32 m0, s67
	s_nop 0
	global_load_lds_dwordx4 v162, s[12:13]
	s_mov_b32 m0, s64
	s_nop 0
	global_load_lds_dwordx4 v163, s[48:49]
	s_mov_b32 m0, s65
	s_nop 0
	global_load_lds_dwordx4 v164, s[48:49]
	s_waitcnt vmcnt(8)
	s_waitcnt lgkmcnt(0)
	s_barrier
	s_setprio 1
	v_mfma_f32_16x16x32_bf16 v[62:65], v[66:69], v[172:175], v[62:65]
	v_mfma_f32_16x16x32_bf16 v[54:57], v[90:93], v[172:175], v[54:57]
	v_mfma_f32_16x16x32_bf16 v[42:45], v[66:69], v[180:183], v[42:45]
	v_mfma_f32_16x16x32_bf16 v[34:37], v[90:93], v[180:183], v[34:37]
	v_mfma_f32_16x16x32_bf16 v[26:29], v[66:69], v[188:191], v[26:29]
	v_mfma_f32_16x16x32_bf16 v[18:21], v[90:93], v[188:191], v[18:21]
	v_mfma_f32_16x16x32_bf16 v[10:13], v[66:69], v[196:199], v[10:13]
	v_mfma_f32_16x16x32_bf16 v[2:5], v[90:93], v[196:199], v[2:5]
	v_mfma_f32_16x16x32_bf16 v[62:65], v[70:73], v[176:179], v[62:65]
	v_mfma_f32_16x16x32_bf16 v[54:57], v[110:113], v[176:179], v[54:57]
	v_mfma_f32_16x16x32_bf16 v[42:45], v[70:73], v[184:187], v[42:45]
	v_mfma_f32_16x16x32_bf16 v[34:37], v[110:113], v[184:187], v[34:37]
	v_mfma_f32_16x16x32_bf16 v[26:29], v[70:73], v[192:195], v[26:29]
	v_mfma_f32_16x16x32_bf16 v[18:21], v[110:113], v[192:195], v[18:21]
	v_mfma_f32_16x16x32_bf16 v[10:13], v[70:73], v[206:209], v[10:13]
	v_mfma_f32_16x16x32_bf16 v[2:5], v[110:113], v[206:209], v[2:5]
	v_mfma_f32_16x16x32_bf16 v[50:53], v[130:133], v[172:175], v[50:53]
	v_mfma_f32_16x16x32_bf16 v[66:69], v[134:137], v[176:179], v[50:53]
	v_mfma_f32_16x16x32_bf16 v[50:53], v[154:157], v[172:175], v[58:61]
	v_mfma_f32_16x16x32_bf16 v[46:49], v[130:133], v[180:183], v[46:49]
	v_mfma_f32_16x16x32_bf16 v[38:41], v[154:157], v[180:183], v[38:41]
	v_mfma_f32_16x16x32_bf16 v[30:33], v[130:133], v[188:191], v[30:33]
	v_mfma_f32_16x16x32_bf16 v[22:25], v[154:157], v[188:191], v[22:25]
	v_mfma_f32_16x16x32_bf16 v[14:17], v[130:133], v[196:199], v[14:17]
	v_mfma_f32_16x16x32_bf16 v[6:9], v[154:157], v[196:199], v[6:9]
	v_mfma_f32_16x16x32_bf16 v[58:61], v[158:161], v[176:179], v[50:53]
	v_mfma_f32_16x16x32_bf16 v[46:49], v[134:137], v[184:187], v[46:49]
	v_mfma_f32_16x16x32_bf16 v[38:41], v[158:161], v[184:187], v[38:41]
	v_mfma_f32_16x16x32_bf16 v[30:33], v[134:137], v[192:195], v[30:33]
	v_mfma_f32_16x16x32_bf16 v[22:25], v[158:161], v[192:195], v[22:25]
	v_mfma_f32_16x16x32_bf16 v[14:17], v[134:137], v[206:209], v[14:17]
	v_mfma_f32_16x16x32_bf16 v[6:9], v[158:161], v[206:209], v[6:9]
	s_setprio 0
	s_barrier
	s_add_i32 s3, s3, 2
	s_add_u32 s0, s0, 0x100
	s_addc_u32 s1, s1, 0
	s_cmp_gt_u32 s3, 13
	s_mov_b64 s[12:13], s[22:23]
	s_cbranch_scc0 .LBB0_1939
	s_and_b64 vcc, exec, s[8:9]
	s_cbranch_vccz .LBB0_1942
	s_barrier

.LBB0_1959:
	v_add_u32_e32 v130, 0x10000, v169
	v_add_u32_e32 v134, 0x14000, v169
	s_add_u32 s42, s22, 0x100
	ds_read_b128 v[154:157], v130
	ds_read_b128 v[158:161], v130 offset:1024
	ds_read_b128 v[146:149], v130 offset:2048
	ds_read_b128 v[150:153], v130 offset:3072
	ds_read_b128 v[138:141], v134
	ds_read_b128 v[142:145], v134 offset:1024
	ds_read_b128 v[130:133], v134 offset:2048
	ds_read_b128 v[134:137], v134 offset:3072
	s_addc_u32 s43, s23, 0
	s_cmp_eq_u32 s17, 4
	s_cselect_b32 s48, s40, s42
	s_cselect_b32 s49, s41, s43
	s_cselect_b32 s44, s38, s5
	s_cselect_b32 s45, s39, s13
	s_add_u32 s46, s48, 0x80
	s_addc_u32 s47, s49, 0
	s_add_u32 s0, s22, 0x80
	s_addc_u32 s1, s23, 0
	ds_read_b128 v[172:175], v170
	ds_read_b128 v[176:179], v170 offset:1024
	ds_read_b128 v[180:183], v170 offset:2048
	ds_read_b128 v[184:187], v170 offset:3072
	ds_read_b128 v[188:191], v170 offset:4096
	ds_read_b128 v[192:195], v170 offset:5120
	ds_read_b128 v[224:227], v170 offset:6144
	ds_read_b128 v[228:231], v170 offset:7168
	s_mov_b32 m0, s62
	s_nop 0
	global_load_lds_dwordx4 v165, s[0:1]
	s_mov_b32 m0, s63
	s_nop 0
	global_load_lds_dwordx4 v166, s[0:1]
	s_waitcnt vmcnt(8)
	s_waitcnt lgkmcnt(0)
	s_barrier
	s_setprio 1
	v_mfma_f32_16x16x128_f8f6f4 v[114:117], v[154:161], v[172:179], v[114:117]
	v_mfma_f32_16x16x128_f8f6f4 v[118:121], v[146:153], v[172:179], v[118:121]
	v_mfma_f32_16x16x128_f8f6f4 v[122:125], v[154:161], v[180:187], v[122:125]
	v_mfma_f32_16x16x128_f8f6f4 v[126:129], v[146:153], v[180:187], v[126:129]
	v_mfma_f32_16x16x128_f8f6f4 v[82:85], v[154:161], v[188:195], v[82:85]
	v_mfma_f32_16x16x128_f8f6f4 v[86:89], v[146:153], v[188:195], v[86:89]
	v_mfma_f32_16x16x128_f8f6f4 v[90:93], v[154:161], v[224:231], v[90:93]
	v_mfma_f32_16x16x128_f8f6f4 v[94:97], v[146:153], v[224:231], v[94:97]
	v_mfma_f32_16x16x128_f8f6f4 v[98:101], v[138:145], v[172:179], v[98:101]
	v_mfma_f32_16x16x128_f8f6f4 v[102:105], v[130:137], v[172:179], v[102:105]
	v_mfma_f32_16x16x128_f8f6f4 v[106:109], v[138:145], v[180:187], v[106:109]
	v_mfma_f32_16x16x128_f8f6f4 v[110:113], v[130:137], v[180:187], v[110:113]
	v_mfma_f32_16x16x128_f8f6f4 v[66:69], v[138:145], v[188:195], v[66:69]
	v_mfma_f32_16x16x128_f8f6f4 v[70:73], v[130:137], v[188:195], v[70:73]
	v_mfma_f32_16x16x128_f8f6f4 v[74:77], v[138:145], v[224:231], v[74:77]
	v_mfma_f32_16x16x128_f8f6f4 v[78:81], v[130:137], v[224:231], v[78:81]
	s_setprio 0
	s_barrier
	ds_read_b128 v[172:175], v170 offset:16384
	ds_read_b128 v[176:179], v170 offset:17408
	ds_read_b128 v[180:183], v170 offset:18432
	ds_read_b128 v[184:187], v170 offset:19456
	ds_read_b128 v[188:191], v170 offset:20480
	ds_read_b128 v[192:195], v170 offset:21504
	ds_read_b128 v[224:227], v170 offset:22528
	ds_read_b128 v[228:231], v170 offset:23552
	s_mov_b32 m0, s34
	s_nop 0
	global_load_lds_dwordx4 v1, s[44:45]
	s_mov_b32 m0, s35
	s_nop 0
	global_load_lds_dwordx4 v162, s[44:45]
	s_add_u32 s0, s44, 0x20000
	s_addc_u32 s1, s45, 0
	s_mov_b32 m0, s37
	s_nop 0
	global_load_lds_dwordx4 v1, s[0:1]
	s_mov_b32 m0, s50
	s_nop 0
	global_load_lds_dwordx4 v162, s[0:1]
	s_mov_b32 m0, s24
	s_nop 0
	global_load_lds_dwordx4 v163, s[48:49]
	s_mov_b32 m0, s51
	s_nop 0
	global_load_lds_dwordx4 v164, s[48:49]
	s_waitcnt vmcnt(8)
	s_waitcnt lgkmcnt(0)
	s_barrier
	s_setprio 1
	v_mfma_f32_16x16x128_f8f6f4 v[50:53], v[154:161], v[172:179], v[50:53]
	v_mfma_f32_16x16x128_f8f6f4 v[54:57], v[146:153], v[172:179], v[54:57]
	v_mfma_f32_16x16x128_f8f6f4 v[58:61], v[154:161], v[180:187], v[58:61]
	v_mfma_f32_16x16x128_f8f6f4 v[62:65], v[146:153], v[180:187], v[62:65]
	v_mfma_f32_16x16x128_f8f6f4 v[196:199], v[154:161], v[188:195], v[18:21]
	v_mfma_f32_16x16x128_f8f6f4 v[206:209], v[146:153], v[188:195], v[22:25]
	v_mfma_f32_16x16x128_f8f6f4 v[218:221], v[154:161], v[224:231], v[26:29]
	v_mfma_f32_16x16x128_f8f6f4 v[232:235], v[146:153], v[224:231], v[30:33]
	v_mfma_f32_16x16x128_f8f6f4 v[236:239], v[138:145], v[172:179], v[34:37]
	v_mfma_f32_16x16x128_f8f6f4 v[240:243], v[130:137], v[172:179], v[38:41]
	v_mfma_f32_16x16x128_f8f6f4 v[244:247], v[138:145], v[180:187], v[42:45]
	v_mfma_f32_16x16x128_f8f6f4 v[180:183], v[130:137], v[180:187], v[46:49]
	v_mfma_f32_16x16x128_f8f6f4 v[184:187], v[138:145], v[188:195], v[2:5]
	v_mfma_f32_16x16x128_f8f6f4 v[188:191], v[130:137], v[188:195], v[6:9]
	v_mfma_f32_16x16x128_f8f6f4 v[192:195], v[138:145], v[224:231], v[10:13]
	v_mfma_f32_16x16x128_f8f6f4 v[224:227], v[130:137], v[224:231], v[14:17]
	s_setprio 0
	s_barrier
	s_nop 4
	v_add_u32_e32 v14, 0x18000, v169
	v_add_u32_e32 v18, 0x1c000, v169
	ds_read_b128 v[2:5], v14
	ds_read_b128 v[6:9], v14 offset:1024
	ds_read_b128 v[10:13], v14 offset:2048
	ds_read_b128 v[14:17], v14 offset:3072
	ds_read_b128 v[130:133], v18
	ds_read_b128 v[134:137], v18 offset:1024
	ds_read_b128 v[138:141], v18 offset:2048
	ds_read_b128 v[142:145], v18 offset:3072
	ds_read_b128 v[18:21], v170 offset:32768
	ds_read_b128 v[22:25], v170 offset:33792
	ds_read_b128 v[26:29], v170 offset:34816
	ds_read_b128 v[30:33], v170 offset:35840
	ds_read_b128 v[34:37], v170 offset:36864
	ds_read_b128 v[38:41], v170 offset:37888
	ds_read_b128 v[42:45], v170 offset:38912
	ds_read_b128 v[46:49], v170 offset:39936
	s_mov_b32 m0, s52
	s_nop 0
	global_load_lds_dwordx4 v165, s[48:49]
	s_mov_b32 m0, s53
	s_nop 0
	global_load_lds_dwordx4 v166, s[48:49]
	s_waitcnt vmcnt(8)
	s_waitcnt lgkmcnt(0)
	s_barrier
	s_setprio 1
	v_mfma_f32_16x16x128_f8f6f4 v[114:117], v[2:9], v[18:25], v[114:117]
	v_mfma_f32_16x16x128_f8f6f4 v[118:121], v[10:17], v[18:25], v[118:121]
	v_mfma_f32_16x16x128_f8f6f4 v[122:125], v[2:9], v[26:33], v[122:125]
	v_mfma_f32_16x16x128_f8f6f4 v[126:129], v[10:17], v[26:33], v[126:129]
	v_mfma_f32_16x16x128_f8f6f4 v[82:85], v[2:9], v[34:41], v[82:85]
	v_mfma_f32_16x16x128_f8f6f4 v[86:89], v[10:17], v[34:41], v[86:89]
	v_mfma_f32_16x16x128_f8f6f4 v[90:93], v[2:9], v[42:49], v[90:93]
	v_mfma_f32_16x16x128_f8f6f4 v[94:97], v[10:17], v[42:49], v[94:97]
	v_mfma_f32_16x16x128_f8f6f4 v[98:101], v[130:137], v[18:25], v[98:101]
	v_mfma_f32_16x16x128_f8f6f4 v[102:105], v[138:145], v[18:25], v[102:105]
	v_mfma_f32_16x16x128_f8f6f4 v[106:109], v[130:137], v[26:33], v[106:109]
	v_mfma_f32_16x16x128_f8f6f4 v[110:113], v[138:145], v[26:33], v[110:113]
	v_mfma_f32_16x16x128_f8f6f4 v[66:69], v[130:137], v[34:41], v[66:69]
	v_mfma_f32_16x16x128_f8f6f4 v[70:73], v[138:145], v[34:41], v[70:73]
	v_mfma_f32_16x16x128_f8f6f4 v[74:77], v[130:137], v[42:49], v[74:77]
	v_mfma_f32_16x16x128_f8f6f4 v[78:81], v[138:145], v[42:49], v[78:81]
	s_setprio 0
	s_barrier
	ds_read_b128 v[38:41], v170 offset:49152
	ds_read_b128 v[42:45], v170 offset:50176
	ds_read_b128 v[146:149], v170 offset:51200
	ds_read_b128 v[150:153], v170 offset:52224
	ds_read_b128 v[154:157], v170 offset:53248
	ds_read_b128 v[158:161], v170 offset:54272
	ds_read_b128 v[172:175], v170 offset:55296
	ds_read_b128 v[176:179], v170 offset:56320
	s_add_u32 s0, s44, 0x80
	s_addc_u32 s1, s45, 0
	s_mov_b32 m0, s56
	s_nop 0
	global_load_lds_dwordx4 v1, s[0:1]
	s_mov_b32 m0, s57
	s_nop 0
	global_load_lds_dwordx4 v162, s[0:1]
	s_add_u32 s0, s44, 0x20080
	s_addc_u32 s1, s45, 0
	s_mov_b32 m0, s60
	s_nop 0
	global_load_lds_dwordx4 v1, s[0:1]
	s_mov_b32 m0, s61
	s_nop 0
	global_load_lds_dwordx4 v162, s[0:1]
	s_mov_b32 m0, s58
	s_nop 0
	global_load_lds_dwordx4 v163, s[46:47]
	s_mov_b32 m0, s59
	s_nop 0
	global_load_lds_dwordx4 v164, s[46:47]
	s_waitcnt vmcnt(8)
	s_waitcnt lgkmcnt(0)
	s_barrier
	s_setprio 1
	v_mfma_f32_16x16x128_f8f6f4 v[50:53], v[2:9], v[38:45], v[50:53]
	v_mfma_f32_16x16x128_f8f6f4 v[54:57], v[10:17], v[38:45], v[54:57]
	v_mfma_f32_16x16x128_f8f6f4 v[58:61], v[2:9], v[146:153], v[58:61]
	v_mfma_f32_16x16x128_f8f6f4 v[62:65], v[10:17], v[146:153], v[62:65]
	v_mfma_f32_16x16x128_f8f6f4 v[18:21], v[2:9], v[154:161], v[196:199]
	v_mfma_f32_16x16x128_f8f6f4 v[22:25], v[10:17], v[154:161], v[206:209]
	v_mfma_f32_16x16x128_f8f6f4 v[26:29], v[2:9], v[172:179], v[218:221]
	v_mfma_f32_16x16x128_f8f6f4 v[30:33], v[10:17], v[172:179], v[232:235]
	v_mfma_f32_16x16x128_f8f6f4 v[34:37], v[130:137], v[38:45], v[236:239]
	v_mfma_f32_16x16x128_f8f6f4 v[38:41], v[138:145], v[38:45], v[240:243]
	v_mfma_f32_16x16x128_f8f6f4 v[42:45], v[130:137], v[146:153], v[244:247]
	v_mfma_f32_16x16x128_f8f6f4 v[46:49], v[138:145], v[146:153], v[180:183]
	v_mfma_f32_16x16x128_f8f6f4 v[2:5], v[130:137], v[154:161], v[184:187]
	v_mfma_f32_16x16x128_f8f6f4 v[6:9], v[138:145], v[154:161], v[188:191]
	v_mfma_f32_16x16x128_f8f6f4 v[10:13], v[130:137], v[172:179], v[192:195]
	v_mfma_f32_16x16x128_f8f6f4 v[14:17], v[138:145], v[172:179], v[224:227]
	s_setprio 0
	s_barrier
	s_add_i32 s17, s17, 2
	s_add_u32 s5, s5, 0x100
	s_addc_u32 s13, s13, 0
	s_cmp_gt_u32 s17, 5
	s_mov_b64 s[22:23], s[42:43]
	s_cbranch_scc0 .LBB0_1959
	s_and_b64 vcc, exec, s[10:11]
	s_cbranch_vccz .LBB0_1962
	s_barrier

.LBB0_2035:
	s_add_u32 s26, s22, 0x100
	v_add_u32_e32 v126, 0x10000, v209
	v_add_u32_e32 v158, 0x14000, v209
	s_addc_u32 s27, s23, 0
	ds_read_b128 v[106:109], v126
	ds_read_b128 v[110:113], v126 offset:1024
	ds_read_b128 v[122:125], v126 offset:2048
	ds_read_b128 v[126:129], v126 offset:3072
	ds_read_b128 v[146:149], v158
	ds_read_b128 v[150:153], v158 offset:1024
	ds_read_b128 v[154:157], v158 offset:2048
	ds_read_b128 v[158:161], v158 offset:3072
	s_cmp_eq_u32 s5, 40
	s_cselect_b32 s44, s12, s26
	s_cselect_b32 s45, s13, s27
	s_cselect_b32 s40, s10, s0
	s_cselect_b32 s41, s11, s1
	s_add_u32 s42, s44, 0x80
	s_addc_u32 s43, s45, 0
	s_add_u32 s22, s22, 0x80
	s_addc_u32 s23, s23, 0
	ds_read_b128 v[162:165], v223
	ds_read_b128 v[166:169], v223 offset:1024
	ds_read_b128 v[170:173], v223 offset:2048
	ds_read_b128 v[174:177], v223 offset:3072
	ds_read_b128 v[178:181], v223 offset:4096
	ds_read_b128 v[182:185], v223 offset:5120
	ds_read_b128 v[186:189], v223 offset:6144
	ds_read_b128 v[190:193], v223 offset:7168
	s_mov_b32 m0, s54
	s_nop 0
	global_load_lds_dwordx4 v195, s[22:23]
	s_mov_b32 m0, s55
	s_nop 0
	global_load_lds_dwordx4 v197, s[22:23]
	s_waitcnt vmcnt(8)
	s_waitcnt lgkmcnt(0)
	s_barrier
	s_setprio 1
	v_mfma_f32_16x16x32_bf16 v[142:145], v[106:109], v[162:165], v[142:145]
	v_mfma_f32_16x16x32_bf16 v[138:141], v[122:125], v[162:165], v[138:141]
	v_mfma_f32_16x16x32_bf16 v[118:121], v[106:109], v[170:173], v[118:121]
	v_mfma_f32_16x16x32_bf16 v[114:117], v[122:125], v[170:173], v[114:117]
	v_mfma_f32_16x16x32_bf16 v[94:97], v[106:109], v[178:181], v[94:97]
	v_mfma_f32_16x16x32_bf16 v[90:93], v[122:125], v[178:181], v[90:93]
	v_mfma_f32_16x16x32_bf16 v[78:81], v[106:109], v[186:189], v[78:81]
	v_mfma_f32_16x16x32_bf16 v[74:77], v[122:125], v[186:189], v[74:77]
	v_mfma_f32_16x16x32_bf16 v[142:145], v[110:113], v[166:169], v[142:145]
	v_mfma_f32_16x16x32_bf16 v[138:141], v[126:129], v[166:169], v[138:141]
	v_mfma_f32_16x16x32_bf16 v[118:121], v[110:113], v[174:177], v[118:121]
	v_mfma_f32_16x16x32_bf16 v[114:117], v[126:129], v[174:177], v[114:117]
	v_mfma_f32_16x16x32_bf16 v[94:97], v[110:113], v[182:185], v[94:97]
	v_mfma_f32_16x16x32_bf16 v[90:93], v[126:129], v[182:185], v[90:93]
	v_mfma_f32_16x16x32_bf16 v[78:81], v[110:113], v[190:193], v[78:81]
	v_mfma_f32_16x16x32_bf16 v[74:77], v[126:129], v[190:193], v[74:77]
	v_mfma_f32_16x16x32_bf16 v[134:137], v[146:149], v[162:165], v[134:137]
	v_mfma_f32_16x16x32_bf16 v[130:133], v[154:157], v[162:165], v[130:133]
	v_mfma_f32_16x16x32_bf16 v[102:105], v[146:149], v[170:173], v[102:105]
	v_mfma_f32_16x16x32_bf16 v[98:101], v[154:157], v[170:173], v[98:101]
	v_mfma_f32_16x16x32_bf16 v[86:89], v[146:149], v[178:181], v[86:89]
	v_mfma_f32_16x16x32_bf16 v[82:85], v[154:157], v[178:181], v[82:85]
	v_mfma_f32_16x16x32_bf16 v[70:73], v[146:149], v[186:189], v[70:73]
	v_mfma_f32_16x16x32_bf16 v[66:69], v[154:157], v[186:189], v[66:69]
	v_mfma_f32_16x16x32_bf16 v[134:137], v[150:153], v[166:169], v[134:137]
	v_mfma_f32_16x16x32_bf16 v[130:133], v[158:161], v[166:169], v[130:133]
	v_mfma_f32_16x16x32_bf16 v[102:105], v[150:153], v[174:177], v[102:105]
	v_mfma_f32_16x16x32_bf16 v[98:101], v[158:161], v[174:177], v[98:101]
	v_mfma_f32_16x16x32_bf16 v[86:89], v[150:153], v[182:185], v[86:89]
	v_mfma_f32_16x16x32_bf16 v[82:85], v[158:161], v[182:185], v[82:85]
	v_mfma_f32_16x16x32_bf16 v[70:73], v[150:153], v[190:193], v[70:73]
	v_mfma_f32_16x16x32_bf16 v[66:69], v[158:161], v[190:193], v[66:69]
	s_setprio 0
	s_barrier
	ds_read_b128 v[162:165], v223 offset:16384
	ds_read_b128 v[166:169], v223 offset:17408
	ds_read_b128 v[170:173], v223 offset:18432
	ds_read_b128 v[174:177], v223 offset:19456
	ds_read_b128 v[178:181], v223 offset:20480
	ds_read_b128 v[182:185], v223 offset:21504
	ds_read_b128 v[186:189], v223 offset:22528
	ds_read_b128 v[190:193], v223 offset:23552
	s_mov_b32 m0, s19
	s_nop 0
	global_load_lds_dwordx4 v1, s[40:41]
	s_mov_b32 m0, s21
	s_nop 0
	global_load_lds_dwordx4 v206, s[40:41]
	s_add_u32 s22, s40, 0xb0000
	s_addc_u32 s23, s41, 0
	s_mov_b32 m0, s24
	s_nop 0
	global_load_lds_dwordx4 v1, s[22:23]
	s_mov_b32 m0, s34
	s_nop 0
	global_load_lds_dwordx4 v206, s[22:23]
	s_mov_b32 m0, s18
	s_nop 0
	global_load_lds_dwordx4 v194, s[44:45]
	s_mov_b32 m0, s35
	s_nop 0
	global_load_lds_dwordx4 v196, s[44:45]
	s_waitcnt vmcnt(8)
	s_waitcnt lgkmcnt(0)
	s_barrier
	s_setprio 1
	v_mfma_f32_16x16x32_bf16 v[54:57], v[106:109], v[162:165], v[54:57]
	v_mfma_f32_16x16x32_bf16 v[50:53], v[122:125], v[162:165], v[50:53]
	v_mfma_f32_16x16x32_bf16 v[38:41], v[106:109], v[170:173], v[38:41]
	v_mfma_f32_16x16x32_bf16 v[34:37], v[122:125], v[170:173], v[34:37]
	v_mfma_f32_16x16x32_bf16 v[22:25], v[106:109], v[178:181], v[22:25]
	v_mfma_f32_16x16x32_bf16 v[18:21], v[122:125], v[178:181], v[18:21]
	v_mfma_f32_16x16x32_bf16 v[6:9], v[106:109], v[186:189], v[6:9]
	v_mfma_f32_16x16x32_bf16 v[2:5], v[122:125], v[186:189], v[2:5]
	v_mfma_f32_16x16x32_bf16 v[54:57], v[110:113], v[166:169], v[54:57]
	v_mfma_f32_16x16x32_bf16 v[50:53], v[126:129], v[166:169], v[50:53]
	v_mfma_f32_16x16x32_bf16 v[38:41], v[110:113], v[174:177], v[38:41]
	v_mfma_f32_16x16x32_bf16 v[34:37], v[126:129], v[174:177], v[34:37]
	v_mfma_f32_16x16x32_bf16 v[22:25], v[110:113], v[182:185], v[22:25]
	v_mfma_f32_16x16x32_bf16 v[18:21], v[126:129], v[182:185], v[18:21]
	v_mfma_f32_16x16x32_bf16 v[6:9], v[110:113], v[190:193], v[6:9]
	v_mfma_f32_16x16x32_bf16 v[2:5], v[126:129], v[190:193], v[2:5]
	v_mfma_f32_16x16x32_bf16 v[62:65], v[146:149], v[162:165], v[62:65]
	v_mfma_f32_16x16x32_bf16 v[58:61], v[154:157], v[162:165], v[58:61]
	v_mfma_f32_16x16x32_bf16 v[46:49], v[146:149], v[170:173], v[46:49]
	v_mfma_f32_16x16x32_bf16 v[42:45], v[154:157], v[170:173], v[42:45]
	v_mfma_f32_16x16x32_bf16 v[30:33], v[146:149], v[178:181], v[30:33]
	v_mfma_f32_16x16x32_bf16 v[26:29], v[154:157], v[178:181], v[26:29]
	v_mfma_f32_16x16x32_bf16 v[14:17], v[146:149], v[186:189], v[14:17]
	v_mfma_f32_16x16x32_bf16 v[10:13], v[154:157], v[186:189], v[10:13]
	v_mfma_f32_16x16x32_bf16 v[62:65], v[150:153], v[166:169], v[62:65]
	v_mfma_f32_16x16x32_bf16 v[58:61], v[158:161], v[166:169], v[58:61]
	v_mfma_f32_16x16x32_bf16 v[46:49], v[150:153], v[174:177], v[46:49]
	v_mfma_f32_16x16x32_bf16 v[42:45], v[158:161], v[174:177], v[42:45]
	v_mfma_f32_16x16x32_bf16 v[30:33], v[150:153], v[182:185], v[30:33]
	v_mfma_f32_16x16x32_bf16 v[26:29], v[158:161], v[182:185], v[26:29]
	v_mfma_f32_16x16x32_bf16 v[14:17], v[150:153], v[190:193], v[14:17]
	v_mfma_f32_16x16x32_bf16 v[10:13], v[158:161], v[190:193], v[10:13]
	s_setprio 0
	s_barrier
	v_add_u32_e32 v126, 0x18000, v209
	v_add_u32_e32 v158, 0x1c000, v209
	ds_read_b128 v[106:109], v126
	ds_read_b128 v[110:113], v126 offset:1024
	ds_read_b128 v[122:125], v126 offset:2048
	ds_read_b128 v[126:129], v126 offset:3072
	ds_read_b128 v[146:149], v158
	ds_read_b128 v[150:153], v158 offset:1024
	ds_read_b128 v[154:157], v158 offset:2048
	ds_read_b128 v[158:161], v158 offset:3072
	ds_read_b128 v[162:165], v223 offset:32768
	ds_read_b128 v[166:169], v223 offset:33792
	ds_read_b128 v[170:173], v223 offset:34816
	ds_read_b128 v[174:177], v223 offset:35840
	ds_read_b128 v[178:181], v223 offset:36864
	ds_read_b128 v[182:185], v223 offset:37888
	ds_read_b128 v[186:189], v223 offset:38912
	ds_read_b128 v[190:193], v223 offset:39936
	s_mov_b32 m0, s37
	s_nop 0
	global_load_lds_dwordx4 v195, s[44:45]
	s_mov_b32 m0, s46
	s_nop 0
	global_load_lds_dwordx4 v197, s[44:45]
	s_waitcnt vmcnt(8)
	s_waitcnt lgkmcnt(0)
	s_barrier
	s_setprio 1
	v_mfma_f32_16x16x32_bf16 v[142:145], v[106:109], v[162:165], v[142:145]
	v_mfma_f32_16x16x32_bf16 v[138:141], v[122:125], v[162:165], v[138:141]
	v_mfma_f32_16x16x32_bf16 v[118:121], v[106:109], v[170:173], v[118:121]
	v_mfma_f32_16x16x32_bf16 v[114:117], v[122:125], v[170:173], v[114:117]
	v_mfma_f32_16x16x32_bf16 v[94:97], v[106:109], v[178:181], v[94:97]
	v_mfma_f32_16x16x32_bf16 v[90:93], v[122:125], v[178:181], v[90:93]
	v_mfma_f32_16x16x32_bf16 v[78:81], v[106:109], v[186:189], v[78:81]
	v_mfma_f32_16x16x32_bf16 v[74:77], v[122:125], v[186:189], v[74:77]
	v_mfma_f32_16x16x32_bf16 v[142:145], v[110:113], v[166:169], v[142:145]
	v_mfma_f32_16x16x32_bf16 v[138:141], v[126:129], v[166:169], v[138:141]
	v_mfma_f32_16x16x32_bf16 v[118:121], v[110:113], v[174:177], v[118:121]
	v_mfma_f32_16x16x32_bf16 v[114:117], v[126:129], v[174:177], v[114:117]
	v_mfma_f32_16x16x32_bf16 v[94:97], v[110:113], v[182:185], v[94:97]
	v_mfma_f32_16x16x32_bf16 v[90:93], v[126:129], v[182:185], v[90:93]
	v_mfma_f32_16x16x32_bf16 v[78:81], v[110:113], v[190:193], v[78:81]
	v_mfma_f32_16x16x32_bf16 v[74:77], v[126:129], v[190:193], v[74:77]
	v_mfma_f32_16x16x32_bf16 v[134:137], v[146:149], v[162:165], v[134:137]
	v_mfma_f32_16x16x32_bf16 v[130:133], v[154:157], v[162:165], v[130:133]
	v_mfma_f32_16x16x32_bf16 v[102:105], v[146:149], v[170:173], v[102:105]
	v_mfma_f32_16x16x32_bf16 v[98:101], v[154:157], v[170:173], v[98:101]
	v_mfma_f32_16x16x32_bf16 v[86:89], v[146:149], v[178:181], v[86:89]
	v_mfma_f32_16x16x32_bf16 v[82:85], v[154:157], v[178:181], v[82:85]
	v_mfma_f32_16x16x32_bf16 v[70:73], v[146:149], v[186:189], v[70:73]
	v_mfma_f32_16x16x32_bf16 v[66:69], v[154:157], v[186:189], v[66:69]
	v_mfma_f32_16x16x32_bf16 v[134:137], v[150:153], v[166:169], v[134:137]
	v_mfma_f32_16x16x32_bf16 v[130:133], v[158:161], v[166:169], v[130:133]
	v_mfma_f32_16x16x32_bf16 v[102:105], v[150:153], v[174:177], v[102:105]
	v_mfma_f32_16x16x32_bf16 v[98:101], v[158:161], v[174:177], v[98:101]
	v_mfma_f32_16x16x32_bf16 v[86:89], v[150:153], v[182:185], v[86:89]
	v_mfma_f32_16x16x32_bf16 v[82:85], v[158:161], v[182:185], v[82:85]
	v_mfma_f32_16x16x32_bf16 v[70:73], v[150:153], v[190:193], v[70:73]
	v_mfma_f32_16x16x32_bf16 v[66:69], v[158:161], v[190:193], v[66:69]
	s_setprio 0
	s_barrier
	ds_read_b128 v[162:165], v223 offset:49152
	ds_read_b128 v[166:169], v223 offset:50176
	ds_read_b128 v[170:173], v223 offset:51200
	ds_read_b128 v[174:177], v223 offset:52224
	ds_read_b128 v[178:181], v223 offset:53248
	ds_read_b128 v[182:185], v223 offset:54272
	ds_read_b128 v[186:189], v223 offset:55296
	ds_read_b128 v[190:193], v223 offset:56320
	s_add_u32 s22, s40, 0x80
	s_addc_u32 s23, s41, 0
	s_mov_b32 m0, s48
	s_nop 0
	global_load_lds_dwordx4 v1, s[22:23]
	s_mov_b32 m0, s49
	s_nop 0
	global_load_lds_dwordx4 v206, s[22:23]
	s_add_u32 s22, s40, 0xb0080
	s_addc_u32 s23, s41, 0
	s_mov_b32 m0, s52
	s_nop 0
	global_load_lds_dwordx4 v1, s[22:23]
	s_mov_b32 m0, s53
	s_nop 0
	global_load_lds_dwordx4 v206, s[22:23]
	s_mov_b32 m0, s50
	s_nop 0
	global_load_lds_dwordx4 v194, s[42:43]
	s_mov_b32 m0, s51
	s_nop 0
	global_load_lds_dwordx4 v196, s[42:43]
	s_waitcnt vmcnt(8)
	s_waitcnt lgkmcnt(0)
	s_barrier
	s_setprio 1
	v_mfma_f32_16x16x32_bf16 v[54:57], v[106:109], v[162:165], v[54:57]
	v_mfma_f32_16x16x32_bf16 v[50:53], v[122:125], v[162:165], v[50:53]
	v_mfma_f32_16x16x32_bf16 v[38:41], v[106:109], v[170:173], v[38:41]
	v_mfma_f32_16x16x32_bf16 v[34:37], v[122:125], v[170:173], v[34:37]
	v_mfma_f32_16x16x32_bf16 v[22:25], v[106:109], v[178:181], v[22:25]
	v_mfma_f32_16x16x32_bf16 v[18:21], v[122:125], v[178:181], v[18:21]
	v_mfma_f32_16x16x32_bf16 v[6:9], v[106:109], v[186:189], v[6:9]
	v_mfma_f32_16x16x32_bf16 v[2:5], v[122:125], v[186:189], v[2:5]
	v_mfma_f32_16x16x32_bf16 v[54:57], v[110:113], v[166:169], v[54:57]
	v_mfma_f32_16x16x32_bf16 v[50:53], v[126:129], v[166:169], v[50:53]
	v_mfma_f32_16x16x32_bf16 v[38:41], v[110:113], v[174:177], v[38:41]
	v_mfma_f32_16x16x32_bf16 v[34:37], v[126:129], v[174:177], v[34:37]
	v_mfma_f32_16x16x32_bf16 v[22:25], v[110:113], v[182:185], v[22:25]
	v_mfma_f32_16x16x32_bf16 v[18:21], v[126:129], v[182:185], v[18:21]
	v_mfma_f32_16x16x32_bf16 v[6:9], v[110:113], v[190:193], v[6:9]
	v_mfma_f32_16x16x32_bf16 v[2:5], v[126:129], v[190:193], v[2:5]
	v_mfma_f32_16x16x32_bf16 v[62:65], v[146:149], v[162:165], v[62:65]
	v_mfma_f32_16x16x32_bf16 v[58:61], v[154:157], v[162:165], v[58:61]
	v_mfma_f32_16x16x32_bf16 v[46:49], v[146:149], v[170:173], v[46:49]
	v_mfma_f32_16x16x32_bf16 v[42:45], v[154:157], v[170:173], v[42:45]
	v_mfma_f32_16x16x32_bf16 v[30:33], v[146:149], v[178:181], v[30:33]
	v_mfma_f32_16x16x32_bf16 v[26:29], v[154:157], v[178:181], v[26:29]
	v_mfma_f32_16x16x32_bf16 v[14:17], v[146:149], v[186:189], v[14:17]
	v_mfma_f32_16x16x32_bf16 v[10:13], v[154:157], v[186:189], v[10:13]
	v_mfma_f32_16x16x32_bf16 v[62:65], v[150:153], v[166:169], v[62:65]
	v_mfma_f32_16x16x32_bf16 v[58:61], v[158:161], v[166:169], v[58:61]
	v_mfma_f32_16x16x32_bf16 v[46:49], v[150:153], v[174:177], v[46:49]
	v_mfma_f32_16x16x32_bf16 v[42:45], v[158:161], v[174:177], v[42:45]
	v_mfma_f32_16x16x32_bf16 v[30:33], v[150:153], v[182:185], v[30:33]
	v_mfma_f32_16x16x32_bf16 v[26:29], v[158:161], v[182:185], v[26:29]
	v_mfma_f32_16x16x32_bf16 v[14:17], v[150:153], v[190:193], v[14:17]
	v_mfma_f32_16x16x32_bf16 v[10:13], v[158:161], v[190:193], v[10:13]
	s_setprio 0
	s_barrier
	s_add_i32 s5, s5, 2
	s_add_u32 s0, s0, 0x100
	s_addc_u32 s1, s1, 0
	s_cmp_gt_u32 s5, 41
	s_mov_b64 s[22:23], s[26:27]
	s_cbranch_scc0 .LBB0_2035
	s_and_b64 vcc, exec, s[8:9]
	s_cbranch_vccz .LBB0_2038
	s_barrier

.LBB0_2073:
	v_add_u32_e32 v130, 0x10000, v209
	v_add_u32_e32 v134, 0x14000, v209
	ds_read_b128 v[154:157], v130
	ds_read_b128 v[158:161], v130 offset:1024
	ds_read_b128 v[146:149], v130 offset:2048
	ds_read_b128 v[150:153], v130 offset:3072
	ds_read_b128 v[138:141], v134
	ds_read_b128 v[142:145], v134 offset:1024
	ds_read_b128 v[130:133], v134 offset:2048
	ds_read_b128 v[134:137], v134 offset:3072
	s_cmp_eq_u32 s21, 18
	s_cselect_b32 s40, s12, s18
	s_cselect_b32 s41, s13, s19
	s_cselect_b32 s38, s10, s5
	s_cselect_b32 s39, s11, s17
	s_add_u32 s26, s40, 0x80
	s_addc_u32 s27, s41, 0
	ds_read_b128 v[162:165], v223
	ds_read_b128 v[166:169], v223 offset:1024
	ds_read_b128 v[170:173], v223 offset:2048
	ds_read_b128 v[174:177], v223 offset:3072
	ds_read_b128 v[178:181], v223 offset:4096
	ds_read_b128 v[182:185], v223 offset:5120
	ds_read_b128 v[186:189], v223 offset:6144
	ds_read_b128 v[190:193], v223 offset:7168
	s_mov_b32 m0, s56
	s_nop 0
	global_load_lds_dwordx4 v195, s[22:23]
	s_mov_b32 m0, s57
	s_nop 0
	global_load_lds_dwordx4 v197, s[22:23]
	s_waitcnt vmcnt(8)
	s_waitcnt lgkmcnt(0)
	s_barrier
	s_setprio 1
	v_mfma_f32_16x16x128_f8f6f4 v[114:117], v[154:161], v[162:169], v[114:117]
	v_mfma_f32_16x16x128_f8f6f4 v[118:121], v[146:153], v[162:169], v[118:121]
	v_mfma_f32_16x16x128_f8f6f4 v[122:125], v[154:161], v[170:177], v[122:125]
	v_mfma_f32_16x16x128_f8f6f4 v[126:129], v[146:153], v[170:177], v[126:129]
	v_mfma_f32_16x16x128_f8f6f4 v[82:85], v[154:161], v[178:185], v[82:85]
	v_mfma_f32_16x16x128_f8f6f4 v[86:89], v[146:153], v[178:185], v[86:89]
	v_mfma_f32_16x16x128_f8f6f4 v[90:93], v[154:161], v[186:193], v[90:93]
	v_mfma_f32_16x16x128_f8f6f4 v[94:97], v[146:153], v[186:193], v[94:97]
	v_mfma_f32_16x16x128_f8f6f4 v[98:101], v[138:145], v[162:169], v[98:101]
	v_mfma_f32_16x16x128_f8f6f4 v[102:105], v[130:137], v[162:169], v[102:105]
	v_mfma_f32_16x16x128_f8f6f4 v[106:109], v[138:145], v[170:177], v[106:109]
	v_mfma_f32_16x16x128_f8f6f4 v[110:113], v[130:137], v[170:177], v[110:113]
	v_mfma_f32_16x16x128_f8f6f4 v[66:69], v[138:145], v[178:185], v[66:69]
	v_mfma_f32_16x16x128_f8f6f4 v[70:73], v[130:137], v[178:185], v[70:73]
	v_mfma_f32_16x16x128_f8f6f4 v[74:77], v[138:145], v[186:193], v[74:77]
	v_mfma_f32_16x16x128_f8f6f4 v[78:81], v[130:137], v[186:193], v[78:81]
	s_setprio 0
	s_barrier
	ds_read_b128 v[162:165], v223 offset:16384
	ds_read_b128 v[166:169], v223 offset:17408
	ds_read_b128 v[170:173], v223 offset:18432
	ds_read_b128 v[174:177], v223 offset:19456
	ds_read_b128 v[178:181], v223 offset:20480
	ds_read_b128 v[182:185], v223 offset:21504
	ds_read_b128 v[186:189], v223 offset:22528
	ds_read_b128 v[190:193], v223 offset:23552
	s_mov_b32 m0, s42
	s_nop 0
	global_load_lds_dwordx4 v1, s[38:39]
	s_mov_b32 m0, s43
	s_nop 0
	global_load_lds_dwordx4 v206, s[38:39]
	s_add_u32 s0, s38, 0x58000
	s_addc_u32 s1, s39, 0
	s_mov_b32 m0, s44
	s_nop 0
	global_load_lds_dwordx4 v1, s[0:1]
	s_mov_b32 m0, s45
	s_nop 0
	global_load_lds_dwordx4 v206, s[0:1]
	s_mov_b32 m0, s24
	s_nop 0
	global_load_lds_dwordx4 v194, s[40:41]
	s_mov_b32 m0, s46
	s_nop 0
	global_load_lds_dwordx4 v196, s[40:41]
	s_waitcnt vmcnt(8)
	s_waitcnt lgkmcnt(0)
	s_barrier
	s_setprio 1
	v_mfma_f32_16x16x128_f8f6f4 v[50:53], v[154:161], v[162:169], v[50:53]
	v_mfma_f32_16x16x128_f8f6f4 v[54:57], v[146:153], v[162:169], v[54:57]
	v_mfma_f32_16x16x128_f8f6f4 v[58:61], v[154:161], v[170:177], v[58:61]
	v_mfma_f32_16x16x128_f8f6f4 v[62:65], v[146:153], v[170:177], v[62:65]
	v_mfma_f32_16x16x128_f8f6f4 v[198:201], v[154:161], v[178:185], v[18:21]
	v_mfma_f32_16x16x128_f8f6f4 v[218:221], v[146:153], v[178:185], v[22:25]
	v_mfma_f32_16x16x128_f8f6f4 v[224:227], v[154:161], v[186:193], v[26:29]
	v_mfma_f32_16x16x128_f8f6f4 v[228:231], v[146:153], v[186:193], v[30:33]
	v_mfma_f32_16x16x128_f8f6f4 v[232:235], v[138:145], v[162:169], v[34:37]
	v_mfma_f32_16x16x128_f8f6f4 v[236:239], v[130:137], v[162:169], v[38:41]
	v_mfma_f32_16x16x128_f8f6f4 v[240:243], v[138:145], v[170:177], v[42:45]
	v_mfma_f32_16x16x128_f8f6f4 v[170:173], v[130:137], v[170:177], v[46:49]
	v_mfma_f32_16x16x128_f8f6f4 v[174:177], v[138:145], v[178:185], v[2:5]
	v_mfma_f32_16x16x128_f8f6f4 v[178:181], v[130:137], v[178:185], v[6:9]
	v_mfma_f32_16x16x128_f8f6f4 v[182:185], v[138:145], v[186:193], v[10:13]
	v_mfma_f32_16x16x128_f8f6f4 v[186:189], v[130:137], v[186:193], v[14:17]
	s_setprio 0
	s_barrier
	s_nop 4
	v_add_u32_e32 v14, 0x18000, v209
	v_add_u32_e32 v18, 0x1c000, v209
	ds_read_b128 v[2:5], v14
	ds_read_b128 v[6:9], v14 offset:1024
	ds_read_b128 v[10:13], v14 offset:2048
	ds_read_b128 v[14:17], v14 offset:3072
	ds_read_b128 v[130:133], v18
	ds_read_b128 v[134:137], v18 offset:1024
	ds_read_b128 v[138:141], v18 offset:2048
	ds_read_b128 v[142:145], v18 offset:3072
	ds_read_b128 v[18:21], v223 offset:32768
	ds_read_b128 v[22:25], v223 offset:33792
	ds_read_b128 v[26:29], v223 offset:34816
	ds_read_b128 v[30:33], v223 offset:35840
	ds_read_b128 v[34:37], v223 offset:36864
	ds_read_b128 v[38:41], v223 offset:37888
	ds_read_b128 v[42:45], v223 offset:38912
	ds_read_b128 v[46:49], v223 offset:39936
	s_mov_b32 m0, s47
	s_nop 0
	global_load_lds_dwordx4 v195, s[40:41]
	s_mov_b32 m0, s48
	s_nop 0
	global_load_lds_dwordx4 v197, s[40:41]
	s_waitcnt vmcnt(8)
	s_waitcnt lgkmcnt(0)
	s_barrier
	s_setprio 1
	v_mfma_f32_16x16x128_f8f6f4 v[114:117], v[2:9], v[18:25], v[114:117]
	v_mfma_f32_16x16x128_f8f6f4 v[118:121], v[10:17], v[18:25], v[118:121]
	v_mfma_f32_16x16x128_f8f6f4 v[122:125], v[2:9], v[26:33], v[122:125]
	v_mfma_f32_16x16x128_f8f6f4 v[126:129], v[10:17], v[26:33], v[126:129]
	v_mfma_f32_16x16x128_f8f6f4 v[82:85], v[2:9], v[34:41], v[82:85]
	v_mfma_f32_16x16x128_f8f6f4 v[86:89], v[10:17], v[34:41], v[86:89]
	v_mfma_f32_16x16x128_f8f6f4 v[90:93], v[2:9], v[42:49], v[90:93]
	v_mfma_f32_16x16x128_f8f6f4 v[94:97], v[10:17], v[42:49], v[94:97]
	v_mfma_f32_16x16x128_f8f6f4 v[98:101], v[130:137], v[18:25], v[98:101]
	v_mfma_f32_16x16x128_f8f6f4 v[102:105], v[138:145], v[18:25], v[102:105]
	v_mfma_f32_16x16x128_f8f6f4 v[106:109], v[130:137], v[26:33], v[106:109]
	v_mfma_f32_16x16x128_f8f6f4 v[110:113], v[138:145], v[26:33], v[110:113]
	v_mfma_f32_16x16x128_f8f6f4 v[66:69], v[130:137], v[34:41], v[66:69]
	v_mfma_f32_16x16x128_f8f6f4 v[70:73], v[138:145], v[34:41], v[70:73]
	v_mfma_f32_16x16x128_f8f6f4 v[74:77], v[130:137], v[42:49], v[74:77]
	v_mfma_f32_16x16x128_f8f6f4 v[78:81], v[138:145], v[42:49], v[78:81]
	s_setprio 0
	s_barrier
	ds_read_b128 v[38:41], v223 offset:49152
	ds_read_b128 v[42:45], v223 offset:50176
	ds_read_b128 v[146:149], v223 offset:51200
	ds_read_b128 v[150:153], v223 offset:52224
	ds_read_b128 v[154:157], v223 offset:53248
	ds_read_b128 v[158:161], v223 offset:54272
	ds_read_b128 v[162:165], v223 offset:55296
	ds_read_b128 v[166:169], v223 offset:56320
	s_add_u32 s0, s38, 0x80
	s_addc_u32 s1, s39, 0
	s_mov_b32 m0, s50
	s_nop 0
	global_load_lds_dwordx4 v1, s[0:1]
	s_mov_b32 m0, s51
	s_nop 0
	global_load_lds_dwordx4 v206, s[0:1]
	s_add_u32 s0, s38, 0x58080
	s_addc_u32 s1, s39, 0
	s_mov_b32 m0, s54
	s_nop 0
	global_load_lds_dwordx4 v1, s[0:1]
	s_mov_b32 m0, s55
	s_nop 0
	global_load_lds_dwordx4 v206, s[0:1]
	s_mov_b32 m0, s52
	s_nop 0
	global_load_lds_dwordx4 v194, s[26:27]
	s_mov_b32 m0, s53
	s_nop 0
	global_load_lds_dwordx4 v196, s[26:27]
	s_waitcnt vmcnt(8)
	s_waitcnt lgkmcnt(0)
	s_barrier
	s_setprio 1
	v_mfma_f32_16x16x128_f8f6f4 v[50:53], v[2:9], v[38:45], v[50:53]
	v_mfma_f32_16x16x128_f8f6f4 v[54:57], v[10:17], v[38:45], v[54:57]
	v_mfma_f32_16x16x128_f8f6f4 v[58:61], v[2:9], v[146:153], v[58:61]
	v_mfma_f32_16x16x128_f8f6f4 v[62:65], v[10:17], v[146:153], v[62:65]
	v_mfma_f32_16x16x128_f8f6f4 v[18:21], v[2:9], v[154:161], v[198:201]
	v_mfma_f32_16x16x128_f8f6f4 v[22:25], v[10:17], v[154:161], v[218:221]
	v_mfma_f32_16x16x128_f8f6f4 v[26:29], v[2:9], v[162:169], v[224:227]
	v_mfma_f32_16x16x128_f8f6f4 v[30:33], v[10:17], v[162:169], v[228:231]
	v_mfma_f32_16x16x128_f8f6f4 v[34:37], v[130:137], v[38:45], v[232:235]
	v_mfma_f32_16x16x128_f8f6f4 v[38:41], v[138:145], v[38:45], v[236:239]
	v_mfma_f32_16x16x128_f8f6f4 v[42:45], v[130:137], v[146:153], v[240:243]
	v_mfma_f32_16x16x128_f8f6f4 v[46:49], v[138:145], v[146:153], v[170:173]
	v_mfma_f32_16x16x128_f8f6f4 v[2:5], v[130:137], v[154:161], v[174:177]
	v_mfma_f32_16x16x128_f8f6f4 v[6:9], v[138:145], v[154:161], v[178:181]
	v_mfma_f32_16x16x128_f8f6f4 v[10:13], v[130:137], v[162:169], v[182:185]
	v_mfma_f32_16x16x128_f8f6f4 v[14:17], v[138:145], v[162:169], v[186:189]
	s_setprio 0
	s_barrier
	s_add_i32 s21, s21, 2
	s_add_u32 s5, s5, 0x100
	s_addc_u32 s17, s17, 0
	s_add_u32 s18, s18, 0x100
	s_addc_u32 s19, s19, 0
	s_add_u32 s22, s22, 0x100
	s_addc_u32 s23, s23, 0
	s_cmp_gt_u32 s21, 19
	s_cbranch_scc0 .LBB0_2073
	s_and_b64 vcc, exec, s[8:9]
	s_cbranch_vccz .LBB0_2076
	s_barrier
